# adds: pooling items on a static per-workgroup schedule (no ticket atomics, one batch per XCD) + hand-written pooling item bodies (loads issued up front, zero row in LDS)
# speedup vs baseline: 1.0407x; 1.0070x over previous
; #define LDS_BARRIER() do { asm volatile("s_waitcnt lgkmcnt(0)" ::: "memory"); __builtin_amdgcn_s_barrier(); asm volatile("" ::: "memory"); } while (0)
; __device__ __forceinline__ void phase3_pool(const Args& a, LAS unsigned char* lds, int tid, int vcu, int G) {
;     ...
;     unsigned nxt = 0;
;     if (tid == 0) nxt = __hip_atomic_fetch_add(ctr, 1u, __ATOMIC_RELAXED, __HIP_MEMORY_SCOPE_AGENT);
;     for (;;) {
;         if (tid == 0) *tk = nxt;
;         LDS_BARRIER();
;         const int item = (int)*tk;
;         if (item >= 1024) break;
;         if (tid == 0) nxt = __hip_atomic_fetch_add(ctr, 1u, __ATOMIC_RELAXED, __HIP_MEMORY_SCOPE_AGENT);
.LBB0_676:
	s_or_b64 exec, exec, s[4:5]
	v_readlane_b32 s4, v246, 2
	s_nop 1
	v_add_u32_e32 v1, s4, v1
.LBB0_677:
	s_or_b64 exec, exec, s[2:3]
	v_and_b32_e32 v193, 0xff, v66
	v_lshlrev_b32_e32 v193, 2, v193
	v_add_u32_e32 v193, 0x10000, v193
	v_mov_b32_e32 v194, 0
	ds_write_b32 v193, v194
	s_add_u32 s44, s92, 0x28800000
	v_lshlrev_b32_e32 v2, 3, v66
	s_addc_u32 s45, s93, 0
	s_add_u32 s46, s92, 0x2ab00000
	v_and_b32_e32 v2, 0xf8, v2
	s_addc_u32 s47, s93, 0
	v_mov_b32_e32 v5, 0
	v_lshlrev_b32_e32 v4, 1, v2
	s_add_i32 s33, 0, 0x23f40
	s_mov_b32 s49, 0
	v_lshl_add_u32 v3, v2, 2, 0
	v_or_b32_e32 v6, 0x200, v2
	v_or_b32_e32 v8, 0x100, v2
	v_lshl_add_u64 v[10:11], s[44:45], 0, v[4:5]
	v_mov_b32_e32 v7, s33
	s_movk_i32 s34, 0x3ff
	s_mov_b32 s35, 0xffff0000
	s_movk_i32 s36, 0x7fff
	s_branch .LBB0_680

; __device__ __forceinline__ void phase3_pool(const Args& a, LAS unsigned char* lds, int tid, int vcu, int G) {
;     ...
;         if (tid == 0) nxt = __hip_atomic_fetch_add(ctr, 1u, __ATOMIC_RELAXED, __HIP_MEMORY_SCOPE_AGENT);
;         const int g = item >> 8, r = (item >> 3) & 31, b = item & 7;
;         const int gg = 3 - g;
;         if (gg == 0) pool_item<1>(P, DP, tmp, tid, b, r, gg); else if (gg == 1) pool_item<2>(P, DP, tmp, tid, b, r, gg); else if (gg == 2) pool_item<4>(P, DP, tmp, tid, b, r, gg); else pool_item<8>(P, DP, tmp, tid, b, r, gg);
.LBB0_686:
	s_or_b64 exec, exec, s[4:5]
	s_add_i32 s4, s8, 0x100
	v_add_u32_e32 v1, s4, v1
.LBB0_687:
	s_or_b64 exec, exec, s[2:3]
	s_ashr_i32 s9, s8, 8
	s_bfe_u32 s37, s8, 0x50003
	s_and_b32 s38, s8, 7
	s_cmp_lt_i32 s9, 2
	s_mov_b64 s[2:3], -1
	s_cbranch_scc1 .LBB0_701
	s_cmp_gt_i32 s9, 2
	s_cbranch_scc0 .LBB0_694
	s_branch .Lpool_h1
	v_sub_u32_e64 v9, s37, 1 clamp
	v_sub_u32_e32 v4, s37, v9
	v_add_u32_e32 v4, 1, v4
	v_cvt_f32_i32_e32 v12, v4
	v_lshlrev_b32_e32 v4, 6, v9
	s_lshl_b32 s2, s38, 11
	s_mov_b32 s3, 0
	v_div_scale_f32 v13, s[4:5], v12, v12, 1.0
	v_rcp_f32_e32 v14, v13
	v_div_scale_f32 v15, vcc, 1.0, v12, 1.0
	v_fma_f32 v16, -v13, v14, 1.0
	v_fmac_f32_e32 v14, v16, v14
	v_mul_f32_e32 v16, v15, v14
	v_fma_f32 v17, -v13, v16, v15
	v_fmac_f32_e32 v16, v17, v14
	v_fma_f32 v13, -v13, v16, v15
	v_div_fmas_f32 v13, v13, v14, v16
	v_cmp_gt_u32_e32 vcc, s37, v9
	v_div_fixup_f32 v12, v13, v12, 1.0
	v_mov_b32_e32 v13, v12
	v_addc_co_u32_e64 v9, s[4:5], 0, v9, vcc
	v_cndmask_b32_e64 v14, 0, 1.0, vcc
	v_lshlrev_b32_e32 v9, 6, v9
	v_mov_b32_e32 v15, v14

; template <int HALFW>
; __device__ __forceinline__ void pool_item(const bf16* P, bf16* DP, LAS float* tmp, int tid, int b, int r, int g) {
;     const int rlo = r - HALFW < 0 ? 0 : r - HALFW, rhi = r + HALFW > 32 ? 32 : r + HALFW;
;     const float rinv = 1.f / (float)(rhi - rlo);
; #pragma unroll 1
;     for (int q = 0; q < 4; ++q) { const int p = tid + 512 * q, c = p >> 5, ch0 = (p & 31) * 8; float acc[8]; v4u x[2 * HALFW];
; #pragma unroll
;         for (int u = 0; u < 2 * HALFW; ++u) { const int rr = (rlo + u < rhi) ? rlo + u : rlo; x[u] = *(const v4u*)(P + ((size_t)(b * 2048 + rr * 64 + c)) * 1024 + g * 256 + ch0); }
; #pragma unroll
;         for (int j = 0; j < 8; ++j) acc[j] = 0.f;
; #pragma unroll
;         for (int u = 0; u < 2 * HALFW; ++u) { const float m = (rlo + u < rhi) ? 1.f : 0.f;
; __device__ __forceinline__ void phase3_pool(const Args& a, LAS unsigned char* lds, int tid, int vcu, int G) {
;     ...
;         const int g = item >> 8, r = (item >> 3) & 31, b = item & 7;
;         const int gg = 3 - g;
;         if (gg == 0) pool_item<1>(P, DP, tmp, tid, b, r, gg); else if (gg == 1) pool_item<2>(P, DP, tmp, tid, b, r, gg); else if (gg == 2) pool_item<4>(P, DP, tmp, tid, b, r, gg); else pool_item<8>(P, DP, tmp, tid, b, r, gg);
.LBB0_694:
	s_and_b64 vcc, exec, s[2:3]
	s_cbranch_vccz .LBB0_700
	s_branch .Lpool_h2
	s_min_u32 s4, s37, 30
	v_sub_u32_e64 v13, s37, 2 clamp
	s_add_i32 s6, s4, 2
	v_sub_u32_e32 v4, s6, v13
	v_cvt_f32_i32_e32 v4, v4
	v_cmp_gt_u32_e64 s[4:5], s4, v13
	v_div_scale_f32 v9, s[2:3], v4, v4, 1.0
	v_rcp_f32_e32 v12, v9
	v_div_scale_f32 v14, vcc, 1.0, v4, 1.0
	v_cndmask_b32_e64 v18, 0, 1.0, s[4:5]
	v_fma_f32 v15, -v9, v12, 1.0
	v_fmac_f32_e32 v12, v15, v12
	v_mul_f32_e32 v15, v14, v12
	v_fma_f32 v16, -v9, v15, v14
	v_fmac_f32_e32 v15, v16, v12
	v_fma_f32 v9, -v9, v15, v14
	v_div_fmas_f32 v9, v9, v12, v15
	v_div_fixup_f32 v12, v9, v4, 1.0
	v_lshlrev_b32_e32 v4, 6, v13
	v_add_u32_e32 v15, 0x80, v4
	v_cmp_gt_u32_e32 vcc, s6, v13
	v_add_u32_e32 v9, 1, v13
	v_cndmask_b32_e64 v22, v4, v15, s[4:5]
	v_add_u32_e32 v15, 3, v13
	v_cndmask_b32_e64 v14, 0, 1.0, vcc
	v_cmp_gt_u32_e32 vcc, s6, v9
	v_cmp_gt_u32_e64 s[6:7], s6, v15
	s_lshl_b32 s2, s38, 11
	v_cndmask_b32_e32 v9, v13, v9, vcc
	v_cndmask_b32_e64 v13, v13, v15, s[6:7]
	v_cndmask_b32_e64 v16, 0, 1.0, vcc
	v_cndmask_b32_e64 v20, 0, 1.0, s[6:7]
	v_lshlrev_b32_e32 v9, 6, v9
	v_lshlrev_b32_e32 v23, 6, v13
	v_mov_b32_e32 v13, v12
	v_mov_b32_e32 v15, v14
	v_mov_b32_e32 v17, v16
	v_mov_b32_e32 v19, v18
	v_mov_b32_e32 v21, v20
	s_mov_b32 s3, 0

; template <int HALFW>
; __device__ __forceinline__ void pool_item(const bf16* P, bf16* DP, LAS float* tmp, int tid, int b, int r, int g) {
;     const int rlo = r - HALFW < 0 ? 0 : r - HALFW, rhi = r + HALFW > 32 ? 32 : r + HALFW;
;     const float rinv = 1.f / (float)(rhi - rlo);
; #pragma unroll 1
;     for (int q = 0; q < 4; ++q) { const int p = tid + 512 * q, c = p >> 5, ch0 = (p & 31) * 8; float acc[8]; v4u x[2 * HALFW];
; #pragma unroll
;         for (int u = 0; u < 2 * HALFW; ++u) { const int rr = (rlo + u < rhi) ? rlo + u : rlo; x[u] = *(const v4u*)(P + ((size_t)(b * 2048 + rr * 64 + c)) * 1024 + g * 256 + ch0); }
; #pragma unroll
;         for (int j = 0; j < 8; ++j) acc[j] = 0.f;
; #pragma unroll
;         for (int u = 0; u < 2 * HALFW; ++u) { const float m = (rlo + u < rhi) ? 1.f : 0.f;
; __device__ __forceinline__ void phase3_pool(const Args& a, LAS unsigned char* lds, int tid, int vcu, int G) {
;     ...
;         const int g = item >> 8, r = (item >> 3) & 31, b = item & 7;
;         const int gg = 3 - g;
;         if (gg == 0) pool_item<1>(P, DP, tmp, tid, b, r, gg); else if (gg == 1) pool_item<2>(P, DP, tmp, tid, b, r, gg); else if (gg == 2) pool_item<4>(P, DP, tmp, tid, b, r, gg); else pool_item<8>(P, DP, tmp, tid, b, r, gg);
.LBB0_701:
	s_andn2_b64 vcc, exec, s[2:3]
	s_cbranch_vccnz .LBB0_678
	s_cmp_lg_u32 s9, 1
	s_mov_b64 s[2:3], -1
	s_cbranch_scc0 .LBB0_708
	s_branch .Lpool_h8
	s_min_u32 s16, s37, 24
	v_sub_u32_e64 v13, s37, 8 clamp
	s_add_i32 s30, s16, 8
	v_sub_u32_e32 v4, s30, v13
	v_add_u32_e32 v17, 2, v13
	v_cvt_f32_i32_e32 v4, v4
	v_cmp_gt_u32_e64 s[4:5], s30, v17
	v_cmp_gt_u32_e64 s[16:17], s16, v13
	v_div_scale_f32 v9, s[2:3], v4, v4, 1.0
	v_cndmask_b32_e64 v17, v13, v17, s[4:5]
	v_lshlrev_b32_e32 v48, 6, v17
	v_add_u32_e32 v17, 3, v13
	v_cmp_gt_u32_e64 s[6:7], s30, v17
	v_rcp_f32_e32 v12, v9
	s_and_b32 s3, s8, 0xffffff00
	v_cndmask_b32_e64 v17, v13, v17, s[6:7]
	v_lshlrev_b32_e32 v49, 6, v17
	v_add_u32_e32 v17, 4, v13
	v_cmp_gt_u32_e64 s[8:9], s30, v17
	v_fma_f32 v15, -v9, v12, 1.0
	v_div_scale_f32 v14, vcc, 1.0, v4, 1.0
	v_cndmask_b32_e64 v17, v13, v17, s[8:9]
	v_lshlrev_b32_e32 v50, 6, v17
	v_add_u32_e32 v17, 5, v13
	v_cmp_gt_u32_e64 s[10:11], s30, v17
	v_fmac_f32_e32 v12, v15, v12
	v_mul_f32_e32 v15, v14, v12
	v_cndmask_b32_e64 v17, v13, v17, s[10:11]
	v_lshlrev_b32_e32 v51, 6, v17
	v_add_u32_e32 v17, 6, v13
	v_fma_f32 v16, -v9, v15, v14
	v_cmp_gt_u32_e64 s[12:13], s30, v17
	v_fmac_f32_e32 v15, v16, v12
	v_fma_f32 v9, -v9, v15, v14
	v_cndmask_b32_e64 v17, v13, v17, s[12:13]
	v_lshlrev_b32_e32 v52, 6, v17
	v_add_u32_e32 v17, 7, v13
	v_div_fmas_f32 v9, v9, v12, v15
	v_cmp_gt_u32_e64 s[14:15], s30, v17
	v_div_fixup_f32 v12, v9, v4, 1.0
	v_lshlrev_b32_e32 v4, 6, v13
	v_cndmask_b32_e64 v17, v13, v17, s[14:15]
	v_lshlrev_b32_e32 v53, 6, v17
	v_add_u32_e32 v17, 0x200, v4
	v_cndmask_b32_e64 v54, v4, v17, s[16:17]
	v_add_u32_e32 v17, 9, v13
	v_cmp_gt_u32_e64 s[18:19], s30, v17
	v_cmp_gt_u32_e32 vcc, s30, v13
	v_add_u32_e32 v9, 1, v13
	v_cndmask_b32_e64 v17, v13, v17, s[18:19]
	v_lshlrev_b32_e32 v55, 6, v17
	v_add_u32_e32 v17, 10, v13
	v_cmp_gt_u32_e64 s[20:21], s30, v17
	v_cndmask_b32_e64 v16, 0, 1.0, vcc
	v_cmp_gt_u32_e32 vcc, s30, v9
	v_cndmask_b32_e64 v17, v13, v17, s[20:21]
	v_lshlrev_b32_e32 v56, 6, v17
	v_add_u32_e32 v17, 11, v13
	v_cmp_gt_u32_e64 s[22:23], s30, v17
	s_sub_i32 s48, 0x300, s3
	v_cndmask_b32_e32 v9, v13, v9, vcc
	v_cndmask_b32_e64 v17, v13, v17, s[22:23]
	v_lshlrev_b32_e32 v57, 6, v17
	v_add_u32_e32 v17, 12, v13
	v_cmp_gt_u32_e64 s[24:25], s30, v17
	v_cndmask_b32_e64 v18, 0, 1.0, vcc
	v_cndmask_b32_e64 v20, 0, 1.0, s[4:5]
	v_cndmask_b32_e64 v17, v13, v17, s[24:25]
	v_lshlrev_b32_e32 v58, 6, v17
	v_add_u32_e32 v17, 13, v13
	v_cmp_gt_u32_e64 s[26:27], s30, v17
	v_cndmask_b32_e64 v22, 0, 1.0, s[6:7]
	v_cndmask_b32_e64 v24, 0, 1.0, s[8:9]
	v_cndmask_b32_e64 v17, v13, v17, s[26:27]
	v_lshlrev_b32_e32 v59, 6, v17
	v_add_u32_e32 v17, 14, v13
	v_cmp_gt_u32_e64 s[28:29], s30, v17
	v_cndmask_b32_e64 v26, 0, 1.0, s[10:11]
	v_cndmask_b32_e64 v28, 0, 1.0, s[12:13]
	v_cndmask_b32_e64 v17, v13, v17, s[28:29]
	v_lshlrev_b32_e32 v60, 6, v17
	v_add_u32_e32 v17, 15, v13
	v_cmp_gt_u32_e64 s[30:31], s30, v17
	v_cndmask_b32_e64 v30, 0, 1.0, s[14:15]
	v_cndmask_b32_e64 v32, 0, 1.0, s[16:17]
	v_cndmask_b32_e64 v13, v13, v17, s[30:31]
	v_cndmask_b32_e64 v34, 0, 1.0, s[18:19]
	v_cndmask_b32_e64 v36, 0, 1.0, s[20:21]
	v_cndmask_b32_e64 v38, 0, 1.0, s[22:23]
	v_cndmask_b32_e64 v40, 0, 1.0, s[24:25]
	v_cndmask_b32_e64 v42, 0, 1.0, s[26:27]
	v_cndmask_b32_e64 v44, 0, 1.0, s[28:29]
	v_cndmask_b32_e64 v46, 0, 1.0, s[30:31]
	s_lshl_b32 s2, s38, 11
	v_lshl_add_u64 v[14:15], s[48:49], 1, v[10:11]
	v_lshlrev_b32_e32 v9, 6, v9
	v_lshlrev_b32_e32 v61, 6, v13
	v_mov_b32_e32 v13, v12
	v_mov_b32_e32 v31, v30
	v_mov_b32_e32 v33, v32
	v_mov_b32_e32 v35, v34
	v_mov_b32_e32 v37, v36
	v_mov_b32_e32 v39, v38
	v_mov_b32_e32 v41, v40
	v_mov_b32_e32 v43, v42
	v_mov_b32_e32 v45, v44
	v_mov_b32_e32 v47, v46
	v_mov_b32_e32 v29, v28
	v_mov_b32_e32 v17, v16
	v_mov_b32_e32 v19, v18
	v_mov_b32_e32 v21, v20
	v_mov_b32_e32 v23, v22
	v_mov_b32_e32 v25, v24
	v_mov_b32_e32 v27, v26
	s_mov_b32 s3, 0

; template <int HALFW>
; __device__ __forceinline__ void pool_item(const bf16* P, bf16* DP, LAS float* tmp, int tid, int b, int r, int g) {
;     const int rlo = r - HALFW < 0 ? 0 : r - HALFW, rhi = r + HALFW > 32 ? 32 : r + HALFW;
;     const float rinv = 1.f / (float)(rhi - rlo);
; #pragma unroll 1
;     for (int q = 0; q < 4; ++q) { const int p = tid + 512 * q, c = p >> 5, ch0 = (p & 31) * 8; float acc[8]; v4u x[2 * HALFW];
; #pragma unroll
;         for (int u = 0; u < 2 * HALFW; ++u) { const int rr = (rlo + u < rhi) ? rlo + u : rlo; x[u] = *(const v4u*)(P + ((size_t)(b * 2048 + rr * 64 + c)) * 1024 + g * 256 + ch0); }
; #pragma unroll
;         for (int j = 0; j < 8; ++j) acc[j] = 0.f;
; #pragma unroll
;         for (int u = 0; u < 2 * HALFW; ++u) { const float m = (rlo + u < rhi) ? 1.f : 0.f;
; __device__ __forceinline__ void phase3_pool(const Args& a, LAS unsigned char* lds, int tid, int vcu, int G) {
;     ...
;         const int g = item >> 8, r = (item >> 3) & 31, b = item & 7;
;         const int gg = 3 - g;
;         if (gg == 0) pool_item<1>(P, DP, tmp, tid, b, r, gg); else if (gg == 1) pool_item<2>(P, DP, tmp, tid, b, r, gg); else if (gg == 2) pool_item<4>(P, DP, tmp, tid, b, r, gg); else pool_item<8>(P, DP, tmp, tid, b, r, gg);
.LBB0_708:
	s_and_b64 vcc, exec, s[2:3]
	s_cbranch_vccz .LBB0_678
	s_branch .Lpool_h4
	s_min_u32 s8, s37, 28
	v_sub_u32_e64 v13, s37, 4 clamp
	s_add_i32 s14, s8, 4
	v_sub_u32_e32 v4, s14, v13
	v_cvt_f32_i32_e32 v4, v4
	v_cmp_gt_u32_e64 s[8:9], s8, v13
	v_div_scale_f32 v9, s[2:3], v4, v4, 1.0
	v_rcp_f32_e32 v12, v9
	v_div_scale_f32 v14, vcc, 1.0, v4, 1.0
	v_cndmask_b32_e64 v22, 0, 1.0, s[8:9]
	v_fma_f32 v15, -v9, v12, 1.0
	v_fmac_f32_e32 v12, v15, v12
	v_mul_f32_e32 v15, v14, v12
	v_fma_f32 v16, -v9, v15, v14
	v_fmac_f32_e32 v15, v16, v12
	v_fma_f32 v9, -v9, v15, v14
	v_div_fmas_f32 v9, v9, v12, v15
	v_add_u32_e32 v15, 2, v13
	v_cmp_gt_u32_e64 s[4:5], s14, v15
	v_div_fixup_f32 v12, v9, v4, 1.0
	v_lshlrev_b32_e32 v4, 6, v13
	v_cndmask_b32_e64 v15, v13, v15, s[4:5]
	v_lshlrev_b32_e32 v30, 6, v15
	v_add_u32_e32 v15, 3, v13
	v_cmp_gt_u32_e64 s[6:7], s14, v15
	v_cmp_gt_u32_e32 vcc, s14, v13
	v_add_u32_e32 v9, 1, v13
	v_cndmask_b32_e64 v15, v13, v15, s[6:7]
	v_lshlrev_b32_e32 v31, 6, v15
	v_add_u32_e32 v15, 0x100, v4
	v_cndmask_b32_e64 v32, v4, v15, s[8:9]
	v_add_u32_e32 v15, 5, v13
	v_cmp_gt_u32_e64 s[10:11], s14, v15
	v_cndmask_b32_e64 v14, 0, 1.0, vcc
	v_cmp_gt_u32_e32 vcc, s14, v9
	v_cndmask_b32_e64 v15, v13, v15, s[10:11]
	v_lshlrev_b32_e32 v33, 6, v15
	v_add_u32_e32 v15, 6, v13
	v_cmp_gt_u32_e64 s[12:13], s14, v15
	v_cndmask_b32_e32 v9, v13, v9, vcc
	v_cndmask_b32_e64 v16, 0, 1.0, vcc
	v_cndmask_b32_e64 v15, v13, v15, s[12:13]
	v_lshlrev_b32_e32 v34, 6, v15
	v_add_u32_e32 v15, 7, v13
	v_cmp_gt_u32_e64 s[14:15], s14, v15
	v_cndmask_b32_e64 v18, 0, 1.0, s[4:5]
	v_cndmask_b32_e64 v20, 0, 1.0, s[6:7]
	v_cndmask_b32_e64 v13, v13, v15, s[14:15]
	v_cndmask_b32_e64 v24, 0, 1.0, s[10:11]
	v_cndmask_b32_e64 v26, 0, 1.0, s[12:13]
	v_cndmask_b32_e64 v28, 0, 1.0, s[14:15]
	s_lshl_b32 s2, s38, 11
	v_lshlrev_b32_e32 v9, 6, v9
	v_lshlrev_b32_e32 v35, 6, v13
	v_mov_b32_e32 v13, v12
	v_mov_b32_e32 v15, v14
	v_mov_b32_e32 v17, v16
	v_mov_b32_e32 v19, v18
	v_mov_b32_e32 v21, v20
	v_mov_b32_e32 v23, v22
	v_mov_b32_e32 v25, v24
	v_mov_b32_e32 v27, v26
	v_mov_b32_e32 v29, v28
	s_mov_b32 s3, 0

; #define LAS __attribute__((address_space(3)))
; template <int HALFW>
; __device__ __forceinline__ void pool_item(const bf16* P, bf16* DP, LAS float* tmp, int tid, int b, int r, int g) {
;     const int rlo = r - HALFW < 0 ? 0 : r - HALFW, rhi = r + HALFW > 32 ? 32 : r + HALFW;
;     const float rinv = 1.f / (float)(rhi - rlo);
; #pragma unroll 1
;     for (int q = 0; q < 4; ++q) { const int p = tid + 512 * q, c = p >> 5, ch0 = (p & 31) * 8; float acc[8]; v4u x[2 * HALFW];
; #pragma unroll
;         for (int u = 0; u < 2 * HALFW; ++u) { const int rr = (rlo + u < rhi) ? rlo + u : rlo; x[u] = *(const v4u*)(P + ((size_t)(b * 2048 + rr * 64 + c)) * 1024 + g * 256 + ch0); }
; #pragma unroll
;         for (int j = 0; j < 8; ++j) acc[j] = 0.f;
; #pragma unroll
;         for (int u = 0; u < 2 * HALFW; ++u) { const float m = (rlo + u < rhi) ? 1.f : 0.f;
;             acc[0] += m * bflo(x[u].x); acc[1] += m * bfhi(x[u].x); acc[2] += m * bflo(x[u].y); acc[3] += m * bfhi(x[u].y); acc[4] += m * bflo(x[u].z); acc[5] += m * bfhi(x[u].z); acc[6] += m * bflo(x[u].w); acc[7] += m * bfhi(x[u].w); }
;         *(LAS f32x4*)(tmp + c * 256 + ch0) = (f32x4){acc[0] * rinv, acc[1] * rinv, acc[2] * rinv, acc[3] * rinv};
;         *(LAS f32x4*)(tmp + c * 256 + ch0 + 4) = (f32x4){acc[4] * rinv, acc[5] * rinv, acc[6] * rinv, acc[7] * rinv}; }
.Lpool_h1:
	s_sub_i32 s27, s37, 1
	s_max_i32 s27, s27, 0
	s_add_i32 s28, s37, 1
	s_min_i32 s28, s28, 32
	s_sub_i32 s26, s28, s27
	s_lshl_b32 s29, s38, 11
	s_lshl_b32 s3, s27, 6
	s_add_i32 s2, s29, s3
	s_lshl_b32 s3, s2, 11
	s_add_u32 s4, s44, s3
	s_addc_u32 s5, s45, 0
	s_lshl_b32 s3, s37, 6
	s_add_i32 s3, s29, s3
	s_lshl_b32 s3, s3, 11
	s_add_u32 s6, s44, s3
	s_addc_u32 s7, s45, 0
	s_add_u32 s24, s46, s3
	s_addc_u32 s25, s47, 0
	s_cmp_gt_u32 s26, 0
	s_cselect_b32 s8, 0x0, 0
	s_cmp_gt_u32 s26, 1
	s_cselect_b32 s9, 0x20000, 0
	v_lshrrev_b32_e32 v50, 5, v66
	v_lshlrev_b32_e32 v12, 11, v50
	v_lshl_or_b32 v12, v2, 1, v12
	v_add_u32_e32 v13, 0x8000, v12
	v_add_u32_e32 v14, 0x10000, v12
	v_add_u32_e32 v15, 0x18000, v12
	v_lshl_add_u32 v49, v50, 10, v3
	v_add_u32_e32 v51, s8, v12
	global_load_dwordx4 v[68:71], v51, s[4:5]
	v_add_u32_e32 v51, s9, v12
	global_load_dwordx4 v[72:75], v51, s[4:5]
	v_add_u32_e32 v51, s8, v13
	global_load_dwordx4 v[76:79], v51, s[4:5]
	v_add_u32_e32 v51, s9, v13
	global_load_dwordx4 v[80:83], v51, s[4:5]
	v_add_u32_e32 v51, s8, v14
	global_load_dwordx4 v[84:87], v51, s[4:5]
	v_add_u32_e32 v51, s9, v14
	global_load_dwordx4 v[88:91], v51, s[4:5]
	v_add_u32_e32 v51, s8, v15
	global_load_dwordx4 v[92:95], v51, s[4:5]
	v_add_u32_e32 v51, s9, v15
	global_load_dwordx4 v[96:99], v51, s[4:5]
	global_load_dwordx4 v[16:19], v12, s[6:7]
	global_load_dwordx4 v[20:23], v13, s[6:7]
	global_load_dwordx4 v[24:27], v14, s[6:7]
	global_load_dwordx4 v[28:31], v15, s[6:7]
	v_cvt_f32_u32_e32 v212, s26
	v_div_scale_f32 v213, s[30:31], v212, v212, 1.0
	v_div_scale_f32 v215, vcc, 1.0, v212, 1.0
	v_rcp_f32_e32 v214, v213
	s_nop 1
	v_fma_f32 v216, -v213, v214, 1.0
	v_fmac_f32_e32 v214, v216, v214
	v_mul_f32_e32 v216, v215, v214
	v_fma_f32 v217, -v213, v216, v215
	v_fmac_f32_e32 v216, v217, v214
	v_fma_f32 v213, -v213, v216, v215
	s_nop 1
	v_div_fmas_f32 v213, v213, v214, v216
	v_div_fixup_f32 v48, v213, v212, 1.0
	s_waitcnt vmcnt(10)
	v_lshlrev_b32_e32 v32, 16, v68
	v_and_b32_e32 v33, 0xffff0000, v68
	v_lshlrev_b32_e32 v34, 16, v69
	v_and_b32_e32 v35, 0xffff0000, v69
	v_lshlrev_b32_e32 v36, 16, v70
	v_and_b32_e32 v37, 0xffff0000, v70
	v_lshlrev_b32_e32 v38, 16, v71
	v_and_b32_e32 v39, 0xffff0000, v71
	s_cmp_gt_u32 s26, 1
	s_cbranch_scc0 .Lpool_h1_q0
	v_lshlrev_b32_e32 v40, 16, v72
	v_and_b32_e32 v41, 0xffff0000, v72
	v_lshlrev_b32_e32 v42, 16, v73
	v_and_b32_e32 v43, 0xffff0000, v73
	v_lshlrev_b32_e32 v44, 16, v74
	v_and_b32_e32 v45, 0xffff0000, v74
	v_lshlrev_b32_e32 v46, 16, v75
	v_and_b32_e32 v47, 0xffff0000, v75
	v_pk_add_f32 v[32:33], v[32:33], v[40:41]
	v_pk_add_f32 v[34:35], v[34:35], v[42:43]
	v_pk_add_f32 v[36:37], v[36:37], v[44:45]
	v_pk_add_f32 v[38:39], v[38:39], v[46:47]
.Lpool_h1_q0:
	v_pk_mul_f32 v[32:33], v[32:33], v[48:49] op_sel_hi:[1,0]
	v_pk_mul_f32 v[34:35], v[34:35], v[48:49] op_sel_hi:[1,0]
	v_pk_mul_f32 v[36:37], v[36:37], v[48:49] op_sel_hi:[1,0]
	v_pk_mul_f32 v[38:39], v[38:39], v[48:49] op_sel_hi:[1,0]
	ds_write_b128 v49, v[32:35] offset:0
	ds_write_b128 v49, v[36:39] offset:16
	s_waitcnt vmcnt(8)
	v_lshlrev_b32_e32 v52, 16, v76
	v_and_b32_e32 v53, 0xffff0000, v76
	v_lshlrev_b32_e32 v54, 16, v77
	v_and_b32_e32 v55, 0xffff0000, v77
	v_lshlrev_b32_e32 v56, 16, v78
	v_and_b32_e32 v57, 0xffff0000, v78
	v_lshlrev_b32_e32 v58, 16, v79
	v_and_b32_e32 v59, 0xffff0000, v79
	s_cmp_gt_u32 s26, 1
	s_cbranch_scc0 .Lpool_h1_q1
	v_lshlrev_b32_e32 v40, 16, v80
	v_and_b32_e32 v41, 0xffff0000, v80
	v_lshlrev_b32_e32 v42, 16, v81
	v_and_b32_e32 v43, 0xffff0000, v81
	v_lshlrev_b32_e32 v44, 16, v82
	v_and_b32_e32 v45, 0xffff0000, v82
	v_lshlrev_b32_e32 v46, 16, v83
	v_and_b32_e32 v47, 0xffff0000, v83
	v_pk_add_f32 v[52:53], v[52:53], v[40:41]
	v_pk_add_f32 v[54:55], v[54:55], v[42:43]
	v_pk_add_f32 v[56:57], v[56:57], v[44:45]
	v_pk_add_f32 v[58:59], v[58:59], v[46:47]
.Lpool_h1_q1:
	v_pk_mul_f32 v[52:53], v[52:53], v[48:49] op_sel_hi:[1,0]
	v_pk_mul_f32 v[54:55], v[54:55], v[48:49] op_sel_hi:[1,0]
	v_pk_mul_f32 v[56:57], v[56:57], v[48:49] op_sel_hi:[1,0]
	v_pk_mul_f32 v[58:59], v[58:59], v[48:49] op_sel_hi:[1,0]
	ds_write_b128 v49, v[52:55] offset:16384
	ds_write_b128 v49, v[56:59] offset:16400
	s_waitcnt vmcnt(6)
	v_lshlrev_b32_e32 v32, 16, v84
	v_and_b32_e32 v33, 0xffff0000, v84
	v_lshlrev_b32_e32 v34, 16, v85
	v_and_b32_e32 v35, 0xffff0000, v85
	v_lshlrev_b32_e32 v36, 16, v86
	v_and_b32_e32 v37, 0xffff0000, v86
	v_lshlrev_b32_e32 v38, 16, v87
	v_and_b32_e32 v39, 0xffff0000, v87
	s_cmp_gt_u32 s26, 1
	s_cbranch_scc0 .Lpool_h1_q2
	v_lshlrev_b32_e32 v40, 16, v88
	v_and_b32_e32 v41, 0xffff0000, v88
	v_lshlrev_b32_e32 v42, 16, v89
	v_and_b32_e32 v43, 0xffff0000, v89
	v_lshlrev_b32_e32 v44, 16, v90
	v_and_b32_e32 v45, 0xffff0000, v90
	v_lshlrev_b32_e32 v46, 16, v91
	v_and_b32_e32 v47, 0xffff0000, v91
	v_pk_add_f32 v[32:33], v[32:33], v[40:41]
	v_pk_add_f32 v[34:35], v[34:35], v[42:43]
	v_pk_add_f32 v[36:37], v[36:37], v[44:45]
	v_pk_add_f32 v[38:39], v[38:39], v[46:47]
.Lpool_h1_q2:
	v_pk_mul_f32 v[32:33], v[32:33], v[48:49] op_sel_hi:[1,0]
	v_pk_mul_f32 v[34:35], v[34:35], v[48:49] op_sel_hi:[1,0]
	v_pk_mul_f32 v[36:37], v[36:37], v[48:49] op_sel_hi:[1,0]
	v_pk_mul_f32 v[38:39], v[38:39], v[48:49] op_sel_hi:[1,0]
	ds_write_b128 v49, v[32:35] offset:32768
	ds_write_b128 v49, v[36:39] offset:32784
	s_waitcnt vmcnt(4)
	v_lshlrev_b32_e32 v52, 16, v92
	v_and_b32_e32 v53, 0xffff0000, v92
	v_lshlrev_b32_e32 v54, 16, v93
	v_and_b32_e32 v55, 0xffff0000, v93
	v_lshlrev_b32_e32 v56, 16, v94
	v_and_b32_e32 v57, 0xffff0000, v94
	v_lshlrev_b32_e32 v58, 16, v95
	v_and_b32_e32 v59, 0xffff0000, v95
	s_cmp_gt_u32 s26, 1
	s_cbranch_scc0 .Lpool_h1_q3
	v_lshlrev_b32_e32 v40, 16, v96
	v_and_b32_e32 v41, 0xffff0000, v96
	v_lshlrev_b32_e32 v42, 16, v97
	v_and_b32_e32 v43, 0xffff0000, v97
	v_lshlrev_b32_e32 v44, 16, v98
	v_and_b32_e32 v45, 0xffff0000, v98
	v_lshlrev_b32_e32 v46, 16, v99
	v_and_b32_e32 v47, 0xffff0000, v99
	v_pk_add_f32 v[52:53], v[52:53], v[40:41]
	v_pk_add_f32 v[54:55], v[54:55], v[42:43]
	v_pk_add_f32 v[56:57], v[56:57], v[44:45]
	v_pk_add_f32 v[58:59], v[58:59], v[46:47]
; #define LAS __attribute__((address_space(3)))
; __device__ __forceinline__ unsigned pk2(float lo, float hi) { return f2bf(lo) | (f2bf(hi) << 16); }
; template <int HALFW>
; __device__ __forceinline__ void pool_item(const bf16* P, bf16* DP, LAS float* tmp, int tid, int b, int r, int g) {
;     ...
;     __syncthreads();
; #pragma unroll 1
;     for (int q = 0; q < 4; ++q) { const int p = tid + 512 * q, c = p >> 5, ch0 = (p & 31) * 8;
;         const int clo = c - HALFW < 0 ? 0 : c - HALFW, chi = c + HALFW > 64 ? 64 : c + HALFW; const float cinv = 1.f / (float)(chi - clo);
;         const size_t o = ((size_t)(b * 2048 + r * 64 + c)) * 1024 + g * 256 + ch0;
;         const v4u x = *(const v4u*)(P + o);
;         f32x4 a0 = (f32x4){0.f, 0.f, 0.f, 0.f}, a1 = a0;
; #pragma unroll
;         for (int u = 0; u < 2 * HALFW; ++u) { const int cc = (clo + u < chi) ? clo + u : clo; const float m = (clo + u < chi) ? 1.f : 0.f;
;             a0 += *(const LAS f32x4*)(tmp + cc * 256 + ch0) * m; a1 += *(const LAS f32x4*)(tmp + cc * 256 + ch0 + 4) * m; }
;         v4u d; d.x = pk2(a0[0] * cinv - bflo(x.x), a0[1] * cinv - bfhi(x.x)); d.y = pk2(a0[2] * cinv - bflo(x.y), a0[3] * cinv - bfhi(x.y));
;         d.z = pk2(a1[0] * cinv - bflo(x.z), a1[1] * cinv - bfhi(x.z)); d.w = pk2(a1[2] * cinv - bflo(x.w), a1[3] * cinv - bfhi(x.w));
;         *(v4u*)(DP + o) = d; }
.Lpool_h1_q3:
	v_pk_mul_f32 v[52:53], v[52:53], v[48:49] op_sel_hi:[1,0]
	v_pk_mul_f32 v[54:55], v[54:55], v[48:49] op_sel_hi:[1,0]
	v_pk_mul_f32 v[56:57], v[56:57], v[48:49] op_sel_hi:[1,0]
	v_pk_mul_f32 v[58:59], v[58:59], v[48:49] op_sel_hi:[1,0]
	ds_write_b128 v49, v[52:55] offset:49152
	ds_write_b128 v49, v[56:59] offset:49168
	v_add_u32_e32 v51, 0, v50
	v_add_u32_e32 v60, 1, v51
	v_min_u32_e32 v60, 64, v60
	v_sub_u32_e64 v61, v51, 1 clamp
	v_sub_u32_e32 v60, v60, v61
	v_cvt_f32_u32_e32 v212, v60
	v_div_scale_f32 v213, s[30:31], v212, v212, 1.0
	v_div_scale_f32 v215, vcc, 1.0, v212, 1.0
	v_rcp_f32_e32 v214, v213
	s_nop 1
	v_fma_f32 v216, -v213, v214, 1.0
	v_fmac_f32_e32 v214, v216, v214
	v_mul_f32_e32 v216, v215, v214
	v_fma_f32 v217, -v213, v216, v215
	v_fmac_f32_e32 v216, v217, v214
	v_fma_f32 v213, -v213, v216, v215
	s_nop 1
	v_div_fmas_f32 v213, v213, v214, v216
	v_div_fixup_f32 v196, v213, v212, 1.0
	v_add_u32_e32 v51, 16, v50
	v_add_u32_e32 v60, 1, v51
	v_min_u32_e32 v60, 64, v60
	v_sub_u32_e64 v61, v51, 1 clamp
	v_sub_u32_e32 v60, v60, v61
	v_cvt_f32_u32_e32 v212, v60
	v_div_scale_f32 v213, s[30:31], v212, v212, 1.0
	v_div_scale_f32 v215, vcc, 1.0, v212, 1.0
	v_rcp_f32_e32 v214, v213
	s_nop 1
	v_fma_f32 v216, -v213, v214, 1.0
	v_fmac_f32_e32 v214, v216, v214
	v_mul_f32_e32 v216, v215, v214
	v_fma_f32 v217, -v213, v216, v215
	v_fmac_f32_e32 v216, v217, v214
	v_fma_f32 v213, -v213, v216, v215
	s_nop 1
	v_div_fmas_f32 v213, v213, v214, v216
	v_div_fixup_f32 v198, v213, v212, 1.0
	v_add_u32_e32 v51, 32, v50
	v_add_u32_e32 v60, 1, v51
	v_min_u32_e32 v60, 64, v60
	v_sub_u32_e64 v61, v51, 1 clamp
	v_sub_u32_e32 v60, v60, v61
	v_cvt_f32_u32_e32 v212, v60
	v_div_scale_f32 v213, s[30:31], v212, v212, 1.0
	v_div_scale_f32 v215, vcc, 1.0, v212, 1.0
	v_rcp_f32_e32 v214, v213
	s_nop 1
	v_fma_f32 v216, -v213, v214, 1.0
	v_fmac_f32_e32 v214, v216, v214
	v_mul_f32_e32 v216, v215, v214
	v_fma_f32 v217, -v213, v216, v215
	v_fmac_f32_e32 v216, v217, v214
	v_fma_f32 v213, -v213, v216, v215
	s_nop 1
	v_div_fmas_f32 v213, v213, v214, v216
	v_div_fixup_f32 v200, v213, v212, 1.0
	v_add_u32_e32 v51, 48, v50
	v_add_u32_e32 v60, 1, v51
	v_min_u32_e32 v60, 64, v60
	v_sub_u32_e64 v61, v51, 1 clamp
	v_sub_u32_e32 v60, v60, v61
	v_cvt_f32_u32_e32 v212, v60
	v_div_scale_f32 v213, s[30:31], v212, v212, 1.0
	v_div_scale_f32 v215, vcc, 1.0, v212, 1.0
	v_rcp_f32_e32 v214, v213
	s_nop 1
	v_fma_f32 v216, -v213, v214, 1.0
	v_fmac_f32_e32 v214, v216, v214
	v_mul_f32_e32 v216, v215, v214
	v_fma_f32 v217, -v213, v216, v215
	v_fmac_f32_e32 v216, v217, v214
	v_fma_f32 v213, -v213, v216, v215
	s_nop 1
	v_div_fmas_f32 v213, v213, v214, v216
	v_div_fixup_f32 v202, v213, v212, 1.0
	s_waitcnt lgkmcnt(0)
	s_barrier
	v_add_u32_e32 v51, -1, v50
	v_add_u32_e32 v60, 0, v51
	v_min_u32_e32 v60, 64, v60
	v_lshl_add_u32 v60, v60, 10, v3
	ds_read_b128 v[204:207], v60
	ds_read_b128 v[208:211], v60 offset:16
	v_add_u32_e32 v60, 1, v51
	v_min_u32_e32 v60, 64, v60
	v_lshl_add_u32 v60, v60, 10, v3
	ds_read_b128 v[76:79], v60
	ds_read_b128 v[80:83], v60 offset:16
	s_waitcnt lgkmcnt(0)
	v_pk_add_f32 v[204:205], v[204:205], v[76:77]
	v_pk_add_f32 v[206:207], v[206:207], v[78:79]
	v_pk_add_f32 v[208:209], v[208:209], v[80:81]
	v_pk_add_f32 v[210:211], v[210:211], v[82:83]
	s_waitcnt vmcnt(0)
	v_lshlrev_b32_e32 v40, 16, v16
	v_and_b32_e32 v41, 0xffff0000, v16
	v_lshlrev_b32_e32 v42, 16, v17
	v_and_b32_e32 v43, 0xffff0000, v17
	v_lshlrev_b32_e32 v44, 16, v18
	v_and_b32_e32 v45, 0xffff0000, v18
	v_lshlrev_b32_e32 v46, 16, v19
	v_and_b32_e32 v47, 0xffff0000, v19
	v_pk_fma_f32 v[40:41], v[196:197], v[204:205], v[40:41] op_sel_hi:[0,1,1] neg_lo:[0,0,1] neg_hi:[0,0,1]
	v_pk_fma_f32 v[42:43], v[196:197], v[206:207], v[42:43] op_sel_hi:[0,1,1] neg_lo:[0,0,1] neg_hi:[0,0,1]
	v_pk_fma_f32 v[44:45], v[196:197], v[208:209], v[44:45] op_sel_hi:[0,1,1] neg_lo:[0,0,1] neg_hi:[0,0,1]
	v_pk_fma_f32 v[46:47], v[196:197], v[210:211], v[46:47] op_sel_hi:[0,1,1] neg_lo:[0,0,1] neg_hi:[0,0,1]
	v_cvt_pk_bf16_f32 v218, v40, v41
	v_cvt_pk_bf16_f32 v219, v42, v43
	v_cvt_pk_bf16_f32 v220, v44, v45
	v_cvt_pk_bf16_f32 v221, v46, v47
	global_store_dwordx4 v12, v[218:221], s[24:25]
	v_add_u32_e32 v51, 15, v50
	v_add_u32_e32 v60, 0, v51
	v_min_u32_e32 v60, 64, v60
	v_lshl_add_u32 v60, v60, 10, v3
	ds_read_b128 v[204:207], v60
	ds_read_b128 v[208:211], v60 offset:16
	v_add_u32_e32 v60, 1, v51
	v_min_u32_e32 v60, 64, v60
	v_lshl_add_u32 v60, v60, 10, v3
	ds_read_b128 v[76:79], v60
	ds_read_b128 v[80:83], v60 offset:16
	s_waitcnt lgkmcnt(0)
	v_pk_add_f32 v[204:205], v[204:205], v[76:77]
	v_pk_add_f32 v[206:207], v[206:207], v[78:79]
	v_pk_add_f32 v[208:209], v[208:209], v[80:81]
	v_pk_add_f32 v[210:211], v[210:211], v[82:83]
	v_lshlrev_b32_e32 v40, 16, v20
	v_and_b32_e32 v41, 0xffff0000, v20
	v_lshlrev_b32_e32 v42, 16, v21
	v_and_b32_e32 v43, 0xffff0000, v21
	v_lshlrev_b32_e32 v44, 16, v22
	v_and_b32_e32 v45, 0xffff0000, v22
	v_lshlrev_b32_e32 v46, 16, v23
	v_and_b32_e32 v47, 0xffff0000, v23
	v_pk_fma_f32 v[40:41], v[198:199], v[204:205], v[40:41] op_sel_hi:[0,1,1] neg_lo:[0,0,1] neg_hi:[0,0,1]
	v_pk_fma_f32 v[42:43], v[198:199], v[206:207], v[42:43] op_sel_hi:[0,1,1] neg_lo:[0,0,1] neg_hi:[0,0,1]
	v_pk_fma_f32 v[44:45], v[198:199], v[208:209], v[44:45] op_sel_hi:[0,1,1] neg_lo:[0,0,1] neg_hi:[0,0,1]
	v_pk_fma_f32 v[46:47], v[198:199], v[210:211], v[46:47] op_sel_hi:[0,1,1] neg_lo:[0,0,1] neg_hi:[0,0,1]
	v_cvt_pk_bf16_f32 v222, v40, v41
	v_cvt_pk_bf16_f32 v223, v42, v43
	v_cvt_pk_bf16_f32 v224, v44, v45
	v_cvt_pk_bf16_f32 v225, v46, v47
	global_store_dwordx4 v13, v[222:225], s[24:25]
	v_add_u32_e32 v51, 31, v50
	v_add_u32_e32 v60, 0, v51
	v_min_u32_e32 v60, 64, v60
	v_lshl_add_u32 v60, v60, 10, v3
	ds_read_b128 v[204:207], v60
	ds_read_b128 v[208:211], v60 offset:16
	v_add_u32_e32 v60, 1, v51
	v_min_u32_e32 v60, 64, v60
	v_lshl_add_u32 v60, v60, 10, v3
	ds_read_b128 v[76:79], v60
	ds_read_b128 v[80:83], v60 offset:16
	s_waitcnt lgkmcnt(0)
; #define LAS __attribute__((address_space(3)))
; template <int HALFW>
; __device__ __forceinline__ void pool_item(const bf16* P, bf16* DP, LAS float* tmp, int tid, int b, int r, int g) {
;     const int rlo = r - HALFW < 0 ? 0 : r - HALFW, rhi = r + HALFW > 32 ? 32 : r + HALFW;
;     const float rinv = 1.f / (float)(rhi - rlo);
; #pragma unroll 1
;     for (int q = 0; q < 4; ++q) { const int p = tid + 512 * q, c = p >> 5, ch0 = (p & 31) * 8; float acc[8]; v4u x[2 * HALFW];
; #pragma unroll
;         for (int u = 0; u < 2 * HALFW; ++u) { const int rr = (rlo + u < rhi) ? rlo + u : rlo; x[u] = *(const v4u*)(P + ((size_t)(b * 2048 + rr * 64 + c)) * 1024 + g * 256 + ch0); }
; #pragma unroll
;         for (int j = 0; j < 8; ++j) acc[j] = 0.f;
; #pragma unroll
;         for (int u = 0; u < 2 * HALFW; ++u) { const float m = (rlo + u < rhi) ? 1.f : 0.f;
;             acc[0] += m * bflo(x[u].x); acc[1] += m * bfhi(x[u].x); acc[2] += m * bflo(x[u].y); acc[3] += m * bfhi(x[u].y); acc[4] += m * bflo(x[u].z); acc[5] += m * bfhi(x[u].z); acc[6] += m * bflo(x[u].w); acc[7] += m * bfhi(x[u].w); }
;         *(LAS f32x4*)(tmp + c * 256 + ch0) = (f32x4){acc[0] * rinv, acc[1] * rinv, acc[2] * rinv, acc[3] * rinv};
;         *(LAS f32x4*)(tmp + c * 256 + ch0 + 4) = (f32x4){acc[4] * rinv, acc[5] * rinv, acc[6] * rinv, acc[7] * rinv}; }
;     ...
;     for (int q = 0; q < 4; ++q) { const int p = tid + 512 * q, c = p >> 5, ch0 = (p & 31) * 8;
;         const int clo = c - HALFW < 0 ? 0 : c - HALFW, chi = c + HALFW > 64 ? 64 : c + HALFW; const float cinv = 1.f / (float)(chi - clo);
;         const size_t o = ((size_t)(b * 2048 + r * 64 + c)) * 1024 + g * 256 + ch0;
;         const v4u x = *(const v4u*)(P + o);
;         f32x4 a0 = (f32x4){0.f, 0.f, 0.f, 0.f}, a1 = a0;
; #pragma unroll
;         for (int u = 0; u < 2 * HALFW; ++u) { const int cc = (clo + u < chi) ? clo + u : clo; const float m = (clo + u < chi) ? 1.f : 0.f;
;             a0 += *(const LAS f32x4*)(tmp + cc * 256 + ch0) * m; a1 += *(const LAS f32x4*)(tmp + cc * 256 + ch0 + 4) * m; }
;         v4u d; d.x = pk2(a0[0] * cinv - bflo(x.x), a0[1] * cinv - bfhi(x.x)); d.y = pk2(a0[2] * cinv - bflo(x.y), a0[3] * cinv - bfhi(x.y));
;         d.z = pk2(a1[0] * cinv - bflo(x.z), a1[1] * cinv - bfhi(x.z)); d.w = pk2(a1[2] * cinv - bflo(x.w), a1[3] * cinv - bfhi(x.w));
;         *(v4u*)(DP + o) = d; }
	v_pk_add_f32 v[204:205], v[204:205], v[76:77]
	v_pk_add_f32 v[206:207], v[206:207], v[78:79]
	v_pk_add_f32 v[208:209], v[208:209], v[80:81]
	v_pk_add_f32 v[210:211], v[210:211], v[82:83]
	v_lshlrev_b32_e32 v40, 16, v24
	v_and_b32_e32 v41, 0xffff0000, v24
	v_lshlrev_b32_e32 v42, 16, v25
	v_and_b32_e32 v43, 0xffff0000, v25
	v_lshlrev_b32_e32 v44, 16, v26
	v_and_b32_e32 v45, 0xffff0000, v26
	v_lshlrev_b32_e32 v46, 16, v27
	v_and_b32_e32 v47, 0xffff0000, v27
	v_pk_fma_f32 v[40:41], v[200:201], v[204:205], v[40:41] op_sel_hi:[0,1,1] neg_lo:[0,0,1] neg_hi:[0,0,1]
	v_pk_fma_f32 v[42:43], v[200:201], v[206:207], v[42:43] op_sel_hi:[0,1,1] neg_lo:[0,0,1] neg_hi:[0,0,1]
	v_pk_fma_f32 v[44:45], v[200:201], v[208:209], v[44:45] op_sel_hi:[0,1,1] neg_lo:[0,0,1] neg_hi:[0,0,1]
	v_pk_fma_f32 v[46:47], v[200:201], v[210:211], v[46:47] op_sel_hi:[0,1,1] neg_lo:[0,0,1] neg_hi:[0,0,1]
	v_cvt_pk_bf16_f32 v218, v40, v41
	v_cvt_pk_bf16_f32 v219, v42, v43
	v_cvt_pk_bf16_f32 v220, v44, v45
	v_cvt_pk_bf16_f32 v221, v46, v47
	global_store_dwordx4 v14, v[218:221], s[24:25]
	v_add_u32_e32 v51, 47, v50
	v_add_u32_e32 v60, 0, v51
	v_min_u32_e32 v60, 64, v60
	v_lshl_add_u32 v60, v60, 10, v3
	ds_read_b128 v[204:207], v60
	ds_read_b128 v[208:211], v60 offset:16
	v_add_u32_e32 v60, 1, v51
	v_min_u32_e32 v60, 64, v60
	v_lshl_add_u32 v60, v60, 10, v3
	ds_read_b128 v[76:79], v60
	ds_read_b128 v[80:83], v60 offset:16
	s_waitcnt lgkmcnt(0)
	v_pk_add_f32 v[204:205], v[204:205], v[76:77]
	v_pk_add_f32 v[206:207], v[206:207], v[78:79]
	v_pk_add_f32 v[208:209], v[208:209], v[80:81]
	v_pk_add_f32 v[210:211], v[210:211], v[82:83]
	v_lshlrev_b32_e32 v40, 16, v28
	v_and_b32_e32 v41, 0xffff0000, v28
	v_lshlrev_b32_e32 v42, 16, v29
	v_and_b32_e32 v43, 0xffff0000, v29
	v_lshlrev_b32_e32 v44, 16, v30
	v_and_b32_e32 v45, 0xffff0000, v30
	v_lshlrev_b32_e32 v46, 16, v31
	v_and_b32_e32 v47, 0xffff0000, v31
	v_pk_fma_f32 v[40:41], v[202:203], v[204:205], v[40:41] op_sel_hi:[0,1,1] neg_lo:[0,0,1] neg_hi:[0,0,1]
	v_pk_fma_f32 v[42:43], v[202:203], v[206:207], v[42:43] op_sel_hi:[0,1,1] neg_lo:[0,0,1] neg_hi:[0,0,1]
	v_pk_fma_f32 v[44:45], v[202:203], v[208:209], v[44:45] op_sel_hi:[0,1,1] neg_lo:[0,0,1] neg_hi:[0,0,1]
	v_pk_fma_f32 v[46:47], v[202:203], v[210:211], v[46:47] op_sel_hi:[0,1,1] neg_lo:[0,0,1] neg_hi:[0,0,1]
	v_cvt_pk_bf16_f32 v222, v40, v41
	v_cvt_pk_bf16_f32 v223, v42, v43
	v_cvt_pk_bf16_f32 v224, v44, v45
	v_cvt_pk_bf16_f32 v225, v46, v47
	global_store_dwordx4 v15, v[222:225], s[24:25]
	s_barrier
	s_branch .LBB0_678
.Lpool_h2:
	s_sub_i32 s27, s37, 2
	s_max_i32 s27, s27, 0
	s_add_i32 s28, s37, 2
	s_min_i32 s28, s28, 32
	s_sub_i32 s26, s28, s27
	s_lshl_b32 s29, s38, 11
	s_lshl_b32 s3, s27, 6
	s_add_i32 s2, s29, s3
	s_lshl_b32 s3, s2, 11
	s_add_u32 s4, s44, s3
	s_addc_u32 s5, s45, 0
	s_lshl_b32 s3, s37, 6
	s_add_i32 s3, s29, s3
	s_lshl_b32 s3, s3, 11
	s_add_u32 s6, s44, s3
	s_addc_u32 s7, s45, 0
	s_add_u32 s24, s46, s3
	s_addc_u32 s25, s47, 0
	s_add_u32 s4, s4, 512
	s_addc_u32 s5, s5, 0
	s_add_u32 s6, s6, 512
	s_addc_u32 s7, s7, 0
	s_add_u32 s24, s24, 512
	s_addc_u32 s25, s25, 0
	s_cmp_gt_u32 s26, 0
	s_cselect_b32 s8, 0x0, 0
	s_cmp_gt_u32 s26, 1
	s_cselect_b32 s9, 0x20000, 0
	s_cmp_gt_u32 s26, 2
	s_cselect_b32 s10, 0x40000, 0
	s_cmp_gt_u32 s26, 3
	s_cselect_b32 s11, 0x60000, 0
	v_lshrrev_b32_e32 v50, 5, v66
	v_lshlrev_b32_e32 v12, 11, v50
	v_lshl_or_b32 v12, v2, 1, v12
	v_add_u32_e32 v13, 0x8000, v12
	v_add_u32_e32 v14, 0x10000, v12
	v_add_u32_e32 v15, 0x18000, v12
	v_lshl_add_u32 v49, v50, 10, v3
	v_add_u32_e32 v51, s8, v12
	global_load_dwordx4 v[68:71], v51, s[4:5]
	v_add_u32_e32 v51, s9, v12
	global_load_dwordx4 v[72:75], v51, s[4:5]
	v_add_u32_e32 v51, s10, v12
	global_load_dwordx4 v[76:79], v51, s[4:5]
	v_add_u32_e32 v51, s11, v12
	global_load_dwordx4 v[80:83], v51, s[4:5]
	v_add_u32_e32 v51, s8, v13
	global_load_dwordx4 v[84:87], v51, s[4:5]
	v_add_u32_e32 v51, s9, v13
	global_load_dwordx4 v[88:91], v51, s[4:5]
	v_add_u32_e32 v51, s10, v13
	global_load_dwordx4 v[92:95], v51, s[4:5]
	v_add_u32_e32 v51, s11, v13
	global_load_dwordx4 v[96:99], v51, s[4:5]
	v_add_u32_e32 v51, s8, v14
	global_load_dwordx4 v[100:103], v51, s[4:5]
	v_add_u32_e32 v51, s9, v14
	global_load_dwordx4 v[104:107], v51, s[4:5]
	v_add_u32_e32 v51, s10, v14
	global_load_dwordx4 v[108:111], v51, s[4:5]
	v_add_u32_e32 v51, s11, v14
	global_load_dwordx4 v[112:115], v51, s[4:5]
	v_add_u32_e32 v51, s8, v15
	global_load_dwordx4 v[116:119], v51, s[4:5]
	v_add_u32_e32 v51, s9, v15
	global_load_dwordx4 v[120:123], v51, s[4:5]
	v_add_u32_e32 v51, s10, v15
	global_load_dwordx4 v[124:127], v51, s[4:5]
	v_add_u32_e32 v51, s11, v15
	global_load_dwordx4 v[128:131], v51, s[4:5]
	global_load_dwordx4 v[16:19], v12, s[6:7]
	global_load_dwordx4 v[20:23], v13, s[6:7]
	global_load_dwordx4 v[24:27], v14, s[6:7]
	global_load_dwordx4 v[28:31], v15, s[6:7]
	v_cvt_f32_u32_e32 v212, s26
	v_div_scale_f32 v213, s[30:31], v212, v212, 1.0
	v_div_scale_f32 v215, vcc, 1.0, v212, 1.0
	v_rcp_f32_e32 v214, v213
	s_nop 1
	v_fma_f32 v216, -v213, v214, 1.0
	v_fmac_f32_e32 v214, v216, v214
	v_mul_f32_e32 v216, v215, v214
	v_fma_f32 v217, -v213, v216, v215
	v_fmac_f32_e32 v216, v217, v214
	v_fma_f32 v213, -v213, v216, v215
	s_nop 1
	v_div_fmas_f32 v213, v213, v214, v216
	v_div_fixup_f32 v48, v213, v212, 1.0
	s_waitcnt vmcnt(16)
	v_lshlrev_b32_e32 v32, 16, v68
	v_and_b32_e32 v33, 0xffff0000, v68
	v_lshlrev_b32_e32 v34, 16, v69
	v_and_b32_e32 v35, 0xffff0000, v69
	v_lshlrev_b32_e32 v36, 16, v70
	v_and_b32_e32 v37, 0xffff0000, v70
	v_lshlrev_b32_e32 v38, 16, v71
	v_and_b32_e32 v39, 0xffff0000, v71
	v_lshlrev_b32_e32 v40, 16, v72
	v_and_b32_e32 v41, 0xffff0000, v72
	v_lshlrev_b32_e32 v42, 16, v73
	v_and_b32_e32 v43, 0xffff0000, v73
	v_lshlrev_b32_e32 v44, 16, v74
	v_and_b32_e32 v45, 0xffff0000, v74
	v_lshlrev_b32_e32 v46, 16, v75
	v_and_b32_e32 v47, 0xffff0000, v75
	v_pk_add_f32 v[32:33], v[32:33], v[40:41]
	v_pk_add_f32 v[34:35], v[34:35], v[42:43]
	v_pk_add_f32 v[36:37], v[36:37], v[44:45]
	v_pk_add_f32 v[38:39], v[38:39], v[46:47]
	s_cmp_gt_u32 s26, 2
	s_cbranch_scc0 .Lpool_h2_q0
	v_lshlrev_b32_e32 v40, 16, v76
	v_and_b32_e32 v41, 0xffff0000, v76
	v_lshlrev_b32_e32 v42, 16, v77
	v_and_b32_e32 v43, 0xffff0000, v77
	v_lshlrev_b32_e32 v44, 16, v78
	v_and_b32_e32 v45, 0xffff0000, v78
	v_lshlrev_b32_e32 v46, 16, v79
	v_and_b32_e32 v47, 0xffff0000, v79
	v_pk_add_f32 v[32:33], v[32:33], v[40:41]
	v_pk_add_f32 v[34:35], v[34:35], v[42:43]
	v_pk_add_f32 v[36:37], v[36:37], v[44:45]
	v_pk_add_f32 v[38:39], v[38:39], v[46:47]
	s_cmp_gt_u32 s26, 3
	s_cbranch_scc0 .Lpool_h2_q0
	v_lshlrev_b32_e32 v40, 16, v80
	v_and_b32_e32 v41, 0xffff0000, v80
	v_lshlrev_b32_e32 v42, 16, v81
	v_and_b32_e32 v43, 0xffff0000, v81
	v_lshlrev_b32_e32 v44, 16, v82
	v_and_b32_e32 v45, 0xffff0000, v82
	v_lshlrev_b32_e32 v46, 16, v83
	v_and_b32_e32 v47, 0xffff0000, v83
	v_pk_add_f32 v[32:33], v[32:33], v[40:41]
	v_pk_add_f32 v[34:35], v[34:35], v[42:43]
	v_pk_add_f32 v[36:37], v[36:37], v[44:45]
	v_pk_add_f32 v[38:39], v[38:39], v[46:47]
; #define LAS __attribute__((address_space(3)))
; template <int HALFW>
; __device__ __forceinline__ void pool_item(const bf16* P, bf16* DP, LAS float* tmp, int tid, int b, int r, int g) {
;     ...
;     for (int q = 0; q < 4; ++q) { const int p = tid + 512 * q, c = p >> 5, ch0 = (p & 31) * 8; float acc[8]; v4u x[2 * HALFW];
; #pragma unroll
;         for (int u = 0; u < 2 * HALFW; ++u) { const int rr = (rlo + u < rhi) ? rlo + u : rlo; x[u] = *(const v4u*)(P + ((size_t)(b * 2048 + rr * 64 + c)) * 1024 + g * 256 + ch0); }
; #pragma unroll
;         for (int j = 0; j < 8; ++j) acc[j] = 0.f;
; #pragma unroll
;         for (int u = 0; u < 2 * HALFW; ++u) { const float m = (rlo + u < rhi) ? 1.f : 0.f;
;             acc[0] += m * bflo(x[u].x); acc[1] += m * bfhi(x[u].x); acc[2] += m * bflo(x[u].y); acc[3] += m * bfhi(x[u].y); acc[4] += m * bflo(x[u].z); acc[5] += m * bfhi(x[u].z); acc[6] += m * bflo(x[u].w); acc[7] += m * bfhi(x[u].w); }
;         *(LAS f32x4*)(tmp + c * 256 + ch0) = (f32x4){acc[0] * rinv, acc[1] * rinv, acc[2] * rinv, acc[3] * rinv};
;         *(LAS f32x4*)(tmp + c * 256 + ch0 + 4) = (f32x4){acc[4] * rinv, acc[5] * rinv, acc[6] * rinv, acc[7] * rinv}; }
.Lpool_h2_q0:
	v_pk_mul_f32 v[32:33], v[32:33], v[48:49] op_sel_hi:[1,0]
	v_pk_mul_f32 v[34:35], v[34:35], v[48:49] op_sel_hi:[1,0]
	v_pk_mul_f32 v[36:37], v[36:37], v[48:49] op_sel_hi:[1,0]
	v_pk_mul_f32 v[38:39], v[38:39], v[48:49] op_sel_hi:[1,0]
	ds_write_b128 v49, v[32:35] offset:0
	ds_write_b128 v49, v[36:39] offset:16
	s_waitcnt vmcnt(12)
	v_lshlrev_b32_e32 v52, 16, v84
	v_and_b32_e32 v53, 0xffff0000, v84
	v_lshlrev_b32_e32 v54, 16, v85
	v_and_b32_e32 v55, 0xffff0000, v85
	v_lshlrev_b32_e32 v56, 16, v86
	v_and_b32_e32 v57, 0xffff0000, v86
	v_lshlrev_b32_e32 v58, 16, v87
	v_and_b32_e32 v59, 0xffff0000, v87
	v_lshlrev_b32_e32 v40, 16, v88
	v_and_b32_e32 v41, 0xffff0000, v88
	v_lshlrev_b32_e32 v42, 16, v89
	v_and_b32_e32 v43, 0xffff0000, v89
	v_lshlrev_b32_e32 v44, 16, v90
	v_and_b32_e32 v45, 0xffff0000, v90
	v_lshlrev_b32_e32 v46, 16, v91
	v_and_b32_e32 v47, 0xffff0000, v91
	v_pk_add_f32 v[52:53], v[52:53], v[40:41]
	v_pk_add_f32 v[54:55], v[54:55], v[42:43]
	v_pk_add_f32 v[56:57], v[56:57], v[44:45]
	v_pk_add_f32 v[58:59], v[58:59], v[46:47]
	s_cmp_gt_u32 s26, 2
	s_cbranch_scc0 .Lpool_h2_q1
	v_lshlrev_b32_e32 v40, 16, v92
	v_and_b32_e32 v41, 0xffff0000, v92
	v_lshlrev_b32_e32 v42, 16, v93
	v_and_b32_e32 v43, 0xffff0000, v93
	v_lshlrev_b32_e32 v44, 16, v94
	v_and_b32_e32 v45, 0xffff0000, v94
	v_lshlrev_b32_e32 v46, 16, v95
	v_and_b32_e32 v47, 0xffff0000, v95
	v_pk_add_f32 v[52:53], v[52:53], v[40:41]
	v_pk_add_f32 v[54:55], v[54:55], v[42:43]
	v_pk_add_f32 v[56:57], v[56:57], v[44:45]
	v_pk_add_f32 v[58:59], v[58:59], v[46:47]
	s_cmp_gt_u32 s26, 3
	s_cbranch_scc0 .Lpool_h2_q1
	v_lshlrev_b32_e32 v40, 16, v96
	v_and_b32_e32 v41, 0xffff0000, v96
	v_lshlrev_b32_e32 v42, 16, v97
	v_and_b32_e32 v43, 0xffff0000, v97
	v_lshlrev_b32_e32 v44, 16, v98
	v_and_b32_e32 v45, 0xffff0000, v98
	v_lshlrev_b32_e32 v46, 16, v99
	v_and_b32_e32 v47, 0xffff0000, v99
	v_pk_add_f32 v[52:53], v[52:53], v[40:41]
	v_pk_add_f32 v[54:55], v[54:55], v[42:43]
	v_pk_add_f32 v[56:57], v[56:57], v[44:45]
	v_pk_add_f32 v[58:59], v[58:59], v[46:47]
.Lpool_h2_q1:
	v_pk_mul_f32 v[52:53], v[52:53], v[48:49] op_sel_hi:[1,0]
	v_pk_mul_f32 v[54:55], v[54:55], v[48:49] op_sel_hi:[1,0]
	v_pk_mul_f32 v[56:57], v[56:57], v[48:49] op_sel_hi:[1,0]
	v_pk_mul_f32 v[58:59], v[58:59], v[48:49] op_sel_hi:[1,0]
	ds_write_b128 v49, v[52:55] offset:16384
	ds_write_b128 v49, v[56:59] offset:16400
	s_waitcnt vmcnt(8)
	v_lshlrev_b32_e32 v32, 16, v100
	v_and_b32_e32 v33, 0xffff0000, v100
	v_lshlrev_b32_e32 v34, 16, v101
	v_and_b32_e32 v35, 0xffff0000, v101
	v_lshlrev_b32_e32 v36, 16, v102
	v_and_b32_e32 v37, 0xffff0000, v102
	v_lshlrev_b32_e32 v38, 16, v103
	v_and_b32_e32 v39, 0xffff0000, v103
	v_lshlrev_b32_e32 v40, 16, v104
	v_and_b32_e32 v41, 0xffff0000, v104
	v_lshlrev_b32_e32 v42, 16, v105
	v_and_b32_e32 v43, 0xffff0000, v105
	v_lshlrev_b32_e32 v44, 16, v106
	v_and_b32_e32 v45, 0xffff0000, v106
	v_lshlrev_b32_e32 v46, 16, v107
	v_and_b32_e32 v47, 0xffff0000, v107
	v_pk_add_f32 v[32:33], v[32:33], v[40:41]
	v_pk_add_f32 v[34:35], v[34:35], v[42:43]
	v_pk_add_f32 v[36:37], v[36:37], v[44:45]
	v_pk_add_f32 v[38:39], v[38:39], v[46:47]
	s_cmp_gt_u32 s26, 2
	s_cbranch_scc0 .Lpool_h2_q2
	v_lshlrev_b32_e32 v40, 16, v108
	v_and_b32_e32 v41, 0xffff0000, v108
	v_lshlrev_b32_e32 v42, 16, v109
	v_and_b32_e32 v43, 0xffff0000, v109
	v_lshlrev_b32_e32 v44, 16, v110
	v_and_b32_e32 v45, 0xffff0000, v110
	v_lshlrev_b32_e32 v46, 16, v111
	v_and_b32_e32 v47, 0xffff0000, v111
	v_pk_add_f32 v[32:33], v[32:33], v[40:41]
	v_pk_add_f32 v[34:35], v[34:35], v[42:43]
	v_pk_add_f32 v[36:37], v[36:37], v[44:45]
	v_pk_add_f32 v[38:39], v[38:39], v[46:47]
	s_cmp_gt_u32 s26, 3
	s_cbranch_scc0 .Lpool_h2_q2
	v_lshlrev_b32_e32 v40, 16, v112
	v_and_b32_e32 v41, 0xffff0000, v112
	v_lshlrev_b32_e32 v42, 16, v113
	v_and_b32_e32 v43, 0xffff0000, v113
	v_lshlrev_b32_e32 v44, 16, v114
	v_and_b32_e32 v45, 0xffff0000, v114
	v_lshlrev_b32_e32 v46, 16, v115
	v_and_b32_e32 v47, 0xffff0000, v115
	v_pk_add_f32 v[32:33], v[32:33], v[40:41]
	v_pk_add_f32 v[34:35], v[34:35], v[42:43]
	v_pk_add_f32 v[36:37], v[36:37], v[44:45]
	v_pk_add_f32 v[38:39], v[38:39], v[46:47]
.Lpool_h2_q2:
	v_pk_mul_f32 v[32:33], v[32:33], v[48:49] op_sel_hi:[1,0]
	v_pk_mul_f32 v[34:35], v[34:35], v[48:49] op_sel_hi:[1,0]
	v_pk_mul_f32 v[36:37], v[36:37], v[48:49] op_sel_hi:[1,0]
	v_pk_mul_f32 v[38:39], v[38:39], v[48:49] op_sel_hi:[1,0]
	ds_write_b128 v49, v[32:35] offset:32768
	ds_write_b128 v49, v[36:39] offset:32784
	s_waitcnt vmcnt(4)
	v_lshlrev_b32_e32 v52, 16, v116
	v_and_b32_e32 v53, 0xffff0000, v116
	v_lshlrev_b32_e32 v54, 16, v117
	v_and_b32_e32 v55, 0xffff0000, v117
	v_lshlrev_b32_e32 v56, 16, v118
	v_and_b32_e32 v57, 0xffff0000, v118
	v_lshlrev_b32_e32 v58, 16, v119
	v_and_b32_e32 v59, 0xffff0000, v119
	v_lshlrev_b32_e32 v40, 16, v120
	v_and_b32_e32 v41, 0xffff0000, v120
	v_lshlrev_b32_e32 v42, 16, v121
	v_and_b32_e32 v43, 0xffff0000, v121
	v_lshlrev_b32_e32 v44, 16, v122
	v_and_b32_e32 v45, 0xffff0000, v122
	v_lshlrev_b32_e32 v46, 16, v123
	v_and_b32_e32 v47, 0xffff0000, v123
	v_pk_add_f32 v[52:53], v[52:53], v[40:41]
	v_pk_add_f32 v[54:55], v[54:55], v[42:43]
	v_pk_add_f32 v[56:57], v[56:57], v[44:45]
	v_pk_add_f32 v[58:59], v[58:59], v[46:47]
	s_cmp_gt_u32 s26, 2
	s_cbranch_scc0 .Lpool_h2_q3
	v_lshlrev_b32_e32 v40, 16, v124
	v_and_b32_e32 v41, 0xffff0000, v124
	v_lshlrev_b32_e32 v42, 16, v125
	v_and_b32_e32 v43, 0xffff0000, v125
	v_lshlrev_b32_e32 v44, 16, v126
	v_and_b32_e32 v45, 0xffff0000, v126
	v_lshlrev_b32_e32 v46, 16, v127
	v_and_b32_e32 v47, 0xffff0000, v127
	v_pk_add_f32 v[52:53], v[52:53], v[40:41]
	v_pk_add_f32 v[54:55], v[54:55], v[42:43]
	v_pk_add_f32 v[56:57], v[56:57], v[44:45]
	v_pk_add_f32 v[58:59], v[58:59], v[46:47]
	s_cmp_gt_u32 s26, 3
	s_cbranch_scc0 .Lpool_h2_q3
	v_lshlrev_b32_e32 v40, 16, v128
	v_and_b32_e32 v41, 0xffff0000, v128
	v_lshlrev_b32_e32 v42, 16, v129
	v_and_b32_e32 v43, 0xffff0000, v129
	v_lshlrev_b32_e32 v44, 16, v130
	v_and_b32_e32 v45, 0xffff0000, v130
	v_lshlrev_b32_e32 v46, 16, v131
	v_and_b32_e32 v47, 0xffff0000, v131
	v_pk_add_f32 v[52:53], v[52:53], v[40:41]
	v_pk_add_f32 v[54:55], v[54:55], v[42:43]
	v_pk_add_f32 v[56:57], v[56:57], v[44:45]
	v_pk_add_f32 v[58:59], v[58:59], v[46:47]
; #define LAS __attribute__((address_space(3)))
; __device__ __forceinline__ unsigned pk2(float lo, float hi) { return f2bf(lo) | (f2bf(hi) << 16); }
; template <int HALFW>
; __device__ __forceinline__ void pool_item(const bf16* P, bf16* DP, LAS float* tmp, int tid, int b, int r, int g) {
;     ...
;         *(LAS f32x4*)(tmp + c * 256 + ch0 + 4) = (f32x4){acc[4] * rinv, acc[5] * rinv, acc[6] * rinv, acc[7] * rinv}; }
;     __syncthreads();
; #pragma unroll 1
;     for (int q = 0; q < 4; ++q) { const int p = tid + 512 * q, c = p >> 5, ch0 = (p & 31) * 8;
;         const int clo = c - HALFW < 0 ? 0 : c - HALFW, chi = c + HALFW > 64 ? 64 : c + HALFW; const float cinv = 1.f / (float)(chi - clo);
;         const size_t o = ((size_t)(b * 2048 + r * 64 + c)) * 1024 + g * 256 + ch0;
;         const v4u x = *(const v4u*)(P + o);
;         f32x4 a0 = (f32x4){0.f, 0.f, 0.f, 0.f}, a1 = a0;
; #pragma unroll
;         for (int u = 0; u < 2 * HALFW; ++u) { const int cc = (clo + u < chi) ? clo + u : clo; const float m = (clo + u < chi) ? 1.f : 0.f;
;             a0 += *(const LAS f32x4*)(tmp + cc * 256 + ch0) * m; a1 += *(const LAS f32x4*)(tmp + cc * 256 + ch0 + 4) * m; }
;         v4u d; d.x = pk2(a0[0] * cinv - bflo(x.x), a0[1] * cinv - bfhi(x.x)); d.y = pk2(a0[2] * cinv - bflo(x.y), a0[3] * cinv - bfhi(x.y));
;         d.z = pk2(a1[0] * cinv - bflo(x.z), a1[1] * cinv - bfhi(x.z)); d.w = pk2(a1[2] * cinv - bflo(x.w), a1[3] * cinv - bfhi(x.w));
;         *(v4u*)(DP + o) = d; }
.Lpool_h2_q3:
	v_pk_mul_f32 v[52:53], v[52:53], v[48:49] op_sel_hi:[1,0]
	v_pk_mul_f32 v[54:55], v[54:55], v[48:49] op_sel_hi:[1,0]
	v_pk_mul_f32 v[56:57], v[56:57], v[48:49] op_sel_hi:[1,0]
	v_pk_mul_f32 v[58:59], v[58:59], v[48:49] op_sel_hi:[1,0]
	ds_write_b128 v49, v[52:55] offset:49152
	ds_write_b128 v49, v[56:59] offset:49168
	v_add_u32_e32 v51, 0, v50
	v_add_u32_e32 v60, 2, v51
	v_min_u32_e32 v60, 64, v60
	v_sub_u32_e64 v61, v51, 2 clamp
	v_sub_u32_e32 v60, v60, v61
	v_cvt_f32_u32_e32 v212, v60
	v_div_scale_f32 v213, s[30:31], v212, v212, 1.0
	v_div_scale_f32 v215, vcc, 1.0, v212, 1.0
	v_rcp_f32_e32 v214, v213
	s_nop 1
	v_fma_f32 v216, -v213, v214, 1.0
	v_fmac_f32_e32 v214, v216, v214
	v_mul_f32_e32 v216, v215, v214
	v_fma_f32 v217, -v213, v216, v215
	v_fmac_f32_e32 v216, v217, v214
	v_fma_f32 v213, -v213, v216, v215
	s_nop 1
	v_div_fmas_f32 v213, v213, v214, v216
	v_div_fixup_f32 v196, v213, v212, 1.0
	v_add_u32_e32 v51, 16, v50
	v_add_u32_e32 v60, 2, v51
	v_min_u32_e32 v60, 64, v60
	v_sub_u32_e64 v61, v51, 2 clamp
	v_sub_u32_e32 v60, v60, v61
	v_cvt_f32_u32_e32 v212, v60
	v_div_scale_f32 v213, s[30:31], v212, v212, 1.0
	v_div_scale_f32 v215, vcc, 1.0, v212, 1.0
	v_rcp_f32_e32 v214, v213
	s_nop 1
	v_fma_f32 v216, -v213, v214, 1.0
	v_fmac_f32_e32 v214, v216, v214
	v_mul_f32_e32 v216, v215, v214
	v_fma_f32 v217, -v213, v216, v215
	v_fmac_f32_e32 v216, v217, v214
	v_fma_f32 v213, -v213, v216, v215
	s_nop 1
	v_div_fmas_f32 v213, v213, v214, v216
	v_div_fixup_f32 v198, v213, v212, 1.0
	v_add_u32_e32 v51, 32, v50
	v_add_u32_e32 v60, 2, v51
	v_min_u32_e32 v60, 64, v60
	v_sub_u32_e64 v61, v51, 2 clamp
	v_sub_u32_e32 v60, v60, v61
	v_cvt_f32_u32_e32 v212, v60
	v_div_scale_f32 v213, s[30:31], v212, v212, 1.0
	v_div_scale_f32 v215, vcc, 1.0, v212, 1.0
	v_rcp_f32_e32 v214, v213
	s_nop 1
	v_fma_f32 v216, -v213, v214, 1.0
	v_fmac_f32_e32 v214, v216, v214
	v_mul_f32_e32 v216, v215, v214
	v_fma_f32 v217, -v213, v216, v215
	v_fmac_f32_e32 v216, v217, v214
	v_fma_f32 v213, -v213, v216, v215
	s_nop 1
	v_div_fmas_f32 v213, v213, v214, v216
	v_div_fixup_f32 v200, v213, v212, 1.0
	v_add_u32_e32 v51, 48, v50
	v_add_u32_e32 v60, 2, v51
	v_min_u32_e32 v60, 64, v60
	v_sub_u32_e64 v61, v51, 2 clamp
	v_sub_u32_e32 v60, v60, v61
	v_cvt_f32_u32_e32 v212, v60
	v_div_scale_f32 v213, s[30:31], v212, v212, 1.0
	v_div_scale_f32 v215, vcc, 1.0, v212, 1.0
	v_rcp_f32_e32 v214, v213
	s_nop 1
	v_fma_f32 v216, -v213, v214, 1.0
	v_fmac_f32_e32 v214, v216, v214
	v_mul_f32_e32 v216, v215, v214
	v_fma_f32 v217, -v213, v216, v215
	v_fmac_f32_e32 v216, v217, v214
	v_fma_f32 v213, -v213, v216, v215
	s_nop 1
	v_div_fmas_f32 v213, v213, v214, v216
	v_div_fixup_f32 v202, v213, v212, 1.0
	s_waitcnt lgkmcnt(0)
	s_barrier
	v_add_u32_e32 v51, -2, v50
	v_add_u32_e32 v60, 0, v51
	v_min_u32_e32 v60, 64, v60
	v_lshl_add_u32 v60, v60, 10, v3
	ds_read_b128 v[204:207], v60
	ds_read_b128 v[208:211], v60 offset:16
	v_add_u32_e32 v60, 1, v51
	v_min_u32_e32 v60, 64, v60
	v_lshl_add_u32 v60, v60, 10, v3
	ds_read_b128 v[76:79], v60
	ds_read_b128 v[80:83], v60 offset:16
	v_add_u32_e32 v60, 2, v51
	v_min_u32_e32 v60, 64, v60
	v_lshl_add_u32 v60, v60, 10, v3
	ds_read_b128 v[84:87], v60
	ds_read_b128 v[88:91], v60 offset:16
	v_add_u32_e32 v60, 3, v51
	v_min_u32_e32 v60, 64, v60
	v_lshl_add_u32 v60, v60, 10, v3
	ds_read_b128 v[92:95], v60
	ds_read_b128 v[96:99], v60 offset:16
	s_waitcnt lgkmcnt(4)
	v_pk_add_f32 v[204:205], v[204:205], v[76:77]
	v_pk_add_f32 v[206:207], v[206:207], v[78:79]
	v_pk_add_f32 v[208:209], v[208:209], v[80:81]
	v_pk_add_f32 v[210:211], v[210:211], v[82:83]
	s_waitcnt lgkmcnt(0)
	v_pk_add_f32 v[204:205], v[204:205], v[84:85]
	v_pk_add_f32 v[206:207], v[206:207], v[86:87]
	v_pk_add_f32 v[208:209], v[208:209], v[88:89]
	v_pk_add_f32 v[210:211], v[210:211], v[90:91]
	v_pk_add_f32 v[204:205], v[204:205], v[92:93]
	v_pk_add_f32 v[206:207], v[206:207], v[94:95]
	v_pk_add_f32 v[208:209], v[208:209], v[96:97]
	v_pk_add_f32 v[210:211], v[210:211], v[98:99]
	s_waitcnt vmcnt(0)
	v_lshlrev_b32_e32 v40, 16, v16
	v_and_b32_e32 v41, 0xffff0000, v16
	v_lshlrev_b32_e32 v42, 16, v17
	v_and_b32_e32 v43, 0xffff0000, v17
	v_lshlrev_b32_e32 v44, 16, v18
	v_and_b32_e32 v45, 0xffff0000, v18
	v_lshlrev_b32_e32 v46, 16, v19
	v_and_b32_e32 v47, 0xffff0000, v19
	v_pk_fma_f32 v[40:41], v[196:197], v[204:205], v[40:41] op_sel_hi:[0,1,1] neg_lo:[0,0,1] neg_hi:[0,0,1]
	v_pk_fma_f32 v[42:43], v[196:197], v[206:207], v[42:43] op_sel_hi:[0,1,1] neg_lo:[0,0,1] neg_hi:[0,0,1]
	v_pk_fma_f32 v[44:45], v[196:197], v[208:209], v[44:45] op_sel_hi:[0,1,1] neg_lo:[0,0,1] neg_hi:[0,0,1]
	v_pk_fma_f32 v[46:47], v[196:197], v[210:211], v[46:47] op_sel_hi:[0,1,1] neg_lo:[0,0,1] neg_hi:[0,0,1]
	v_cvt_pk_bf16_f32 v218, v40, v41
	v_cvt_pk_bf16_f32 v219, v42, v43
	v_cvt_pk_bf16_f32 v220, v44, v45
	v_cvt_pk_bf16_f32 v221, v46, v47
	global_store_dwordx4 v12, v[218:221], s[24:25]
	v_add_u32_e32 v51, 14, v50
	v_add_u32_e32 v60, 0, v51
	v_min_u32_e32 v60, 64, v60
	v_lshl_add_u32 v60, v60, 10, v3
	ds_read_b128 v[204:207], v60
	ds_read_b128 v[208:211], v60 offset:16
	v_add_u32_e32 v60, 1, v51
	v_min_u32_e32 v60, 64, v60
	v_lshl_add_u32 v60, v60, 10, v3
	ds_read_b128 v[76:79], v60
	ds_read_b128 v[80:83], v60 offset:16
	v_add_u32_e32 v60, 2, v51
	v_min_u32_e32 v60, 64, v60
	v_lshl_add_u32 v60, v60, 10, v3
	ds_read_b128 v[84:87], v60
	ds_read_b128 v[88:91], v60 offset:16
	v_add_u32_e32 v60, 3, v51
	v_min_u32_e32 v60, 64, v60
	v_lshl_add_u32 v60, v60, 10, v3
	ds_read_b128 v[92:95], v60
	ds_read_b128 v[96:99], v60 offset:16
	s_waitcnt lgkmcnt(4)
; #define LAS __attribute__((address_space(3)))
; __device__ __forceinline__ unsigned pk2(float lo, float hi) { return f2bf(lo) | (f2bf(hi) << 16); }
; template <int HALFW>
; __device__ __forceinline__ void pool_item(const bf16* P, bf16* DP, LAS float* tmp, int tid, int b, int r, int g) {
;     ...
;     for (int q = 0; q < 4; ++q) { const int p = tid + 512 * q, c = p >> 5, ch0 = (p & 31) * 8;
;         const int clo = c - HALFW < 0 ? 0 : c - HALFW, chi = c + HALFW > 64 ? 64 : c + HALFW; const float cinv = 1.f / (float)(chi - clo);
;         const size_t o = ((size_t)(b * 2048 + r * 64 + c)) * 1024 + g * 256 + ch0;
;         const v4u x = *(const v4u*)(P + o);
;         f32x4 a0 = (f32x4){0.f, 0.f, 0.f, 0.f}, a1 = a0;
; #pragma unroll
;         for (int u = 0; u < 2 * HALFW; ++u) { const int cc = (clo + u < chi) ? clo + u : clo; const float m = (clo + u < chi) ? 1.f : 0.f;
;             a0 += *(const LAS f32x4*)(tmp + cc * 256 + ch0) * m; a1 += *(const LAS f32x4*)(tmp + cc * 256 + ch0 + 4) * m; }
;         v4u d; d.x = pk2(a0[0] * cinv - bflo(x.x), a0[1] * cinv - bfhi(x.x)); d.y = pk2(a0[2] * cinv - bflo(x.y), a0[3] * cinv - bfhi(x.y));
;         d.z = pk2(a1[0] * cinv - bflo(x.z), a1[1] * cinv - bfhi(x.z)); d.w = pk2(a1[2] * cinv - bflo(x.w), a1[3] * cinv - bfhi(x.w));
;         *(v4u*)(DP + o) = d; }
;     __syncthreads();
	v_pk_add_f32 v[204:205], v[204:205], v[76:77]
	v_pk_add_f32 v[206:207], v[206:207], v[78:79]
	v_pk_add_f32 v[208:209], v[208:209], v[80:81]
	v_pk_add_f32 v[210:211], v[210:211], v[82:83]
	s_waitcnt lgkmcnt(0)
	v_pk_add_f32 v[204:205], v[204:205], v[84:85]
	v_pk_add_f32 v[206:207], v[206:207], v[86:87]
	v_pk_add_f32 v[208:209], v[208:209], v[88:89]
	v_pk_add_f32 v[210:211], v[210:211], v[90:91]
	v_pk_add_f32 v[204:205], v[204:205], v[92:93]
	v_pk_add_f32 v[206:207], v[206:207], v[94:95]
	v_pk_add_f32 v[208:209], v[208:209], v[96:97]
	v_pk_add_f32 v[210:211], v[210:211], v[98:99]
	v_lshlrev_b32_e32 v40, 16, v20
	v_and_b32_e32 v41, 0xffff0000, v20
	v_lshlrev_b32_e32 v42, 16, v21
	v_and_b32_e32 v43, 0xffff0000, v21
	v_lshlrev_b32_e32 v44, 16, v22
	v_and_b32_e32 v45, 0xffff0000, v22
	v_lshlrev_b32_e32 v46, 16, v23
	v_and_b32_e32 v47, 0xffff0000, v23
	v_pk_fma_f32 v[40:41], v[198:199], v[204:205], v[40:41] op_sel_hi:[0,1,1] neg_lo:[0,0,1] neg_hi:[0,0,1]
	v_pk_fma_f32 v[42:43], v[198:199], v[206:207], v[42:43] op_sel_hi:[0,1,1] neg_lo:[0,0,1] neg_hi:[0,0,1]
	v_pk_fma_f32 v[44:45], v[198:199], v[208:209], v[44:45] op_sel_hi:[0,1,1] neg_lo:[0,0,1] neg_hi:[0,0,1]
	v_pk_fma_f32 v[46:47], v[198:199], v[210:211], v[46:47] op_sel_hi:[0,1,1] neg_lo:[0,0,1] neg_hi:[0,0,1]
	v_cvt_pk_bf16_f32 v222, v40, v41
	v_cvt_pk_bf16_f32 v223, v42, v43
	v_cvt_pk_bf16_f32 v224, v44, v45
	v_cvt_pk_bf16_f32 v225, v46, v47
	global_store_dwordx4 v13, v[222:225], s[24:25]
	v_add_u32_e32 v51, 30, v50
	v_add_u32_e32 v60, 0, v51
	v_min_u32_e32 v60, 64, v60
	v_lshl_add_u32 v60, v60, 10, v3
	ds_read_b128 v[204:207], v60
	ds_read_b128 v[208:211], v60 offset:16
	v_add_u32_e32 v60, 1, v51
	v_min_u32_e32 v60, 64, v60
	v_lshl_add_u32 v60, v60, 10, v3
	ds_read_b128 v[76:79], v60
	ds_read_b128 v[80:83], v60 offset:16
	v_add_u32_e32 v60, 2, v51
	v_min_u32_e32 v60, 64, v60
	v_lshl_add_u32 v60, v60, 10, v3
	ds_read_b128 v[84:87], v60
	ds_read_b128 v[88:91], v60 offset:16
	v_add_u32_e32 v60, 3, v51
	v_min_u32_e32 v60, 64, v60
	v_lshl_add_u32 v60, v60, 10, v3
	ds_read_b128 v[92:95], v60
	ds_read_b128 v[96:99], v60 offset:16
	s_waitcnt lgkmcnt(4)
	v_pk_add_f32 v[204:205], v[204:205], v[76:77]
	v_pk_add_f32 v[206:207], v[206:207], v[78:79]
	v_pk_add_f32 v[208:209], v[208:209], v[80:81]
	v_pk_add_f32 v[210:211], v[210:211], v[82:83]
	s_waitcnt lgkmcnt(0)
	v_pk_add_f32 v[204:205], v[204:205], v[84:85]
	v_pk_add_f32 v[206:207], v[206:207], v[86:87]
	v_pk_add_f32 v[208:209], v[208:209], v[88:89]
	v_pk_add_f32 v[210:211], v[210:211], v[90:91]
	v_pk_add_f32 v[204:205], v[204:205], v[92:93]
	v_pk_add_f32 v[206:207], v[206:207], v[94:95]
	v_pk_add_f32 v[208:209], v[208:209], v[96:97]
	v_pk_add_f32 v[210:211], v[210:211], v[98:99]
	v_lshlrev_b32_e32 v40, 16, v24
	v_and_b32_e32 v41, 0xffff0000, v24
	v_lshlrev_b32_e32 v42, 16, v25
	v_and_b32_e32 v43, 0xffff0000, v25
	v_lshlrev_b32_e32 v44, 16, v26
	v_and_b32_e32 v45, 0xffff0000, v26
	v_lshlrev_b32_e32 v46, 16, v27
	v_and_b32_e32 v47, 0xffff0000, v27
	v_pk_fma_f32 v[40:41], v[200:201], v[204:205], v[40:41] op_sel_hi:[0,1,1] neg_lo:[0,0,1] neg_hi:[0,0,1]
	v_pk_fma_f32 v[42:43], v[200:201], v[206:207], v[42:43] op_sel_hi:[0,1,1] neg_lo:[0,0,1] neg_hi:[0,0,1]
	v_pk_fma_f32 v[44:45], v[200:201], v[208:209], v[44:45] op_sel_hi:[0,1,1] neg_lo:[0,0,1] neg_hi:[0,0,1]
	v_pk_fma_f32 v[46:47], v[200:201], v[210:211], v[46:47] op_sel_hi:[0,1,1] neg_lo:[0,0,1] neg_hi:[0,0,1]
	v_cvt_pk_bf16_f32 v218, v40, v41
	v_cvt_pk_bf16_f32 v219, v42, v43
	v_cvt_pk_bf16_f32 v220, v44, v45
	v_cvt_pk_bf16_f32 v221, v46, v47
	global_store_dwordx4 v14, v[218:221], s[24:25]
	v_add_u32_e32 v51, 46, v50
	v_add_u32_e32 v60, 0, v51
	v_min_u32_e32 v60, 64, v60
	v_lshl_add_u32 v60, v60, 10, v3
	ds_read_b128 v[204:207], v60
	ds_read_b128 v[208:211], v60 offset:16
	v_add_u32_e32 v60, 1, v51
	v_min_u32_e32 v60, 64, v60
	v_lshl_add_u32 v60, v60, 10, v3
	ds_read_b128 v[76:79], v60
	ds_read_b128 v[80:83], v60 offset:16
	v_add_u32_e32 v60, 2, v51
	v_min_u32_e32 v60, 64, v60
	v_lshl_add_u32 v60, v60, 10, v3
	ds_read_b128 v[84:87], v60
	ds_read_b128 v[88:91], v60 offset:16
	v_add_u32_e32 v60, 3, v51
	v_min_u32_e32 v60, 64, v60
	v_lshl_add_u32 v60, v60, 10, v3
	ds_read_b128 v[92:95], v60
	ds_read_b128 v[96:99], v60 offset:16
	s_waitcnt lgkmcnt(4)
	v_pk_add_f32 v[204:205], v[204:205], v[76:77]
	v_pk_add_f32 v[206:207], v[206:207], v[78:79]
	v_pk_add_f32 v[208:209], v[208:209], v[80:81]
	v_pk_add_f32 v[210:211], v[210:211], v[82:83]
	s_waitcnt lgkmcnt(0)
	v_pk_add_f32 v[204:205], v[204:205], v[84:85]
	v_pk_add_f32 v[206:207], v[206:207], v[86:87]
	v_pk_add_f32 v[208:209], v[208:209], v[88:89]
	v_pk_add_f32 v[210:211], v[210:211], v[90:91]
	v_pk_add_f32 v[204:205], v[204:205], v[92:93]
	v_pk_add_f32 v[206:207], v[206:207], v[94:95]
	v_pk_add_f32 v[208:209], v[208:209], v[96:97]
	v_pk_add_f32 v[210:211], v[210:211], v[98:99]
	v_lshlrev_b32_e32 v40, 16, v28
	v_and_b32_e32 v41, 0xffff0000, v28
	v_lshlrev_b32_e32 v42, 16, v29
	v_and_b32_e32 v43, 0xffff0000, v29
	v_lshlrev_b32_e32 v44, 16, v30
	v_and_b32_e32 v45, 0xffff0000, v30
	v_lshlrev_b32_e32 v46, 16, v31
	v_and_b32_e32 v47, 0xffff0000, v31
	v_pk_fma_f32 v[40:41], v[202:203], v[204:205], v[40:41] op_sel_hi:[0,1,1] neg_lo:[0,0,1] neg_hi:[0,0,1]
	v_pk_fma_f32 v[42:43], v[202:203], v[206:207], v[42:43] op_sel_hi:[0,1,1] neg_lo:[0,0,1] neg_hi:[0,0,1]
	v_pk_fma_f32 v[44:45], v[202:203], v[208:209], v[44:45] op_sel_hi:[0,1,1] neg_lo:[0,0,1] neg_hi:[0,0,1]
	v_pk_fma_f32 v[46:47], v[202:203], v[210:211], v[46:47] op_sel_hi:[0,1,1] neg_lo:[0,0,1] neg_hi:[0,0,1]
	v_cvt_pk_bf16_f32 v222, v40, v41
	v_cvt_pk_bf16_f32 v223, v42, v43
	v_cvt_pk_bf16_f32 v224, v44, v45
	v_cvt_pk_bf16_f32 v225, v46, v47
	global_store_dwordx4 v15, v[222:225], s[24:25]
	s_barrier
	s_branch .LBB0_678
; #define LAS __attribute__((address_space(3)))
; template <int HALFW>
; __device__ __forceinline__ void pool_item(const bf16* P, bf16* DP, LAS float* tmp, int tid, int b, int r, int g) {
;     const int rlo = r - HALFW < 0 ? 0 : r - HALFW, rhi = r + HALFW > 32 ? 32 : r + HALFW;
;     const float rinv = 1.f / (float)(rhi - rlo);
; #pragma unroll 1
;     for (int q = 0; q < 4; ++q) { const int p = tid + 512 * q, c = p >> 5, ch0 = (p & 31) * 8; float acc[8]; v4u x[2 * HALFW];
; #pragma unroll
;         for (int u = 0; u < 2 * HALFW; ++u) { const int rr = (rlo + u < rhi) ? rlo + u : rlo; x[u] = *(const v4u*)(P + ((size_t)(b * 2048 + rr * 64 + c)) * 1024 + g * 256 + ch0); }
; #pragma unroll
;         for (int j = 0; j < 8; ++j) acc[j] = 0.f;
; #pragma unroll
;         for (int u = 0; u < 2 * HALFW; ++u) { const float m = (rlo + u < rhi) ? 1.f : 0.f;
;             acc[0] += m * bflo(x[u].x); acc[1] += m * bfhi(x[u].x); acc[2] += m * bflo(x[u].y); acc[3] += m * bfhi(x[u].y); acc[4] += m * bflo(x[u].z); acc[5] += m * bfhi(x[u].z); acc[6] += m * bflo(x[u].w); acc[7] += m * bfhi(x[u].w); }
;         *(LAS f32x4*)(tmp + c * 256 + ch0) = (f32x4){acc[0] * rinv, acc[1] * rinv, acc[2] * rinv, acc[3] * rinv};
;         *(LAS f32x4*)(tmp + c * 256 + ch0 + 4) = (f32x4){acc[4] * rinv, acc[5] * rinv, acc[6] * rinv, acc[7] * rinv}; }
.Lpool_h4:
	s_sub_i32 s27, s37, 4
	s_max_i32 s27, s27, 0
	s_add_i32 s28, s37, 4
	s_min_i32 s28, s28, 32
	s_sub_i32 s26, s28, s27
	s_lshl_b32 s29, s38, 11
	s_lshl_b32 s3, s27, 6
	s_add_i32 s2, s29, s3
	s_lshl_b32 s3, s2, 11
	s_add_u32 s4, s44, s3
	s_addc_u32 s5, s45, 0
	s_lshl_b32 s3, s37, 6
	s_add_i32 s3, s29, s3
	s_lshl_b32 s3, s3, 11
	s_add_u32 s6, s44, s3
	s_addc_u32 s7, s45, 0
	s_add_u32 s24, s46, s3
	s_addc_u32 s25, s47, 0
	s_add_u32 s4, s4, 1024
	s_addc_u32 s5, s5, 0
	s_add_u32 s6, s6, 1024
	s_addc_u32 s7, s7, 0
	s_add_u32 s24, s24, 1024
	s_addc_u32 s25, s25, 0
	s_cmp_gt_u32 s26, 0
	s_cselect_b32 s8, 0x0, 0
	s_cmp_gt_u32 s26, 1
	s_cselect_b32 s9, 0x20000, 0
	s_cmp_gt_u32 s26, 2
	s_cselect_b32 s10, 0x40000, 0
	s_cmp_gt_u32 s26, 3
	s_cselect_b32 s11, 0x60000, 0
	s_cmp_gt_u32 s26, 4
	s_cselect_b32 s12, 0x80000, 0
	s_cmp_gt_u32 s26, 5
	s_cselect_b32 s13, 0xa0000, 0
	s_cmp_gt_u32 s26, 6
	s_cselect_b32 s14, 0xc0000, 0
	s_cmp_gt_u32 s26, 7
	s_cselect_b32 s15, 0xe0000, 0
	v_lshrrev_b32_e32 v50, 5, v66
	v_lshlrev_b32_e32 v12, 11, v50
	v_lshl_or_b32 v12, v2, 1, v12
	v_add_u32_e32 v13, 0x8000, v12
	v_add_u32_e32 v14, 0x10000, v12
	v_add_u32_e32 v15, 0x18000, v12
	v_lshl_add_u32 v49, v50, 10, v3
	v_add_u32_e32 v51, s8, v12
	global_load_dwordx4 v[68:71], v51, s[4:5]
	v_add_u32_e32 v51, s9, v12
	global_load_dwordx4 v[72:75], v51, s[4:5]
	v_add_u32_e32 v51, s10, v12
	global_load_dwordx4 v[76:79], v51, s[4:5]
	v_add_u32_e32 v51, s11, v12
	global_load_dwordx4 v[80:83], v51, s[4:5]
	v_add_u32_e32 v51, s12, v12
	global_load_dwordx4 v[84:87], v51, s[4:5]
	v_add_u32_e32 v51, s13, v12
	global_load_dwordx4 v[88:91], v51, s[4:5]
	v_add_u32_e32 v51, s14, v12
	global_load_dwordx4 v[92:95], v51, s[4:5]
	v_add_u32_e32 v51, s15, v12
	global_load_dwordx4 v[96:99], v51, s[4:5]
	v_add_u32_e32 v51, s8, v13
	global_load_dwordx4 v[100:103], v51, s[4:5]
	v_add_u32_e32 v51, s9, v13
	global_load_dwordx4 v[104:107], v51, s[4:5]
	v_add_u32_e32 v51, s10, v13
	global_load_dwordx4 v[108:111], v51, s[4:5]
	v_add_u32_e32 v51, s11, v13
	global_load_dwordx4 v[112:115], v51, s[4:5]
	v_add_u32_e32 v51, s12, v13
	global_load_dwordx4 v[116:119], v51, s[4:5]
	v_add_u32_e32 v51, s13, v13
	global_load_dwordx4 v[120:123], v51, s[4:5]
	v_add_u32_e32 v51, s14, v13
	global_load_dwordx4 v[124:127], v51, s[4:5]
	v_add_u32_e32 v51, s15, v13
	global_load_dwordx4 v[128:131], v51, s[4:5]
	v_add_u32_e32 v51, s8, v14
	global_load_dwordx4 v[132:135], v51, s[4:5]
	v_add_u32_e32 v51, s9, v14
	global_load_dwordx4 v[136:139], v51, s[4:5]
	v_add_u32_e32 v51, s10, v14
	global_load_dwordx4 v[140:143], v51, s[4:5]
	v_add_u32_e32 v51, s11, v14
	global_load_dwordx4 v[144:147], v51, s[4:5]
	v_add_u32_e32 v51, s12, v14
	global_load_dwordx4 v[148:151], v51, s[4:5]
	v_add_u32_e32 v51, s13, v14
	global_load_dwordx4 v[152:155], v51, s[4:5]
	v_add_u32_e32 v51, s14, v14
	global_load_dwordx4 v[156:159], v51, s[4:5]
	v_add_u32_e32 v51, s15, v14
	global_load_dwordx4 v[160:163], v51, s[4:5]
	v_add_u32_e32 v51, s8, v15
	global_load_dwordx4 v[164:167], v51, s[4:5]
	v_add_u32_e32 v51, s9, v15
	global_load_dwordx4 v[168:171], v51, s[4:5]
	v_add_u32_e32 v51, s10, v15
	global_load_dwordx4 v[172:175], v51, s[4:5]
	v_add_u32_e32 v51, s11, v15
	global_load_dwordx4 v[176:179], v51, s[4:5]
	v_add_u32_e32 v51, s12, v15
	global_load_dwordx4 v[180:183], v51, s[4:5]
	v_add_u32_e32 v51, s13, v15
	global_load_dwordx4 v[184:187], v51, s[4:5]
	v_add_u32_e32 v51, s14, v15
	global_load_dwordx4 v[188:191], v51, s[4:5]
	v_add_u32_e32 v51, s15, v15
	global_load_dwordx4 v[192:195], v51, s[4:5]
	global_load_dwordx4 v[16:19], v12, s[6:7]
	global_load_dwordx4 v[20:23], v13, s[6:7]
	global_load_dwordx4 v[24:27], v14, s[6:7]
	global_load_dwordx4 v[28:31], v15, s[6:7]
	v_cvt_f32_u32_e32 v212, s26
	v_div_scale_f32 v213, s[30:31], v212, v212, 1.0
	v_div_scale_f32 v215, vcc, 1.0, v212, 1.0
	v_rcp_f32_e32 v214, v213
	s_nop 1
	v_fma_f32 v216, -v213, v214, 1.0
	v_fmac_f32_e32 v214, v216, v214
	v_mul_f32_e32 v216, v215, v214
	v_fma_f32 v217, -v213, v216, v215
	v_fmac_f32_e32 v216, v217, v214
	v_fma_f32 v213, -v213, v216, v215
	s_nop 1
	v_div_fmas_f32 v213, v213, v214, v216
	v_div_fixup_f32 v48, v213, v212, 1.0
	s_waitcnt vmcnt(28)
	v_lshlrev_b32_e32 v32, 16, v68
	v_and_b32_e32 v33, 0xffff0000, v68
	v_lshlrev_b32_e32 v34, 16, v69
	v_and_b32_e32 v35, 0xffff0000, v69
	v_lshlrev_b32_e32 v36, 16, v70
	v_and_b32_e32 v37, 0xffff0000, v70
	v_lshlrev_b32_e32 v38, 16, v71
	v_and_b32_e32 v39, 0xffff0000, v71
	v_lshlrev_b32_e32 v40, 16, v72
	v_and_b32_e32 v41, 0xffff0000, v72
	v_lshlrev_b32_e32 v42, 16, v73
	v_and_b32_e32 v43, 0xffff0000, v73
	v_lshlrev_b32_e32 v44, 16, v74
	v_and_b32_e32 v45, 0xffff0000, v74
	v_lshlrev_b32_e32 v46, 16, v75
	v_and_b32_e32 v47, 0xffff0000, v75
	v_pk_add_f32 v[32:33], v[32:33], v[40:41]
	v_pk_add_f32 v[34:35], v[34:35], v[42:43]
	v_pk_add_f32 v[36:37], v[36:37], v[44:45]
	v_pk_add_f32 v[38:39], v[38:39], v[46:47]
	v_lshlrev_b32_e32 v40, 16, v76
	v_and_b32_e32 v41, 0xffff0000, v76
	v_lshlrev_b32_e32 v42, 16, v77
	v_and_b32_e32 v43, 0xffff0000, v77
	v_lshlrev_b32_e32 v44, 16, v78
	v_and_b32_e32 v45, 0xffff0000, v78
	v_lshlrev_b32_e32 v46, 16, v79
	v_and_b32_e32 v47, 0xffff0000, v79
	v_pk_add_f32 v[32:33], v[32:33], v[40:41]
	v_pk_add_f32 v[34:35], v[34:35], v[42:43]
	v_pk_add_f32 v[36:37], v[36:37], v[44:45]
	v_pk_add_f32 v[38:39], v[38:39], v[46:47]
	v_lshlrev_b32_e32 v40, 16, v80
	v_and_b32_e32 v41, 0xffff0000, v80
	v_lshlrev_b32_e32 v42, 16, v81
	v_and_b32_e32 v43, 0xffff0000, v81
	v_lshlrev_b32_e32 v44, 16, v82
	v_and_b32_e32 v45, 0xffff0000, v82
	v_lshlrev_b32_e32 v46, 16, v83
	v_and_b32_e32 v47, 0xffff0000, v83
	v_pk_add_f32 v[32:33], v[32:33], v[40:41]
	v_pk_add_f32 v[34:35], v[34:35], v[42:43]
	v_pk_add_f32 v[36:37], v[36:37], v[44:45]
	v_pk_add_f32 v[38:39], v[38:39], v[46:47]
	s_cmp_gt_u32 s26, 4
	s_cbranch_scc0 .Lpool_h4_q0
; #define LAS __attribute__((address_space(3)))
; template <int HALFW>
; __device__ __forceinline__ void pool_item(const bf16* P, bf16* DP, LAS float* tmp, int tid, int b, int r, int g) {
;     ...
;     for (int q = 0; q < 4; ++q) { const int p = tid + 512 * q, c = p >> 5, ch0 = (p & 31) * 8; float acc[8]; v4u x[2 * HALFW];
; #pragma unroll
;         for (int u = 0; u < 2 * HALFW; ++u) { const int rr = (rlo + u < rhi) ? rlo + u : rlo; x[u] = *(const v4u*)(P + ((size_t)(b * 2048 + rr * 64 + c)) * 1024 + g * 256 + ch0); }
; #pragma unroll
;         for (int j = 0; j < 8; ++j) acc[j] = 0.f;
; #pragma unroll
;         for (int u = 0; u < 2 * HALFW; ++u) { const float m = (rlo + u < rhi) ? 1.f : 0.f;
;             acc[0] += m * bflo(x[u].x); acc[1] += m * bfhi(x[u].x); acc[2] += m * bflo(x[u].y); acc[3] += m * bfhi(x[u].y); acc[4] += m * bflo(x[u].z); acc[5] += m * bfhi(x[u].z); acc[6] += m * bflo(x[u].w); acc[7] += m * bfhi(x[u].w); }
;         *(LAS f32x4*)(tmp + c * 256 + ch0) = (f32x4){acc[0] * rinv, acc[1] * rinv, acc[2] * rinv, acc[3] * rinv};
;         *(LAS f32x4*)(tmp + c * 256 + ch0 + 4) = (f32x4){acc[4] * rinv, acc[5] * rinv, acc[6] * rinv, acc[7] * rinv}; }
	v_lshlrev_b32_e32 v40, 16, v84
	v_and_b32_e32 v41, 0xffff0000, v84
	v_lshlrev_b32_e32 v42, 16, v85
	v_and_b32_e32 v43, 0xffff0000, v85
	v_lshlrev_b32_e32 v44, 16, v86
	v_and_b32_e32 v45, 0xffff0000, v86
	v_lshlrev_b32_e32 v46, 16, v87
	v_and_b32_e32 v47, 0xffff0000, v87
	v_pk_add_f32 v[32:33], v[32:33], v[40:41]
	v_pk_add_f32 v[34:35], v[34:35], v[42:43]
	v_pk_add_f32 v[36:37], v[36:37], v[44:45]
	v_pk_add_f32 v[38:39], v[38:39], v[46:47]
	s_cmp_gt_u32 s26, 5
	s_cbranch_scc0 .Lpool_h4_q0
	v_lshlrev_b32_e32 v40, 16, v88
	v_and_b32_e32 v41, 0xffff0000, v88
	v_lshlrev_b32_e32 v42, 16, v89
	v_and_b32_e32 v43, 0xffff0000, v89
	v_lshlrev_b32_e32 v44, 16, v90
	v_and_b32_e32 v45, 0xffff0000, v90
	v_lshlrev_b32_e32 v46, 16, v91
	v_and_b32_e32 v47, 0xffff0000, v91
	v_pk_add_f32 v[32:33], v[32:33], v[40:41]
	v_pk_add_f32 v[34:35], v[34:35], v[42:43]
	v_pk_add_f32 v[36:37], v[36:37], v[44:45]
	v_pk_add_f32 v[38:39], v[38:39], v[46:47]
	s_cmp_gt_u32 s26, 6
	s_cbranch_scc0 .Lpool_h4_q0
	v_lshlrev_b32_e32 v40, 16, v92
	v_and_b32_e32 v41, 0xffff0000, v92
	v_lshlrev_b32_e32 v42, 16, v93
	v_and_b32_e32 v43, 0xffff0000, v93
	v_lshlrev_b32_e32 v44, 16, v94
	v_and_b32_e32 v45, 0xffff0000, v94
	v_lshlrev_b32_e32 v46, 16, v95
	v_and_b32_e32 v47, 0xffff0000, v95
	v_pk_add_f32 v[32:33], v[32:33], v[40:41]
	v_pk_add_f32 v[34:35], v[34:35], v[42:43]
	v_pk_add_f32 v[36:37], v[36:37], v[44:45]
	v_pk_add_f32 v[38:39], v[38:39], v[46:47]
	s_cmp_gt_u32 s26, 7
	s_cbranch_scc0 .Lpool_h4_q0
	v_lshlrev_b32_e32 v40, 16, v96
	v_and_b32_e32 v41, 0xffff0000, v96
	v_lshlrev_b32_e32 v42, 16, v97
	v_and_b32_e32 v43, 0xffff0000, v97
	v_lshlrev_b32_e32 v44, 16, v98
	v_and_b32_e32 v45, 0xffff0000, v98
	v_lshlrev_b32_e32 v46, 16, v99
	v_and_b32_e32 v47, 0xffff0000, v99
	v_pk_add_f32 v[32:33], v[32:33], v[40:41]
	v_pk_add_f32 v[34:35], v[34:35], v[42:43]
	v_pk_add_f32 v[36:37], v[36:37], v[44:45]
	v_pk_add_f32 v[38:39], v[38:39], v[46:47]
.Lpool_h4_q0:
	v_pk_mul_f32 v[32:33], v[32:33], v[48:49] op_sel_hi:[1,0]
	v_pk_mul_f32 v[34:35], v[34:35], v[48:49] op_sel_hi:[1,0]
	v_pk_mul_f32 v[36:37], v[36:37], v[48:49] op_sel_hi:[1,0]
	v_pk_mul_f32 v[38:39], v[38:39], v[48:49] op_sel_hi:[1,0]
	ds_write_b128 v49, v[32:35] offset:0
	ds_write_b128 v49, v[36:39] offset:16
	s_waitcnt vmcnt(20)
	v_lshlrev_b32_e32 v52, 16, v100
	v_and_b32_e32 v53, 0xffff0000, v100
	v_lshlrev_b32_e32 v54, 16, v101
	v_and_b32_e32 v55, 0xffff0000, v101
	v_lshlrev_b32_e32 v56, 16, v102
	v_and_b32_e32 v57, 0xffff0000, v102
	v_lshlrev_b32_e32 v58, 16, v103
	v_and_b32_e32 v59, 0xffff0000, v103
	v_lshlrev_b32_e32 v40, 16, v104
	v_and_b32_e32 v41, 0xffff0000, v104
	v_lshlrev_b32_e32 v42, 16, v105
	v_and_b32_e32 v43, 0xffff0000, v105
	v_lshlrev_b32_e32 v44, 16, v106
	v_and_b32_e32 v45, 0xffff0000, v106
	v_lshlrev_b32_e32 v46, 16, v107
	v_and_b32_e32 v47, 0xffff0000, v107
	v_pk_add_f32 v[52:53], v[52:53], v[40:41]
	v_pk_add_f32 v[54:55], v[54:55], v[42:43]
	v_pk_add_f32 v[56:57], v[56:57], v[44:45]
	v_pk_add_f32 v[58:59], v[58:59], v[46:47]
	v_lshlrev_b32_e32 v40, 16, v108
	v_and_b32_e32 v41, 0xffff0000, v108
	v_lshlrev_b32_e32 v42, 16, v109
	v_and_b32_e32 v43, 0xffff0000, v109
	v_lshlrev_b32_e32 v44, 16, v110
	v_and_b32_e32 v45, 0xffff0000, v110
	v_lshlrev_b32_e32 v46, 16, v111
	v_and_b32_e32 v47, 0xffff0000, v111
	v_pk_add_f32 v[52:53], v[52:53], v[40:41]
	v_pk_add_f32 v[54:55], v[54:55], v[42:43]
	v_pk_add_f32 v[56:57], v[56:57], v[44:45]
	v_pk_add_f32 v[58:59], v[58:59], v[46:47]
	v_lshlrev_b32_e32 v40, 16, v112
	v_and_b32_e32 v41, 0xffff0000, v112
	v_lshlrev_b32_e32 v42, 16, v113
	v_and_b32_e32 v43, 0xffff0000, v113
	v_lshlrev_b32_e32 v44, 16, v114
	v_and_b32_e32 v45, 0xffff0000, v114
	v_lshlrev_b32_e32 v46, 16, v115
	v_and_b32_e32 v47, 0xffff0000, v115
	v_pk_add_f32 v[52:53], v[52:53], v[40:41]
	v_pk_add_f32 v[54:55], v[54:55], v[42:43]
	v_pk_add_f32 v[56:57], v[56:57], v[44:45]
	v_pk_add_f32 v[58:59], v[58:59], v[46:47]
	s_cmp_gt_u32 s26, 4
	s_cbranch_scc0 .Lpool_h4_q1
	v_lshlrev_b32_e32 v40, 16, v116
	v_and_b32_e32 v41, 0xffff0000, v116
	v_lshlrev_b32_e32 v42, 16, v117
	v_and_b32_e32 v43, 0xffff0000, v117
	v_lshlrev_b32_e32 v44, 16, v118
	v_and_b32_e32 v45, 0xffff0000, v118
	v_lshlrev_b32_e32 v46, 16, v119
	v_and_b32_e32 v47, 0xffff0000, v119
	v_pk_add_f32 v[52:53], v[52:53], v[40:41]
	v_pk_add_f32 v[54:55], v[54:55], v[42:43]
	v_pk_add_f32 v[56:57], v[56:57], v[44:45]
	v_pk_add_f32 v[58:59], v[58:59], v[46:47]
	s_cmp_gt_u32 s26, 5
	s_cbranch_scc0 .Lpool_h4_q1
	v_lshlrev_b32_e32 v40, 16, v120
	v_and_b32_e32 v41, 0xffff0000, v120
	v_lshlrev_b32_e32 v42, 16, v121
	v_and_b32_e32 v43, 0xffff0000, v121
	v_lshlrev_b32_e32 v44, 16, v122
	v_and_b32_e32 v45, 0xffff0000, v122
	v_lshlrev_b32_e32 v46, 16, v123
	v_and_b32_e32 v47, 0xffff0000, v123
	v_pk_add_f32 v[52:53], v[52:53], v[40:41]
	v_pk_add_f32 v[54:55], v[54:55], v[42:43]
	v_pk_add_f32 v[56:57], v[56:57], v[44:45]
	v_pk_add_f32 v[58:59], v[58:59], v[46:47]
	s_cmp_gt_u32 s26, 6
	s_cbranch_scc0 .Lpool_h4_q1
	v_lshlrev_b32_e32 v40, 16, v124
	v_and_b32_e32 v41, 0xffff0000, v124
	v_lshlrev_b32_e32 v42, 16, v125
	v_and_b32_e32 v43, 0xffff0000, v125
	v_lshlrev_b32_e32 v44, 16, v126
	v_and_b32_e32 v45, 0xffff0000, v126
	v_lshlrev_b32_e32 v46, 16, v127
	v_and_b32_e32 v47, 0xffff0000, v127
	v_pk_add_f32 v[52:53], v[52:53], v[40:41]
	v_pk_add_f32 v[54:55], v[54:55], v[42:43]
	v_pk_add_f32 v[56:57], v[56:57], v[44:45]
	v_pk_add_f32 v[58:59], v[58:59], v[46:47]
	s_cmp_gt_u32 s26, 7
	s_cbranch_scc0 .Lpool_h4_q1
	v_lshlrev_b32_e32 v40, 16, v128
	v_and_b32_e32 v41, 0xffff0000, v128
	v_lshlrev_b32_e32 v42, 16, v129
	v_and_b32_e32 v43, 0xffff0000, v129
	v_lshlrev_b32_e32 v44, 16, v130
	v_and_b32_e32 v45, 0xffff0000, v130
	v_lshlrev_b32_e32 v46, 16, v131
	v_and_b32_e32 v47, 0xffff0000, v131
	v_pk_add_f32 v[52:53], v[52:53], v[40:41]
	v_pk_add_f32 v[54:55], v[54:55], v[42:43]
	v_pk_add_f32 v[56:57], v[56:57], v[44:45]
	v_pk_add_f32 v[58:59], v[58:59], v[46:47]
; #define LAS __attribute__((address_space(3)))
; template <int HALFW>
; __device__ __forceinline__ void pool_item(const bf16* P, bf16* DP, LAS float* tmp, int tid, int b, int r, int g) {
;     ...
;     for (int q = 0; q < 4; ++q) { const int p = tid + 512 * q, c = p >> 5, ch0 = (p & 31) * 8; float acc[8]; v4u x[2 * HALFW];
; #pragma unroll
;         for (int u = 0; u < 2 * HALFW; ++u) { const int rr = (rlo + u < rhi) ? rlo + u : rlo; x[u] = *(const v4u*)(P + ((size_t)(b * 2048 + rr * 64 + c)) * 1024 + g * 256 + ch0); }
; #pragma unroll
;         for (int j = 0; j < 8; ++j) acc[j] = 0.f;
; #pragma unroll
;         for (int u = 0; u < 2 * HALFW; ++u) { const float m = (rlo + u < rhi) ? 1.f : 0.f;
;             acc[0] += m * bflo(x[u].x); acc[1] += m * bfhi(x[u].x); acc[2] += m * bflo(x[u].y); acc[3] += m * bfhi(x[u].y); acc[4] += m * bflo(x[u].z); acc[5] += m * bfhi(x[u].z); acc[6] += m * bflo(x[u].w); acc[7] += m * bfhi(x[u].w); }
;         *(LAS f32x4*)(tmp + c * 256 + ch0) = (f32x4){acc[0] * rinv, acc[1] * rinv, acc[2] * rinv, acc[3] * rinv};
;         *(LAS f32x4*)(tmp + c * 256 + ch0 + 4) = (f32x4){acc[4] * rinv, acc[5] * rinv, acc[6] * rinv, acc[7] * rinv}; }
.Lpool_h4_q1:
	v_pk_mul_f32 v[52:53], v[52:53], v[48:49] op_sel_hi:[1,0]
	v_pk_mul_f32 v[54:55], v[54:55], v[48:49] op_sel_hi:[1,0]
	v_pk_mul_f32 v[56:57], v[56:57], v[48:49] op_sel_hi:[1,0]
	v_pk_mul_f32 v[58:59], v[58:59], v[48:49] op_sel_hi:[1,0]
	ds_write_b128 v49, v[52:55] offset:16384
	ds_write_b128 v49, v[56:59] offset:16400
	s_waitcnt vmcnt(12)
	v_lshlrev_b32_e32 v32, 16, v132
	v_and_b32_e32 v33, 0xffff0000, v132
	v_lshlrev_b32_e32 v34, 16, v133
	v_and_b32_e32 v35, 0xffff0000, v133
	v_lshlrev_b32_e32 v36, 16, v134
	v_and_b32_e32 v37, 0xffff0000, v134
	v_lshlrev_b32_e32 v38, 16, v135
	v_and_b32_e32 v39, 0xffff0000, v135
	v_lshlrev_b32_e32 v40, 16, v136
	v_and_b32_e32 v41, 0xffff0000, v136
	v_lshlrev_b32_e32 v42, 16, v137
	v_and_b32_e32 v43, 0xffff0000, v137
	v_lshlrev_b32_e32 v44, 16, v138
	v_and_b32_e32 v45, 0xffff0000, v138
	v_lshlrev_b32_e32 v46, 16, v139
	v_and_b32_e32 v47, 0xffff0000, v139
	v_pk_add_f32 v[32:33], v[32:33], v[40:41]
	v_pk_add_f32 v[34:35], v[34:35], v[42:43]
	v_pk_add_f32 v[36:37], v[36:37], v[44:45]
	v_pk_add_f32 v[38:39], v[38:39], v[46:47]
	v_lshlrev_b32_e32 v40, 16, v140
	v_and_b32_e32 v41, 0xffff0000, v140
	v_lshlrev_b32_e32 v42, 16, v141
	v_and_b32_e32 v43, 0xffff0000, v141
	v_lshlrev_b32_e32 v44, 16, v142
	v_and_b32_e32 v45, 0xffff0000, v142
	v_lshlrev_b32_e32 v46, 16, v143
	v_and_b32_e32 v47, 0xffff0000, v143
	v_pk_add_f32 v[32:33], v[32:33], v[40:41]
	v_pk_add_f32 v[34:35], v[34:35], v[42:43]
	v_pk_add_f32 v[36:37], v[36:37], v[44:45]
	v_pk_add_f32 v[38:39], v[38:39], v[46:47]
	v_lshlrev_b32_e32 v40, 16, v144
	v_and_b32_e32 v41, 0xffff0000, v144
	v_lshlrev_b32_e32 v42, 16, v145
	v_and_b32_e32 v43, 0xffff0000, v145
	v_lshlrev_b32_e32 v44, 16, v146
	v_and_b32_e32 v45, 0xffff0000, v146
	v_lshlrev_b32_e32 v46, 16, v147
	v_and_b32_e32 v47, 0xffff0000, v147
	v_pk_add_f32 v[32:33], v[32:33], v[40:41]
	v_pk_add_f32 v[34:35], v[34:35], v[42:43]
	v_pk_add_f32 v[36:37], v[36:37], v[44:45]
	v_pk_add_f32 v[38:39], v[38:39], v[46:47]
	s_cmp_gt_u32 s26, 4
	s_cbranch_scc0 .Lpool_h4_q2
	v_lshlrev_b32_e32 v40, 16, v148
	v_and_b32_e32 v41, 0xffff0000, v148
	v_lshlrev_b32_e32 v42, 16, v149
	v_and_b32_e32 v43, 0xffff0000, v149
	v_lshlrev_b32_e32 v44, 16, v150
	v_and_b32_e32 v45, 0xffff0000, v150
	v_lshlrev_b32_e32 v46, 16, v151
	v_and_b32_e32 v47, 0xffff0000, v151
	v_pk_add_f32 v[32:33], v[32:33], v[40:41]
	v_pk_add_f32 v[34:35], v[34:35], v[42:43]
	v_pk_add_f32 v[36:37], v[36:37], v[44:45]
	v_pk_add_f32 v[38:39], v[38:39], v[46:47]
	s_cmp_gt_u32 s26, 5
	s_cbranch_scc0 .Lpool_h4_q2
	v_lshlrev_b32_e32 v40, 16, v152
	v_and_b32_e32 v41, 0xffff0000, v152
	v_lshlrev_b32_e32 v42, 16, v153
	v_and_b32_e32 v43, 0xffff0000, v153
	v_lshlrev_b32_e32 v44, 16, v154
	v_and_b32_e32 v45, 0xffff0000, v154
	v_lshlrev_b32_e32 v46, 16, v155
	v_and_b32_e32 v47, 0xffff0000, v155
	v_pk_add_f32 v[32:33], v[32:33], v[40:41]
	v_pk_add_f32 v[34:35], v[34:35], v[42:43]
	v_pk_add_f32 v[36:37], v[36:37], v[44:45]
	v_pk_add_f32 v[38:39], v[38:39], v[46:47]
	s_cmp_gt_u32 s26, 6
	s_cbranch_scc0 .Lpool_h4_q2
	v_lshlrev_b32_e32 v40, 16, v156
	v_and_b32_e32 v41, 0xffff0000, v156
	v_lshlrev_b32_e32 v42, 16, v157
	v_and_b32_e32 v43, 0xffff0000, v157
	v_lshlrev_b32_e32 v44, 16, v158
	v_and_b32_e32 v45, 0xffff0000, v158
	v_lshlrev_b32_e32 v46, 16, v159
	v_and_b32_e32 v47, 0xffff0000, v159
	v_pk_add_f32 v[32:33], v[32:33], v[40:41]
	v_pk_add_f32 v[34:35], v[34:35], v[42:43]
	v_pk_add_f32 v[36:37], v[36:37], v[44:45]
	v_pk_add_f32 v[38:39], v[38:39], v[46:47]
	s_cmp_gt_u32 s26, 7
	s_cbranch_scc0 .Lpool_h4_q2
	v_lshlrev_b32_e32 v40, 16, v160
	v_and_b32_e32 v41, 0xffff0000, v160
	v_lshlrev_b32_e32 v42, 16, v161
	v_and_b32_e32 v43, 0xffff0000, v161
	v_lshlrev_b32_e32 v44, 16, v162
	v_and_b32_e32 v45, 0xffff0000, v162
	v_lshlrev_b32_e32 v46, 16, v163
	v_and_b32_e32 v47, 0xffff0000, v163
	v_pk_add_f32 v[32:33], v[32:33], v[40:41]
	v_pk_add_f32 v[34:35], v[34:35], v[42:43]
	v_pk_add_f32 v[36:37], v[36:37], v[44:45]
	v_pk_add_f32 v[38:39], v[38:39], v[46:47]
.Lpool_h4_q2:
	v_pk_mul_f32 v[32:33], v[32:33], v[48:49] op_sel_hi:[1,0]
	v_pk_mul_f32 v[34:35], v[34:35], v[48:49] op_sel_hi:[1,0]
	v_pk_mul_f32 v[36:37], v[36:37], v[48:49] op_sel_hi:[1,0]
	v_pk_mul_f32 v[38:39], v[38:39], v[48:49] op_sel_hi:[1,0]
	ds_write_b128 v49, v[32:35] offset:32768
	ds_write_b128 v49, v[36:39] offset:32784
	s_waitcnt vmcnt(4)
	v_lshlrev_b32_e32 v52, 16, v164
	v_and_b32_e32 v53, 0xffff0000, v164
	v_lshlrev_b32_e32 v54, 16, v165
	v_and_b32_e32 v55, 0xffff0000, v165
	v_lshlrev_b32_e32 v56, 16, v166
	v_and_b32_e32 v57, 0xffff0000, v166
	v_lshlrev_b32_e32 v58, 16, v167
	v_and_b32_e32 v59, 0xffff0000, v167
	v_lshlrev_b32_e32 v40, 16, v168
	v_and_b32_e32 v41, 0xffff0000, v168
	v_lshlrev_b32_e32 v42, 16, v169
	v_and_b32_e32 v43, 0xffff0000, v169
	v_lshlrev_b32_e32 v44, 16, v170
	v_and_b32_e32 v45, 0xffff0000, v170
	v_lshlrev_b32_e32 v46, 16, v171
	v_and_b32_e32 v47, 0xffff0000, v171
	v_pk_add_f32 v[52:53], v[52:53], v[40:41]
	v_pk_add_f32 v[54:55], v[54:55], v[42:43]
	v_pk_add_f32 v[56:57], v[56:57], v[44:45]
	v_pk_add_f32 v[58:59], v[58:59], v[46:47]
	v_lshlrev_b32_e32 v40, 16, v172
	v_and_b32_e32 v41, 0xffff0000, v172
	v_lshlrev_b32_e32 v42, 16, v173
	v_and_b32_e32 v43, 0xffff0000, v173
	v_lshlrev_b32_e32 v44, 16, v174
	v_and_b32_e32 v45, 0xffff0000, v174
	v_lshlrev_b32_e32 v46, 16, v175
	v_and_b32_e32 v47, 0xffff0000, v175
	v_pk_add_f32 v[52:53], v[52:53], v[40:41]
	v_pk_add_f32 v[54:55], v[54:55], v[42:43]
	v_pk_add_f32 v[56:57], v[56:57], v[44:45]
	v_pk_add_f32 v[58:59], v[58:59], v[46:47]
	v_lshlrev_b32_e32 v40, 16, v176
	v_and_b32_e32 v41, 0xffff0000, v176
	v_lshlrev_b32_e32 v42, 16, v177
	v_and_b32_e32 v43, 0xffff0000, v177
	v_lshlrev_b32_e32 v44, 16, v178
	v_and_b32_e32 v45, 0xffff0000, v178
	v_lshlrev_b32_e32 v46, 16, v179
	v_and_b32_e32 v47, 0xffff0000, v179
	v_pk_add_f32 v[52:53], v[52:53], v[40:41]
	v_pk_add_f32 v[54:55], v[54:55], v[42:43]
	v_pk_add_f32 v[56:57], v[56:57], v[44:45]
	v_pk_add_f32 v[58:59], v[58:59], v[46:47]
	s_cmp_gt_u32 s26, 4
	s_cbranch_scc0 .Lpool_h4_q3
; #define LAS __attribute__((address_space(3)))
; template <int HALFW>
; __device__ __forceinline__ void pool_item(const bf16* P, bf16* DP, LAS float* tmp, int tid, int b, int r, int g) {
;     ...
;         for (int u = 0; u < 2 * HALFW; ++u) { const float m = (rlo + u < rhi) ? 1.f : 0.f;
;             acc[0] += m * bflo(x[u].x); acc[1] += m * bfhi(x[u].x); acc[2] += m * bflo(x[u].y); acc[3] += m * bfhi(x[u].y); acc[4] += m * bflo(x[u].z); acc[5] += m * bfhi(x[u].z); acc[6] += m * bflo(x[u].w); acc[7] += m * bfhi(x[u].w); }
;         *(LAS f32x4*)(tmp + c * 256 + ch0) = (f32x4){acc[0] * rinv, acc[1] * rinv, acc[2] * rinv, acc[3] * rinv};
;         *(LAS f32x4*)(tmp + c * 256 + ch0 + 4) = (f32x4){acc[4] * rinv, acc[5] * rinv, acc[6] * rinv, acc[7] * rinv}; }
;     __syncthreads();
; #pragma unroll 1
;     for (int q = 0; q < 4; ++q) { const int p = tid + 512 * q, c = p >> 5, ch0 = (p & 31) * 8;
;         const int clo = c - HALFW < 0 ? 0 : c - HALFW, chi = c + HALFW > 64 ? 64 : c + HALFW; const float cinv = 1.f / (float)(chi - clo);
	v_lshlrev_b32_e32 v40, 16, v180
	v_and_b32_e32 v41, 0xffff0000, v180
	v_lshlrev_b32_e32 v42, 16, v181
	v_and_b32_e32 v43, 0xffff0000, v181
	v_lshlrev_b32_e32 v44, 16, v182
	v_and_b32_e32 v45, 0xffff0000, v182
	v_lshlrev_b32_e32 v46, 16, v183
	v_and_b32_e32 v47, 0xffff0000, v183
	v_pk_add_f32 v[52:53], v[52:53], v[40:41]
	v_pk_add_f32 v[54:55], v[54:55], v[42:43]
	v_pk_add_f32 v[56:57], v[56:57], v[44:45]
	v_pk_add_f32 v[58:59], v[58:59], v[46:47]
	s_cmp_gt_u32 s26, 5
	s_cbranch_scc0 .Lpool_h4_q3
	v_lshlrev_b32_e32 v40, 16, v184
	v_and_b32_e32 v41, 0xffff0000, v184
	v_lshlrev_b32_e32 v42, 16, v185
	v_and_b32_e32 v43, 0xffff0000, v185
	v_lshlrev_b32_e32 v44, 16, v186
	v_and_b32_e32 v45, 0xffff0000, v186
	v_lshlrev_b32_e32 v46, 16, v187
	v_and_b32_e32 v47, 0xffff0000, v187
	v_pk_add_f32 v[52:53], v[52:53], v[40:41]
	v_pk_add_f32 v[54:55], v[54:55], v[42:43]
	v_pk_add_f32 v[56:57], v[56:57], v[44:45]
	v_pk_add_f32 v[58:59], v[58:59], v[46:47]
	s_cmp_gt_u32 s26, 6
	s_cbranch_scc0 .Lpool_h4_q3
	v_lshlrev_b32_e32 v40, 16, v188
	v_and_b32_e32 v41, 0xffff0000, v188
	v_lshlrev_b32_e32 v42, 16, v189
	v_and_b32_e32 v43, 0xffff0000, v189
	v_lshlrev_b32_e32 v44, 16, v190
	v_and_b32_e32 v45, 0xffff0000, v190
	v_lshlrev_b32_e32 v46, 16, v191
	v_and_b32_e32 v47, 0xffff0000, v191
	v_pk_add_f32 v[52:53], v[52:53], v[40:41]
	v_pk_add_f32 v[54:55], v[54:55], v[42:43]
	v_pk_add_f32 v[56:57], v[56:57], v[44:45]
	v_pk_add_f32 v[58:59], v[58:59], v[46:47]
	s_cmp_gt_u32 s26, 7
	s_cbranch_scc0 .Lpool_h4_q3
	v_lshlrev_b32_e32 v40, 16, v192
	v_and_b32_e32 v41, 0xffff0000, v192
	v_lshlrev_b32_e32 v42, 16, v193
	v_and_b32_e32 v43, 0xffff0000, v193
	v_lshlrev_b32_e32 v44, 16, v194
	v_and_b32_e32 v45, 0xffff0000, v194
	v_lshlrev_b32_e32 v46, 16, v195
	v_and_b32_e32 v47, 0xffff0000, v195
	v_pk_add_f32 v[52:53], v[52:53], v[40:41]
	v_pk_add_f32 v[54:55], v[54:55], v[42:43]
	v_pk_add_f32 v[56:57], v[56:57], v[44:45]
	v_pk_add_f32 v[58:59], v[58:59], v[46:47]
.Lpool_h4_q3:
	v_pk_mul_f32 v[52:53], v[52:53], v[48:49] op_sel_hi:[1,0]
	v_pk_mul_f32 v[54:55], v[54:55], v[48:49] op_sel_hi:[1,0]
	v_pk_mul_f32 v[56:57], v[56:57], v[48:49] op_sel_hi:[1,0]
	v_pk_mul_f32 v[58:59], v[58:59], v[48:49] op_sel_hi:[1,0]
	ds_write_b128 v49, v[52:55] offset:49152
	ds_write_b128 v49, v[56:59] offset:49168
	v_add_u32_e32 v51, 0, v50
	v_add_u32_e32 v60, 4, v51
	v_min_u32_e32 v60, 64, v60
	v_sub_u32_e64 v61, v51, 4 clamp
	v_sub_u32_e32 v60, v60, v61
	v_cvt_f32_u32_e32 v212, v60
	v_div_scale_f32 v213, s[30:31], v212, v212, 1.0
	v_div_scale_f32 v215, vcc, 1.0, v212, 1.0
	v_rcp_f32_e32 v214, v213
	s_nop 1
	v_fma_f32 v216, -v213, v214, 1.0
	v_fmac_f32_e32 v214, v216, v214
	v_mul_f32_e32 v216, v215, v214
	v_fma_f32 v217, -v213, v216, v215
	v_fmac_f32_e32 v216, v217, v214
	v_fma_f32 v213, -v213, v216, v215
	s_nop 1
	v_div_fmas_f32 v213, v213, v214, v216
	v_div_fixup_f32 v196, v213, v212, 1.0
	v_add_u32_e32 v51, 16, v50
	v_add_u32_e32 v60, 4, v51
	v_min_u32_e32 v60, 64, v60
	v_sub_u32_e64 v61, v51, 4 clamp
	v_sub_u32_e32 v60, v60, v61
	v_cvt_f32_u32_e32 v212, v60
	v_div_scale_f32 v213, s[30:31], v212, v212, 1.0
	v_div_scale_f32 v215, vcc, 1.0, v212, 1.0
	v_rcp_f32_e32 v214, v213
	s_nop 1
	v_fma_f32 v216, -v213, v214, 1.0
	v_fmac_f32_e32 v214, v216, v214
	v_mul_f32_e32 v216, v215, v214
	v_fma_f32 v217, -v213, v216, v215
	v_fmac_f32_e32 v216, v217, v214
	v_fma_f32 v213, -v213, v216, v215
	s_nop 1
	v_div_fmas_f32 v213, v213, v214, v216
	v_div_fixup_f32 v198, v213, v212, 1.0
	v_add_u32_e32 v51, 32, v50
	v_add_u32_e32 v60, 4, v51
	v_min_u32_e32 v60, 64, v60
	v_sub_u32_e64 v61, v51, 4 clamp
	v_sub_u32_e32 v60, v60, v61
	v_cvt_f32_u32_e32 v212, v60
	v_div_scale_f32 v213, s[30:31], v212, v212, 1.0
	v_div_scale_f32 v215, vcc, 1.0, v212, 1.0
	v_rcp_f32_e32 v214, v213
	s_nop 1
	v_fma_f32 v216, -v213, v214, 1.0
	v_fmac_f32_e32 v214, v216, v214
	v_mul_f32_e32 v216, v215, v214
	v_fma_f32 v217, -v213, v216, v215
	v_fmac_f32_e32 v216, v217, v214
	v_fma_f32 v213, -v213, v216, v215
	s_nop 1
	v_div_fmas_f32 v213, v213, v214, v216
	v_div_fixup_f32 v200, v213, v212, 1.0
	v_add_u32_e32 v51, 48, v50
	v_add_u32_e32 v60, 4, v51
	v_min_u32_e32 v60, 64, v60
	v_sub_u32_e64 v61, v51, 4 clamp
	v_sub_u32_e32 v60, v60, v61
	v_cvt_f32_u32_e32 v212, v60
	v_div_scale_f32 v213, s[30:31], v212, v212, 1.0
	v_div_scale_f32 v215, vcc, 1.0, v212, 1.0
	v_rcp_f32_e32 v214, v213
	s_nop 1
	v_fma_f32 v216, -v213, v214, 1.0
	v_fmac_f32_e32 v214, v216, v214
	v_mul_f32_e32 v216, v215, v214
	v_fma_f32 v217, -v213, v216, v215
	v_fmac_f32_e32 v216, v217, v214
	v_fma_f32 v213, -v213, v216, v215
	s_nop 1
	v_div_fmas_f32 v213, v213, v214, v216
	v_div_fixup_f32 v202, v213, v212, 1.0
	s_waitcnt lgkmcnt(0)
	s_barrier
; #define LAS __attribute__((address_space(3)))
; __device__ __forceinline__ unsigned pk2(float lo, float hi) { return f2bf(lo) | (f2bf(hi) << 16); }
; template <int HALFW>
; __device__ __forceinline__ void pool_item(const bf16* P, bf16* DP, LAS float* tmp, int tid, int b, int r, int g) {
;     ...
;     for (int q = 0; q < 4; ++q) { const int p = tid + 512 * q, c = p >> 5, ch0 = (p & 31) * 8;
;         const int clo = c - HALFW < 0 ? 0 : c - HALFW, chi = c + HALFW > 64 ? 64 : c + HALFW; const float cinv = 1.f / (float)(chi - clo);
;         const size_t o = ((size_t)(b * 2048 + r * 64 + c)) * 1024 + g * 256 + ch0;
;         const v4u x = *(const v4u*)(P + o);
;         f32x4 a0 = (f32x4){0.f, 0.f, 0.f, 0.f}, a1 = a0;
; #pragma unroll
;         for (int u = 0; u < 2 * HALFW; ++u) { const int cc = (clo + u < chi) ? clo + u : clo; const float m = (clo + u < chi) ? 1.f : 0.f;
;             a0 += *(const LAS f32x4*)(tmp + cc * 256 + ch0) * m; a1 += *(const LAS f32x4*)(tmp + cc * 256 + ch0 + 4) * m; }
;         v4u d; d.x = pk2(a0[0] * cinv - bflo(x.x), a0[1] * cinv - bfhi(x.x)); d.y = pk2(a0[2] * cinv - bflo(x.y), a0[3] * cinv - bfhi(x.y));
;         d.z = pk2(a1[0] * cinv - bflo(x.z), a1[1] * cinv - bfhi(x.z)); d.w = pk2(a1[2] * cinv - bflo(x.w), a1[3] * cinv - bfhi(x.w));
;         *(v4u*)(DP + o) = d; }
	v_add_u32_e32 v51, -4, v50
	v_add_u32_e32 v60, 0, v51
	v_min_u32_e32 v60, 64, v60
	v_lshl_add_u32 v60, v60, 10, v3
	ds_read_b128 v[204:207], v60
	ds_read_b128 v[208:211], v60 offset:16
	v_add_u32_e32 v60, 1, v51
	v_min_u32_e32 v60, 64, v60
	v_lshl_add_u32 v60, v60, 10, v3
	ds_read_b128 v[76:79], v60
	ds_read_b128 v[80:83], v60 offset:16
	v_add_u32_e32 v60, 2, v51
	v_min_u32_e32 v60, 64, v60
	v_lshl_add_u32 v60, v60, 10, v3
	ds_read_b128 v[84:87], v60
	ds_read_b128 v[88:91], v60 offset:16
	v_add_u32_e32 v60, 3, v51
	v_min_u32_e32 v60, 64, v60
	v_lshl_add_u32 v60, v60, 10, v3
	ds_read_b128 v[92:95], v60
	ds_read_b128 v[96:99], v60 offset:16
	v_add_u32_e32 v60, 4, v51
	v_min_u32_e32 v60, 64, v60
	v_lshl_add_u32 v60, v60, 10, v3
	ds_read_b128 v[100:103], v60
	ds_read_b128 v[104:107], v60 offset:16
	v_add_u32_e32 v60, 5, v51
	v_min_u32_e32 v60, 64, v60
	v_lshl_add_u32 v60, v60, 10, v3
	ds_read_b128 v[108:111], v60
	ds_read_b128 v[112:115], v60 offset:16
	s_waitcnt lgkmcnt(8)
	v_pk_add_f32 v[204:205], v[204:205], v[76:77]
	v_pk_add_f32 v[206:207], v[206:207], v[78:79]
	v_pk_add_f32 v[208:209], v[208:209], v[80:81]
	v_pk_add_f32 v[210:211], v[210:211], v[82:83]
	v_add_u32_e32 v60, 6, v51
	v_min_u32_e32 v60, 64, v60
	v_lshl_add_u32 v60, v60, 10, v3
	ds_read_b128 v[68:71], v60
	ds_read_b128 v[72:75], v60 offset:16
	v_add_u32_e32 v60, 7, v51
	v_min_u32_e32 v60, 64, v60
	v_lshl_add_u32 v60, v60, 10, v3
	ds_read_b128 v[76:79], v60
	ds_read_b128 v[80:83], v60 offset:16
	s_waitcnt lgkmcnt(8)
	v_pk_add_f32 v[204:205], v[204:205], v[84:85]
	v_pk_add_f32 v[206:207], v[206:207], v[86:87]
	v_pk_add_f32 v[208:209], v[208:209], v[88:89]
	v_pk_add_f32 v[210:211], v[210:211], v[90:91]
	v_pk_add_f32 v[204:205], v[204:205], v[92:93]
	v_pk_add_f32 v[206:207], v[206:207], v[94:95]
	v_pk_add_f32 v[208:209], v[208:209], v[96:97]
	v_pk_add_f32 v[210:211], v[210:211], v[98:99]
	s_waitcnt lgkmcnt(4)
	v_pk_add_f32 v[204:205], v[204:205], v[100:101]
	v_pk_add_f32 v[206:207], v[206:207], v[102:103]
	v_pk_add_f32 v[208:209], v[208:209], v[104:105]
	v_pk_add_f32 v[210:211], v[210:211], v[106:107]
	v_pk_add_f32 v[204:205], v[204:205], v[108:109]
	v_pk_add_f32 v[206:207], v[206:207], v[110:111]
	v_pk_add_f32 v[208:209], v[208:209], v[112:113]
	v_pk_add_f32 v[210:211], v[210:211], v[114:115]
	s_waitcnt lgkmcnt(0)
	v_pk_add_f32 v[204:205], v[204:205], v[68:69]
	v_pk_add_f32 v[206:207], v[206:207], v[70:71]
	v_pk_add_f32 v[208:209], v[208:209], v[72:73]
	v_pk_add_f32 v[210:211], v[210:211], v[74:75]
	v_pk_add_f32 v[204:205], v[204:205], v[76:77]
	v_pk_add_f32 v[206:207], v[206:207], v[78:79]
	v_pk_add_f32 v[208:209], v[208:209], v[80:81]
	v_pk_add_f32 v[210:211], v[210:211], v[82:83]
	s_waitcnt vmcnt(0)
	v_lshlrev_b32_e32 v40, 16, v16
	v_and_b32_e32 v41, 0xffff0000, v16
	v_lshlrev_b32_e32 v42, 16, v17
	v_and_b32_e32 v43, 0xffff0000, v17
	v_lshlrev_b32_e32 v44, 16, v18
	v_and_b32_e32 v45, 0xffff0000, v18
	v_lshlrev_b32_e32 v46, 16, v19
	v_and_b32_e32 v47, 0xffff0000, v19
	v_pk_fma_f32 v[40:41], v[196:197], v[204:205], v[40:41] op_sel_hi:[0,1,1] neg_lo:[0,0,1] neg_hi:[0,0,1]
	v_pk_fma_f32 v[42:43], v[196:197], v[206:207], v[42:43] op_sel_hi:[0,1,1] neg_lo:[0,0,1] neg_hi:[0,0,1]
	v_pk_fma_f32 v[44:45], v[196:197], v[208:209], v[44:45] op_sel_hi:[0,1,1] neg_lo:[0,0,1] neg_hi:[0,0,1]
	v_pk_fma_f32 v[46:47], v[196:197], v[210:211], v[46:47] op_sel_hi:[0,1,1] neg_lo:[0,0,1] neg_hi:[0,0,1]
	v_cvt_pk_bf16_f32 v218, v40, v41
	v_cvt_pk_bf16_f32 v219, v42, v43
	v_cvt_pk_bf16_f32 v220, v44, v45
	v_cvt_pk_bf16_f32 v221, v46, v47
	global_store_dwordx4 v12, v[218:221], s[24:25]
	v_add_u32_e32 v51, 12, v50
	v_add_u32_e32 v60, 0, v51
	v_min_u32_e32 v60, 64, v60
	v_lshl_add_u32 v60, v60, 10, v3
	ds_read_b128 v[204:207], v60
	ds_read_b128 v[208:211], v60 offset:16
	v_add_u32_e32 v60, 1, v51
	v_min_u32_e32 v60, 64, v60
	v_lshl_add_u32 v60, v60, 10, v3
	ds_read_b128 v[76:79], v60
	ds_read_b128 v[80:83], v60 offset:16
	v_add_u32_e32 v60, 2, v51
	v_min_u32_e32 v60, 64, v60
	v_lshl_add_u32 v60, v60, 10, v3
	ds_read_b128 v[84:87], v60
	ds_read_b128 v[88:91], v60 offset:16
	v_add_u32_e32 v60, 3, v51
	v_min_u32_e32 v60, 64, v60
	v_lshl_add_u32 v60, v60, 10, v3
	ds_read_b128 v[92:95], v60
	ds_read_b128 v[96:99], v60 offset:16
	v_add_u32_e32 v60, 4, v51
	v_min_u32_e32 v60, 64, v60
	v_lshl_add_u32 v60, v60, 10, v3
	ds_read_b128 v[100:103], v60
	ds_read_b128 v[104:107], v60 offset:16
	v_add_u32_e32 v60, 5, v51
	v_min_u32_e32 v60, 64, v60
	v_lshl_add_u32 v60, v60, 10, v3
	ds_read_b128 v[108:111], v60
	ds_read_b128 v[112:115], v60 offset:16
	s_waitcnt lgkmcnt(8)
	v_pk_add_f32 v[204:205], v[204:205], v[76:77]
	v_pk_add_f32 v[206:207], v[206:207], v[78:79]
	v_pk_add_f32 v[208:209], v[208:209], v[80:81]
	v_pk_add_f32 v[210:211], v[210:211], v[82:83]
	v_add_u32_e32 v60, 6, v51
	v_min_u32_e32 v60, 64, v60
	v_lshl_add_u32 v60, v60, 10, v3
	ds_read_b128 v[68:71], v60
	ds_read_b128 v[72:75], v60 offset:16
	v_add_u32_e32 v60, 7, v51
	v_min_u32_e32 v60, 64, v60
	v_lshl_add_u32 v60, v60, 10, v3
	ds_read_b128 v[76:79], v60
	ds_read_b128 v[80:83], v60 offset:16
	s_waitcnt lgkmcnt(8)
	v_pk_add_f32 v[204:205], v[204:205], v[84:85]
	v_pk_add_f32 v[206:207], v[206:207], v[86:87]
	v_pk_add_f32 v[208:209], v[208:209], v[88:89]
	v_pk_add_f32 v[210:211], v[210:211], v[90:91]
	v_pk_add_f32 v[204:205], v[204:205], v[92:93]
	v_pk_add_f32 v[206:207], v[206:207], v[94:95]
	v_pk_add_f32 v[208:209], v[208:209], v[96:97]
	v_pk_add_f32 v[210:211], v[210:211], v[98:99]
	s_waitcnt lgkmcnt(4)
; #define LAS __attribute__((address_space(3)))
; __device__ __forceinline__ unsigned pk2(float lo, float hi) { return f2bf(lo) | (f2bf(hi) << 16); }
; template <int HALFW>
; __device__ __forceinline__ void pool_item(const bf16* P, bf16* DP, LAS float* tmp, int tid, int b, int r, int g) {
;     ...
;     for (int q = 0; q < 4; ++q) { const int p = tid + 512 * q, c = p >> 5, ch0 = (p & 31) * 8;
;         const int clo = c - HALFW < 0 ? 0 : c - HALFW, chi = c + HALFW > 64 ? 64 : c + HALFW; const float cinv = 1.f / (float)(chi - clo);
;         const size_t o = ((size_t)(b * 2048 + r * 64 + c)) * 1024 + g * 256 + ch0;
;         const v4u x = *(const v4u*)(P + o);
;         f32x4 a0 = (f32x4){0.f, 0.f, 0.f, 0.f}, a1 = a0;
; #pragma unroll
;         for (int u = 0; u < 2 * HALFW; ++u) { const int cc = (clo + u < chi) ? clo + u : clo; const float m = (clo + u < chi) ? 1.f : 0.f;
;             a0 += *(const LAS f32x4*)(tmp + cc * 256 + ch0) * m; a1 += *(const LAS f32x4*)(tmp + cc * 256 + ch0 + 4) * m; }
;         v4u d; d.x = pk2(a0[0] * cinv - bflo(x.x), a0[1] * cinv - bfhi(x.x)); d.y = pk2(a0[2] * cinv - bflo(x.y), a0[3] * cinv - bfhi(x.y));
;         d.z = pk2(a1[0] * cinv - bflo(x.z), a1[1] * cinv - bfhi(x.z)); d.w = pk2(a1[2] * cinv - bflo(x.w), a1[3] * cinv - bfhi(x.w));
;         *(v4u*)(DP + o) = d; }
	v_pk_add_f32 v[204:205], v[204:205], v[100:101]
	v_pk_add_f32 v[206:207], v[206:207], v[102:103]
	v_pk_add_f32 v[208:209], v[208:209], v[104:105]
	v_pk_add_f32 v[210:211], v[210:211], v[106:107]
	v_pk_add_f32 v[204:205], v[204:205], v[108:109]
	v_pk_add_f32 v[206:207], v[206:207], v[110:111]
	v_pk_add_f32 v[208:209], v[208:209], v[112:113]
	v_pk_add_f32 v[210:211], v[210:211], v[114:115]
	s_waitcnt lgkmcnt(0)
	v_pk_add_f32 v[204:205], v[204:205], v[68:69]
	v_pk_add_f32 v[206:207], v[206:207], v[70:71]
	v_pk_add_f32 v[208:209], v[208:209], v[72:73]
	v_pk_add_f32 v[210:211], v[210:211], v[74:75]
	v_pk_add_f32 v[204:205], v[204:205], v[76:77]
	v_pk_add_f32 v[206:207], v[206:207], v[78:79]
	v_pk_add_f32 v[208:209], v[208:209], v[80:81]
	v_pk_add_f32 v[210:211], v[210:211], v[82:83]
	v_lshlrev_b32_e32 v40, 16, v20
	v_and_b32_e32 v41, 0xffff0000, v20
	v_lshlrev_b32_e32 v42, 16, v21
	v_and_b32_e32 v43, 0xffff0000, v21
	v_lshlrev_b32_e32 v44, 16, v22
	v_and_b32_e32 v45, 0xffff0000, v22
	v_lshlrev_b32_e32 v46, 16, v23
	v_and_b32_e32 v47, 0xffff0000, v23
	v_pk_fma_f32 v[40:41], v[198:199], v[204:205], v[40:41] op_sel_hi:[0,1,1] neg_lo:[0,0,1] neg_hi:[0,0,1]
	v_pk_fma_f32 v[42:43], v[198:199], v[206:207], v[42:43] op_sel_hi:[0,1,1] neg_lo:[0,0,1] neg_hi:[0,0,1]
	v_pk_fma_f32 v[44:45], v[198:199], v[208:209], v[44:45] op_sel_hi:[0,1,1] neg_lo:[0,0,1] neg_hi:[0,0,1]
	v_pk_fma_f32 v[46:47], v[198:199], v[210:211], v[46:47] op_sel_hi:[0,1,1] neg_lo:[0,0,1] neg_hi:[0,0,1]
	v_cvt_pk_bf16_f32 v222, v40, v41
	v_cvt_pk_bf16_f32 v223, v42, v43
	v_cvt_pk_bf16_f32 v224, v44, v45
	v_cvt_pk_bf16_f32 v225, v46, v47
	global_store_dwordx4 v13, v[222:225], s[24:25]
	v_add_u32_e32 v51, 28, v50
	v_add_u32_e32 v60, 0, v51
	v_min_u32_e32 v60, 64, v60
	v_lshl_add_u32 v60, v60, 10, v3
	ds_read_b128 v[204:207], v60
	ds_read_b128 v[208:211], v60 offset:16
	v_add_u32_e32 v60, 1, v51
	v_min_u32_e32 v60, 64, v60
	v_lshl_add_u32 v60, v60, 10, v3
	ds_read_b128 v[76:79], v60
	ds_read_b128 v[80:83], v60 offset:16
	v_add_u32_e32 v60, 2, v51
	v_min_u32_e32 v60, 64, v60
	v_lshl_add_u32 v60, v60, 10, v3
	ds_read_b128 v[84:87], v60
	ds_read_b128 v[88:91], v60 offset:16
	v_add_u32_e32 v60, 3, v51
	v_min_u32_e32 v60, 64, v60
	v_lshl_add_u32 v60, v60, 10, v3
	ds_read_b128 v[92:95], v60
	ds_read_b128 v[96:99], v60 offset:16
	v_add_u32_e32 v60, 4, v51
	v_min_u32_e32 v60, 64, v60
	v_lshl_add_u32 v60, v60, 10, v3
	ds_read_b128 v[100:103], v60
	ds_read_b128 v[104:107], v60 offset:16
	v_add_u32_e32 v60, 5, v51
	v_min_u32_e32 v60, 64, v60
	v_lshl_add_u32 v60, v60, 10, v3
	ds_read_b128 v[108:111], v60
	ds_read_b128 v[112:115], v60 offset:16
	s_waitcnt lgkmcnt(8)
	v_pk_add_f32 v[204:205], v[204:205], v[76:77]
	v_pk_add_f32 v[206:207], v[206:207], v[78:79]
	v_pk_add_f32 v[208:209], v[208:209], v[80:81]
	v_pk_add_f32 v[210:211], v[210:211], v[82:83]
	v_add_u32_e32 v60, 6, v51
	v_min_u32_e32 v60, 64, v60
	v_lshl_add_u32 v60, v60, 10, v3
	ds_read_b128 v[68:71], v60
	ds_read_b128 v[72:75], v60 offset:16
	v_add_u32_e32 v60, 7, v51
	v_min_u32_e32 v60, 64, v60
	v_lshl_add_u32 v60, v60, 10, v3
	ds_read_b128 v[76:79], v60
	ds_read_b128 v[80:83], v60 offset:16
	s_waitcnt lgkmcnt(8)
	v_pk_add_f32 v[204:205], v[204:205], v[84:85]
	v_pk_add_f32 v[206:207], v[206:207], v[86:87]
	v_pk_add_f32 v[208:209], v[208:209], v[88:89]
	v_pk_add_f32 v[210:211], v[210:211], v[90:91]
	v_pk_add_f32 v[204:205], v[204:205], v[92:93]
	v_pk_add_f32 v[206:207], v[206:207], v[94:95]
	v_pk_add_f32 v[208:209], v[208:209], v[96:97]
	v_pk_add_f32 v[210:211], v[210:211], v[98:99]
	s_waitcnt lgkmcnt(4)
	v_pk_add_f32 v[204:205], v[204:205], v[100:101]
	v_pk_add_f32 v[206:207], v[206:207], v[102:103]
	v_pk_add_f32 v[208:209], v[208:209], v[104:105]
	v_pk_add_f32 v[210:211], v[210:211], v[106:107]
	v_pk_add_f32 v[204:205], v[204:205], v[108:109]
	v_pk_add_f32 v[206:207], v[206:207], v[110:111]
	v_pk_add_f32 v[208:209], v[208:209], v[112:113]
	v_pk_add_f32 v[210:211], v[210:211], v[114:115]
	s_waitcnt lgkmcnt(0)
	v_pk_add_f32 v[204:205], v[204:205], v[68:69]
	v_pk_add_f32 v[206:207], v[206:207], v[70:71]
	v_pk_add_f32 v[208:209], v[208:209], v[72:73]
	v_pk_add_f32 v[210:211], v[210:211], v[74:75]
	v_pk_add_f32 v[204:205], v[204:205], v[76:77]
	v_pk_add_f32 v[206:207], v[206:207], v[78:79]
	v_pk_add_f32 v[208:209], v[208:209], v[80:81]
	v_pk_add_f32 v[210:211], v[210:211], v[82:83]
	v_lshlrev_b32_e32 v40, 16, v24
	v_and_b32_e32 v41, 0xffff0000, v24
	v_lshlrev_b32_e32 v42, 16, v25
	v_and_b32_e32 v43, 0xffff0000, v25
	v_lshlrev_b32_e32 v44, 16, v26
	v_and_b32_e32 v45, 0xffff0000, v26
	v_lshlrev_b32_e32 v46, 16, v27
	v_and_b32_e32 v47, 0xffff0000, v27
	v_pk_fma_f32 v[40:41], v[200:201], v[204:205], v[40:41] op_sel_hi:[0,1,1] neg_lo:[0,0,1] neg_hi:[0,0,1]
	v_pk_fma_f32 v[42:43], v[200:201], v[206:207], v[42:43] op_sel_hi:[0,1,1] neg_lo:[0,0,1] neg_hi:[0,0,1]
	v_pk_fma_f32 v[44:45], v[200:201], v[208:209], v[44:45] op_sel_hi:[0,1,1] neg_lo:[0,0,1] neg_hi:[0,0,1]
	v_pk_fma_f32 v[46:47], v[200:201], v[210:211], v[46:47] op_sel_hi:[0,1,1] neg_lo:[0,0,1] neg_hi:[0,0,1]
	v_cvt_pk_bf16_f32 v218, v40, v41
	v_cvt_pk_bf16_f32 v219, v42, v43
	v_cvt_pk_bf16_f32 v220, v44, v45
	v_cvt_pk_bf16_f32 v221, v46, v47
	global_store_dwordx4 v14, v[218:221], s[24:25]
	v_add_u32_e32 v51, 44, v50
	v_add_u32_e32 v60, 0, v51
	v_min_u32_e32 v60, 64, v60
	v_lshl_add_u32 v60, v60, 10, v3
	ds_read_b128 v[204:207], v60
	ds_read_b128 v[208:211], v60 offset:16
	v_add_u32_e32 v60, 1, v51
	v_min_u32_e32 v60, 64, v60
	v_lshl_add_u32 v60, v60, 10, v3
	ds_read_b128 v[76:79], v60
	ds_read_b128 v[80:83], v60 offset:16
	v_add_u32_e32 v60, 2, v51
	v_min_u32_e32 v60, 64, v60
	v_lshl_add_u32 v60, v60, 10, v3
	ds_read_b128 v[84:87], v60
	ds_read_b128 v[88:91], v60 offset:16
	v_add_u32_e32 v60, 3, v51
	v_min_u32_e32 v60, 64, v60
	v_lshl_add_u32 v60, v60, 10, v3
	ds_read_b128 v[92:95], v60
	ds_read_b128 v[96:99], v60 offset:16
	v_add_u32_e32 v60, 4, v51
	v_min_u32_e32 v60, 64, v60
	v_lshl_add_u32 v60, v60, 10, v3
	ds_read_b128 v[100:103], v60
	ds_read_b128 v[104:107], v60 offset:16
	v_add_u32_e32 v60, 5, v51
	v_min_u32_e32 v60, 64, v60
	v_lshl_add_u32 v60, v60, 10, v3
	ds_read_b128 v[108:111], v60
	ds_read_b128 v[112:115], v60 offset:16
	s_waitcnt lgkmcnt(8)
; #define LAS __attribute__((address_space(3)))
; __device__ __forceinline__ unsigned pk2(float lo, float hi) { return f2bf(lo) | (f2bf(hi) << 16); }
; template <int HALFW>
; __device__ __forceinline__ void pool_item(const bf16* P, bf16* DP, LAS float* tmp, int tid, int b, int r, int g) {
;     const int rlo = r - HALFW < 0 ? 0 : r - HALFW, rhi = r + HALFW > 32 ? 32 : r + HALFW;
;     const float rinv = 1.f / (float)(rhi - rlo);
; #pragma unroll 1
;     for (int q = 0; q < 4; ++q) { const int p = tid + 512 * q, c = p >> 5, ch0 = (p & 31) * 8; float acc[8]; v4u x[2 * HALFW];
; #pragma unroll
;         for (int u = 0; u < 2 * HALFW; ++u) { const int rr = (rlo + u < rhi) ? rlo + u : rlo; x[u] = *(const v4u*)(P + ((size_t)(b * 2048 + rr * 64 + c)) * 1024 + g * 256 + ch0); }
;     ...
;     for (int q = 0; q < 4; ++q) { const int p = tid + 512 * q, c = p >> 5, ch0 = (p & 31) * 8;
;         const int clo = c - HALFW < 0 ? 0 : c - HALFW, chi = c + HALFW > 64 ? 64 : c + HALFW; const float cinv = 1.f / (float)(chi - clo);
;         const size_t o = ((size_t)(b * 2048 + r * 64 + c)) * 1024 + g * 256 + ch0;
;         const v4u x = *(const v4u*)(P + o);
;         f32x4 a0 = (f32x4){0.f, 0.f, 0.f, 0.f}, a1 = a0;
; #pragma unroll
;         for (int u = 0; u < 2 * HALFW; ++u) { const int cc = (clo + u < chi) ? clo + u : clo; const float m = (clo + u < chi) ? 1.f : 0.f;
;             a0 += *(const LAS f32x4*)(tmp + cc * 256 + ch0) * m; a1 += *(const LAS f32x4*)(tmp + cc * 256 + ch0 + 4) * m; }
;         v4u d; d.x = pk2(a0[0] * cinv - bflo(x.x), a0[1] * cinv - bfhi(x.x)); d.y = pk2(a0[2] * cinv - bflo(x.y), a0[3] * cinv - bfhi(x.y));
;         d.z = pk2(a1[0] * cinv - bflo(x.z), a1[1] * cinv - bfhi(x.z)); d.w = pk2(a1[2] * cinv - bflo(x.w), a1[3] * cinv - bfhi(x.w));
;         *(v4u*)(DP + o) = d; }
;     __syncthreads();
	v_pk_add_f32 v[204:205], v[204:205], v[76:77]
	v_pk_add_f32 v[206:207], v[206:207], v[78:79]
	v_pk_add_f32 v[208:209], v[208:209], v[80:81]
	v_pk_add_f32 v[210:211], v[210:211], v[82:83]
	v_add_u32_e32 v60, 6, v51
	v_min_u32_e32 v60, 64, v60
	v_lshl_add_u32 v60, v60, 10, v3
	ds_read_b128 v[68:71], v60
	ds_read_b128 v[72:75], v60 offset:16
	v_add_u32_e32 v60, 7, v51
	v_min_u32_e32 v60, 64, v60
	v_lshl_add_u32 v60, v60, 10, v3
	ds_read_b128 v[76:79], v60
	ds_read_b128 v[80:83], v60 offset:16
	s_waitcnt lgkmcnt(8)
	v_pk_add_f32 v[204:205], v[204:205], v[84:85]
	v_pk_add_f32 v[206:207], v[206:207], v[86:87]
	v_pk_add_f32 v[208:209], v[208:209], v[88:89]
	v_pk_add_f32 v[210:211], v[210:211], v[90:91]
	v_pk_add_f32 v[204:205], v[204:205], v[92:93]
	v_pk_add_f32 v[206:207], v[206:207], v[94:95]
	v_pk_add_f32 v[208:209], v[208:209], v[96:97]
	v_pk_add_f32 v[210:211], v[210:211], v[98:99]
	s_waitcnt lgkmcnt(4)
	v_pk_add_f32 v[204:205], v[204:205], v[100:101]
	v_pk_add_f32 v[206:207], v[206:207], v[102:103]
	v_pk_add_f32 v[208:209], v[208:209], v[104:105]
	v_pk_add_f32 v[210:211], v[210:211], v[106:107]
	v_pk_add_f32 v[204:205], v[204:205], v[108:109]
	v_pk_add_f32 v[206:207], v[206:207], v[110:111]
	v_pk_add_f32 v[208:209], v[208:209], v[112:113]
	v_pk_add_f32 v[210:211], v[210:211], v[114:115]
	s_waitcnt lgkmcnt(0)
	v_pk_add_f32 v[204:205], v[204:205], v[68:69]
	v_pk_add_f32 v[206:207], v[206:207], v[70:71]
	v_pk_add_f32 v[208:209], v[208:209], v[72:73]
	v_pk_add_f32 v[210:211], v[210:211], v[74:75]
	v_pk_add_f32 v[204:205], v[204:205], v[76:77]
	v_pk_add_f32 v[206:207], v[206:207], v[78:79]
	v_pk_add_f32 v[208:209], v[208:209], v[80:81]
	v_pk_add_f32 v[210:211], v[210:211], v[82:83]
	v_lshlrev_b32_e32 v40, 16, v28
	v_and_b32_e32 v41, 0xffff0000, v28
	v_lshlrev_b32_e32 v42, 16, v29
	v_and_b32_e32 v43, 0xffff0000, v29
	v_lshlrev_b32_e32 v44, 16, v30
	v_and_b32_e32 v45, 0xffff0000, v30
	v_lshlrev_b32_e32 v46, 16, v31
	v_and_b32_e32 v47, 0xffff0000, v31
	v_pk_fma_f32 v[40:41], v[202:203], v[204:205], v[40:41] op_sel_hi:[0,1,1] neg_lo:[0,0,1] neg_hi:[0,0,1]
	v_pk_fma_f32 v[42:43], v[202:203], v[206:207], v[42:43] op_sel_hi:[0,1,1] neg_lo:[0,0,1] neg_hi:[0,0,1]
	v_pk_fma_f32 v[44:45], v[202:203], v[208:209], v[44:45] op_sel_hi:[0,1,1] neg_lo:[0,0,1] neg_hi:[0,0,1]
	v_pk_fma_f32 v[46:47], v[202:203], v[210:211], v[46:47] op_sel_hi:[0,1,1] neg_lo:[0,0,1] neg_hi:[0,0,1]
	v_cvt_pk_bf16_f32 v222, v40, v41
	v_cvt_pk_bf16_f32 v223, v42, v43
	v_cvt_pk_bf16_f32 v224, v44, v45
	v_cvt_pk_bf16_f32 v225, v46, v47
	global_store_dwordx4 v15, v[222:225], s[24:25]
	s_barrier
	s_branch .LBB0_678
.Lpool_h8:
	s_sub_i32 s27, s37, 8
	s_max_i32 s27, s27, 0
	s_add_i32 s28, s37, 8
	s_min_i32 s28, s28, 32
	s_sub_i32 s26, s28, s27
	s_lshl_b32 s29, s38, 11
	s_lshl_b32 s3, s27, 6
	s_add_i32 s2, s29, s3
	s_lshl_b32 s3, s2, 11
	s_add_u32 s4, s44, s3
	s_addc_u32 s5, s45, 0
	s_lshl_b32 s3, s37, 6
	s_add_i32 s3, s29, s3
	s_lshl_b32 s3, s3, 11
	s_add_u32 s6, s44, s3
	s_addc_u32 s7, s45, 0
	s_add_u32 s24, s46, s3
	s_addc_u32 s25, s47, 0
	s_add_u32 s4, s4, 1536
	s_addc_u32 s5, s5, 0
	s_add_u32 s6, s6, 1536
	s_addc_u32 s7, s7, 0
	s_add_u32 s24, s24, 1536
	s_addc_u32 s25, s25, 0
	s_cmp_gt_u32 s26, 0
	s_cselect_b32 s8, 0x0, 0
	s_cmp_gt_u32 s26, 1
	s_cselect_b32 s9, 0x20000, 0
	s_cmp_gt_u32 s26, 2
	s_cselect_b32 s10, 0x40000, 0
	s_cmp_gt_u32 s26, 3
	s_cselect_b32 s11, 0x60000, 0
	s_cmp_gt_u32 s26, 4
	s_cselect_b32 s12, 0x80000, 0
	s_cmp_gt_u32 s26, 5
	s_cselect_b32 s13, 0xa0000, 0
	s_cmp_gt_u32 s26, 6
	s_cselect_b32 s14, 0xc0000, 0
	s_cmp_gt_u32 s26, 7
	s_cselect_b32 s15, 0xe0000, 0
	s_cmp_gt_u32 s26, 8
	s_cselect_b32 s16, 0x100000, 0
	s_cmp_gt_u32 s26, 9
	s_cselect_b32 s17, 0x120000, 0
	s_cmp_gt_u32 s26, 10
	s_cselect_b32 s18, 0x140000, 0
	s_cmp_gt_u32 s26, 11
	s_cselect_b32 s19, 0x160000, 0
	s_cmp_gt_u32 s26, 12
	s_cselect_b32 s20, 0x180000, 0
	s_cmp_gt_u32 s26, 13
	s_cselect_b32 s21, 0x1a0000, 0
	s_cmp_gt_u32 s26, 14
	s_cselect_b32 s22, 0x1c0000, 0
	s_cmp_gt_u32 s26, 15
	s_cselect_b32 s23, 0x1e0000, 0
	v_lshrrev_b32_e32 v50, 5, v66
	v_lshlrev_b32_e32 v12, 11, v50
	v_lshl_or_b32 v12, v2, 1, v12
	v_add_u32_e32 v13, 0x8000, v12
	v_add_u32_e32 v14, 0x10000, v12
	v_add_u32_e32 v15, 0x18000, v12
	v_lshl_add_u32 v49, v50, 10, v3
	v_add_u32_e32 v51, s8, v12
	global_load_dwordx4 v[68:71], v51, s[4:5]
	v_add_u32_e32 v51, s9, v12
	global_load_dwordx4 v[72:75], v51, s[4:5]
	v_add_u32_e32 v51, s10, v12
	global_load_dwordx4 v[76:79], v51, s[4:5]
	v_add_u32_e32 v51, s11, v12
	global_load_dwordx4 v[80:83], v51, s[4:5]
	v_add_u32_e32 v51, s12, v12
	global_load_dwordx4 v[84:87], v51, s[4:5]
	v_add_u32_e32 v51, s13, v12
	global_load_dwordx4 v[88:91], v51, s[4:5]
	v_add_u32_e32 v51, s14, v12
	global_load_dwordx4 v[92:95], v51, s[4:5]
	v_add_u32_e32 v51, s15, v12
	global_load_dwordx4 v[96:99], v51, s[4:5]
	v_add_u32_e32 v51, s16, v12
	global_load_dwordx4 v[100:103], v51, s[4:5]
	v_add_u32_e32 v51, s17, v12
	global_load_dwordx4 v[104:107], v51, s[4:5]
	v_add_u32_e32 v51, s18, v12
	global_load_dwordx4 v[108:111], v51, s[4:5]
	v_add_u32_e32 v51, s19, v12
	global_load_dwordx4 v[112:115], v51, s[4:5]
	v_add_u32_e32 v51, s20, v12
	global_load_dwordx4 v[116:119], v51, s[4:5]
	v_add_u32_e32 v51, s21, v12
	global_load_dwordx4 v[120:123], v51, s[4:5]
	v_add_u32_e32 v51, s22, v12
	global_load_dwordx4 v[124:127], v51, s[4:5]
	v_add_u32_e32 v51, s23, v12
	global_load_dwordx4 v[128:131], v51, s[4:5]
	v_add_u32_e32 v51, s8, v13
	global_load_dwordx4 v[132:135], v51, s[4:5]
	v_add_u32_e32 v51, s9, v13
	global_load_dwordx4 v[136:139], v51, s[4:5]
	v_add_u32_e32 v51, s10, v13
	global_load_dwordx4 v[140:143], v51, s[4:5]
; #define LAS __attribute__((address_space(3)))
; template <int HALFW>
; __device__ __forceinline__ void pool_item(const bf16* P, bf16* DP, LAS float* tmp, int tid, int b, int r, int g) {
;     ...
;     for (int q = 0; q < 4; ++q) { const int p = tid + 512 * q, c = p >> 5, ch0 = (p & 31) * 8; float acc[8]; v4u x[2 * HALFW];
; #pragma unroll
;         for (int u = 0; u < 2 * HALFW; ++u) { const int rr = (rlo + u < rhi) ? rlo + u : rlo; x[u] = *(const v4u*)(P + ((size_t)(b * 2048 + rr * 64 + c)) * 1024 + g * 256 + ch0); }
; #pragma unroll
;         for (int j = 0; j < 8; ++j) acc[j] = 0.f;
; #pragma unroll
;         for (int u = 0; u < 2 * HALFW; ++u) { const float m = (rlo + u < rhi) ? 1.f : 0.f;
;             acc[0] += m * bflo(x[u].x); acc[1] += m * bfhi(x[u].x); acc[2] += m * bflo(x[u].y); acc[3] += m * bfhi(x[u].y); acc[4] += m * bflo(x[u].z); acc[5] += m * bfhi(x[u].z); acc[6] += m * bflo(x[u].w); acc[7] += m * bfhi(x[u].w); }
;         *(LAS f32x4*)(tmp + c * 256 + ch0) = (f32x4){acc[0] * rinv, acc[1] * rinv, acc[2] * rinv, acc[3] * rinv};
;         *(LAS f32x4*)(tmp + c * 256 + ch0 + 4) = (f32x4){acc[4] * rinv, acc[5] * rinv, acc[6] * rinv, acc[7] * rinv}; }
	v_add_u32_e32 v51, s11, v13
	global_load_dwordx4 v[144:147], v51, s[4:5]
	v_add_u32_e32 v51, s12, v13
	global_load_dwordx4 v[148:151], v51, s[4:5]
	v_add_u32_e32 v51, s13, v13
	global_load_dwordx4 v[152:155], v51, s[4:5]
	v_add_u32_e32 v51, s14, v13
	global_load_dwordx4 v[156:159], v51, s[4:5]
	v_add_u32_e32 v51, s15, v13
	global_load_dwordx4 v[160:163], v51, s[4:5]
	v_add_u32_e32 v51, s16, v13
	global_load_dwordx4 v[164:167], v51, s[4:5]
	v_add_u32_e32 v51, s17, v13
	global_load_dwordx4 v[168:171], v51, s[4:5]
	v_add_u32_e32 v51, s18, v13
	global_load_dwordx4 v[172:175], v51, s[4:5]
	v_add_u32_e32 v51, s19, v13
	global_load_dwordx4 v[176:179], v51, s[4:5]
	v_add_u32_e32 v51, s20, v13
	global_load_dwordx4 v[180:183], v51, s[4:5]
	v_add_u32_e32 v51, s21, v13
	global_load_dwordx4 v[184:187], v51, s[4:5]
	v_add_u32_e32 v51, s22, v13
	global_load_dwordx4 v[188:191], v51, s[4:5]
	v_add_u32_e32 v51, s23, v13
	global_load_dwordx4 v[192:195], v51, s[4:5]
	global_load_dwordx4 v[16:19], v12, s[6:7]
	global_load_dwordx4 v[20:23], v13, s[6:7]
	global_load_dwordx4 v[24:27], v14, s[6:7]
	global_load_dwordx4 v[28:31], v15, s[6:7]
	v_cvt_f32_u32_e32 v212, s26
	v_div_scale_f32 v213, s[30:31], v212, v212, 1.0
	v_div_scale_f32 v215, vcc, 1.0, v212, 1.0
	v_rcp_f32_e32 v214, v213
	s_nop 1
	v_fma_f32 v216, -v213, v214, 1.0
	v_fmac_f32_e32 v214, v216, v214
	v_mul_f32_e32 v216, v215, v214
	v_fma_f32 v217, -v213, v216, v215
	v_fmac_f32_e32 v216, v217, v214
	v_fma_f32 v213, -v213, v216, v215
	s_nop 1
	v_div_fmas_f32 v213, v213, v214, v216
	v_div_fixup_f32 v48, v213, v212, 1.0
	s_waitcnt vmcnt(20)
	v_lshlrev_b32_e32 v32, 16, v68
	v_and_b32_e32 v33, 0xffff0000, v68
	v_lshlrev_b32_e32 v34, 16, v69
	v_and_b32_e32 v35, 0xffff0000, v69
	v_lshlrev_b32_e32 v36, 16, v70
	v_and_b32_e32 v37, 0xffff0000, v70
	v_lshlrev_b32_e32 v38, 16, v71
	v_and_b32_e32 v39, 0xffff0000, v71
	v_lshlrev_b32_e32 v40, 16, v72
	v_and_b32_e32 v41, 0xffff0000, v72
	v_lshlrev_b32_e32 v42, 16, v73
	v_and_b32_e32 v43, 0xffff0000, v73
	v_lshlrev_b32_e32 v44, 16, v74
	v_and_b32_e32 v45, 0xffff0000, v74
	v_lshlrev_b32_e32 v46, 16, v75
	v_and_b32_e32 v47, 0xffff0000, v75
	v_pk_add_f32 v[32:33], v[32:33], v[40:41]
	v_pk_add_f32 v[34:35], v[34:35], v[42:43]
	v_pk_add_f32 v[36:37], v[36:37], v[44:45]
	v_pk_add_f32 v[38:39], v[38:39], v[46:47]
	v_lshlrev_b32_e32 v40, 16, v76
	v_and_b32_e32 v41, 0xffff0000, v76
	v_lshlrev_b32_e32 v42, 16, v77
	v_and_b32_e32 v43, 0xffff0000, v77
	v_lshlrev_b32_e32 v44, 16, v78
	v_and_b32_e32 v45, 0xffff0000, v78
	v_lshlrev_b32_e32 v46, 16, v79
	v_and_b32_e32 v47, 0xffff0000, v79
	v_pk_add_f32 v[32:33], v[32:33], v[40:41]
	v_pk_add_f32 v[34:35], v[34:35], v[42:43]
	v_pk_add_f32 v[36:37], v[36:37], v[44:45]
	v_pk_add_f32 v[38:39], v[38:39], v[46:47]
	v_lshlrev_b32_e32 v40, 16, v80
	v_and_b32_e32 v41, 0xffff0000, v80
	v_lshlrev_b32_e32 v42, 16, v81
	v_and_b32_e32 v43, 0xffff0000, v81
	v_lshlrev_b32_e32 v44, 16, v82
	v_and_b32_e32 v45, 0xffff0000, v82
	v_lshlrev_b32_e32 v46, 16, v83
	v_and_b32_e32 v47, 0xffff0000, v83
	v_pk_add_f32 v[32:33], v[32:33], v[40:41]
	v_pk_add_f32 v[34:35], v[34:35], v[42:43]
	v_pk_add_f32 v[36:37], v[36:37], v[44:45]
	v_pk_add_f32 v[38:39], v[38:39], v[46:47]
	v_lshlrev_b32_e32 v40, 16, v84
	v_and_b32_e32 v41, 0xffff0000, v84
	v_lshlrev_b32_e32 v42, 16, v85
	v_and_b32_e32 v43, 0xffff0000, v85
	v_lshlrev_b32_e32 v44, 16, v86
	v_and_b32_e32 v45, 0xffff0000, v86
	v_lshlrev_b32_e32 v46, 16, v87
	v_and_b32_e32 v47, 0xffff0000, v87
	v_pk_add_f32 v[32:33], v[32:33], v[40:41]
	v_pk_add_f32 v[34:35], v[34:35], v[42:43]
	v_pk_add_f32 v[36:37], v[36:37], v[44:45]
	v_pk_add_f32 v[38:39], v[38:39], v[46:47]
	v_lshlrev_b32_e32 v40, 16, v88
	v_and_b32_e32 v41, 0xffff0000, v88
	v_lshlrev_b32_e32 v42, 16, v89
	v_and_b32_e32 v43, 0xffff0000, v89
	v_lshlrev_b32_e32 v44, 16, v90
	v_and_b32_e32 v45, 0xffff0000, v90
	v_lshlrev_b32_e32 v46, 16, v91
	v_and_b32_e32 v47, 0xffff0000, v91
	v_pk_add_f32 v[32:33], v[32:33], v[40:41]
	v_pk_add_f32 v[34:35], v[34:35], v[42:43]
	v_pk_add_f32 v[36:37], v[36:37], v[44:45]
	v_pk_add_f32 v[38:39], v[38:39], v[46:47]
	v_lshlrev_b32_e32 v40, 16, v92
	v_and_b32_e32 v41, 0xffff0000, v92
	v_lshlrev_b32_e32 v42, 16, v93
	v_and_b32_e32 v43, 0xffff0000, v93
	v_lshlrev_b32_e32 v44, 16, v94
	v_and_b32_e32 v45, 0xffff0000, v94
	v_lshlrev_b32_e32 v46, 16, v95
	v_and_b32_e32 v47, 0xffff0000, v95
	v_pk_add_f32 v[32:33], v[32:33], v[40:41]
	v_pk_add_f32 v[34:35], v[34:35], v[42:43]
	v_pk_add_f32 v[36:37], v[36:37], v[44:45]
	v_pk_add_f32 v[38:39], v[38:39], v[46:47]
	v_lshlrev_b32_e32 v40, 16, v96
	v_and_b32_e32 v41, 0xffff0000, v96
	v_lshlrev_b32_e32 v42, 16, v97
	v_and_b32_e32 v43, 0xffff0000, v97
	v_lshlrev_b32_e32 v44, 16, v98
	v_and_b32_e32 v45, 0xffff0000, v98
	v_lshlrev_b32_e32 v46, 16, v99
	v_and_b32_e32 v47, 0xffff0000, v99
	v_pk_add_f32 v[32:33], v[32:33], v[40:41]
	v_pk_add_f32 v[34:35], v[34:35], v[42:43]
	v_pk_add_f32 v[36:37], v[36:37], v[44:45]
	v_pk_add_f32 v[38:39], v[38:39], v[46:47]
	s_cmp_gt_u32 s26, 8
	s_cbranch_scc0 .Lpool_h8_q0
	v_lshlrev_b32_e32 v40, 16, v100
	v_and_b32_e32 v41, 0xffff0000, v100
	v_lshlrev_b32_e32 v42, 16, v101
	v_and_b32_e32 v43, 0xffff0000, v101
	v_lshlrev_b32_e32 v44, 16, v102
	v_and_b32_e32 v45, 0xffff0000, v102
	v_lshlrev_b32_e32 v46, 16, v103
	v_and_b32_e32 v47, 0xffff0000, v103
	v_pk_add_f32 v[32:33], v[32:33], v[40:41]
	v_pk_add_f32 v[34:35], v[34:35], v[42:43]
	v_pk_add_f32 v[36:37], v[36:37], v[44:45]
	v_pk_add_f32 v[38:39], v[38:39], v[46:47]
	s_cmp_gt_u32 s26, 9
	s_cbranch_scc0 .Lpool_h8_q0
; #define LAS __attribute__((address_space(3)))
; template <int HALFW>
; __device__ __forceinline__ void pool_item(const bf16* P, bf16* DP, LAS float* tmp, int tid, int b, int r, int g) {
;     ...
;     for (int q = 0; q < 4; ++q) { const int p = tid + 512 * q, c = p >> 5, ch0 = (p & 31) * 8; float acc[8]; v4u x[2 * HALFW];
; #pragma unroll
;         for (int u = 0; u < 2 * HALFW; ++u) { const int rr = (rlo + u < rhi) ? rlo + u : rlo; x[u] = *(const v4u*)(P + ((size_t)(b * 2048 + rr * 64 + c)) * 1024 + g * 256 + ch0); }
; #pragma unroll
;         for (int j = 0; j < 8; ++j) acc[j] = 0.f;
; #pragma unroll
;         for (int u = 0; u < 2 * HALFW; ++u) { const float m = (rlo + u < rhi) ? 1.f : 0.f;
;             acc[0] += m * bflo(x[u].x); acc[1] += m * bfhi(x[u].x); acc[2] += m * bflo(x[u].y); acc[3] += m * bfhi(x[u].y); acc[4] += m * bflo(x[u].z); acc[5] += m * bfhi(x[u].z); acc[6] += m * bflo(x[u].w); acc[7] += m * bfhi(x[u].w); }
;         *(LAS f32x4*)(tmp + c * 256 + ch0) = (f32x4){acc[0] * rinv, acc[1] * rinv, acc[2] * rinv, acc[3] * rinv};
;         *(LAS f32x4*)(tmp + c * 256 + ch0 + 4) = (f32x4){acc[4] * rinv, acc[5] * rinv, acc[6] * rinv, acc[7] * rinv}; }
	v_lshlrev_b32_e32 v40, 16, v104
	v_and_b32_e32 v41, 0xffff0000, v104
	v_lshlrev_b32_e32 v42, 16, v105
	v_and_b32_e32 v43, 0xffff0000, v105
	v_lshlrev_b32_e32 v44, 16, v106
	v_and_b32_e32 v45, 0xffff0000, v106
	v_lshlrev_b32_e32 v46, 16, v107
	v_and_b32_e32 v47, 0xffff0000, v107
	v_pk_add_f32 v[32:33], v[32:33], v[40:41]
	v_pk_add_f32 v[34:35], v[34:35], v[42:43]
	v_pk_add_f32 v[36:37], v[36:37], v[44:45]
	v_pk_add_f32 v[38:39], v[38:39], v[46:47]
	s_cmp_gt_u32 s26, 10
	s_cbranch_scc0 .Lpool_h8_q0
	v_lshlrev_b32_e32 v40, 16, v108
	v_and_b32_e32 v41, 0xffff0000, v108
	v_lshlrev_b32_e32 v42, 16, v109
	v_and_b32_e32 v43, 0xffff0000, v109
	v_lshlrev_b32_e32 v44, 16, v110
	v_and_b32_e32 v45, 0xffff0000, v110
	v_lshlrev_b32_e32 v46, 16, v111
	v_and_b32_e32 v47, 0xffff0000, v111
	v_pk_add_f32 v[32:33], v[32:33], v[40:41]
	v_pk_add_f32 v[34:35], v[34:35], v[42:43]
	v_pk_add_f32 v[36:37], v[36:37], v[44:45]
	v_pk_add_f32 v[38:39], v[38:39], v[46:47]
	s_cmp_gt_u32 s26, 11
	s_cbranch_scc0 .Lpool_h8_q0
	v_lshlrev_b32_e32 v40, 16, v112
	v_and_b32_e32 v41, 0xffff0000, v112
	v_lshlrev_b32_e32 v42, 16, v113
	v_and_b32_e32 v43, 0xffff0000, v113
	v_lshlrev_b32_e32 v44, 16, v114
	v_and_b32_e32 v45, 0xffff0000, v114
	v_lshlrev_b32_e32 v46, 16, v115
	v_and_b32_e32 v47, 0xffff0000, v115
	v_pk_add_f32 v[32:33], v[32:33], v[40:41]
	v_pk_add_f32 v[34:35], v[34:35], v[42:43]
	v_pk_add_f32 v[36:37], v[36:37], v[44:45]
	v_pk_add_f32 v[38:39], v[38:39], v[46:47]
	s_cmp_gt_u32 s26, 12
	s_cbranch_scc0 .Lpool_h8_q0
	v_lshlrev_b32_e32 v40, 16, v116
	v_and_b32_e32 v41, 0xffff0000, v116
	v_lshlrev_b32_e32 v42, 16, v117
	v_and_b32_e32 v43, 0xffff0000, v117
	v_lshlrev_b32_e32 v44, 16, v118
	v_and_b32_e32 v45, 0xffff0000, v118
	v_lshlrev_b32_e32 v46, 16, v119
	v_and_b32_e32 v47, 0xffff0000, v119
	v_pk_add_f32 v[32:33], v[32:33], v[40:41]
	v_pk_add_f32 v[34:35], v[34:35], v[42:43]
	v_pk_add_f32 v[36:37], v[36:37], v[44:45]
	v_pk_add_f32 v[38:39], v[38:39], v[46:47]
	s_cmp_gt_u32 s26, 13
	s_cbranch_scc0 .Lpool_h8_q0
	v_lshlrev_b32_e32 v40, 16, v120
	v_and_b32_e32 v41, 0xffff0000, v120
	v_lshlrev_b32_e32 v42, 16, v121
	v_and_b32_e32 v43, 0xffff0000, v121
	v_lshlrev_b32_e32 v44, 16, v122
	v_and_b32_e32 v45, 0xffff0000, v122
	v_lshlrev_b32_e32 v46, 16, v123
	v_and_b32_e32 v47, 0xffff0000, v123
	v_pk_add_f32 v[32:33], v[32:33], v[40:41]
	v_pk_add_f32 v[34:35], v[34:35], v[42:43]
	v_pk_add_f32 v[36:37], v[36:37], v[44:45]
	v_pk_add_f32 v[38:39], v[38:39], v[46:47]
	s_cmp_gt_u32 s26, 14
	s_cbranch_scc0 .Lpool_h8_q0
	v_lshlrev_b32_e32 v40, 16, v124
	v_and_b32_e32 v41, 0xffff0000, v124
	v_lshlrev_b32_e32 v42, 16, v125
	v_and_b32_e32 v43, 0xffff0000, v125
	v_lshlrev_b32_e32 v44, 16, v126
	v_and_b32_e32 v45, 0xffff0000, v126
	v_lshlrev_b32_e32 v46, 16, v127
	v_and_b32_e32 v47, 0xffff0000, v127
	v_pk_add_f32 v[32:33], v[32:33], v[40:41]
	v_pk_add_f32 v[34:35], v[34:35], v[42:43]
	v_pk_add_f32 v[36:37], v[36:37], v[44:45]
	v_pk_add_f32 v[38:39], v[38:39], v[46:47]
	s_cmp_gt_u32 s26, 15
	s_cbranch_scc0 .Lpool_h8_q0
	v_lshlrev_b32_e32 v40, 16, v128
	v_and_b32_e32 v41, 0xffff0000, v128
	v_lshlrev_b32_e32 v42, 16, v129
	v_and_b32_e32 v43, 0xffff0000, v129
	v_lshlrev_b32_e32 v44, 16, v130
	v_and_b32_e32 v45, 0xffff0000, v130
	v_lshlrev_b32_e32 v46, 16, v131
	v_and_b32_e32 v47, 0xffff0000, v131
	v_pk_add_f32 v[32:33], v[32:33], v[40:41]
	v_pk_add_f32 v[34:35], v[34:35], v[42:43]
	v_pk_add_f32 v[36:37], v[36:37], v[44:45]
	v_pk_add_f32 v[38:39], v[38:39], v[46:47]
.Lpool_h8_q0:
	v_pk_mul_f32 v[32:33], v[32:33], v[48:49] op_sel_hi:[1,0]
	v_pk_mul_f32 v[34:35], v[34:35], v[48:49] op_sel_hi:[1,0]
	v_pk_mul_f32 v[36:37], v[36:37], v[48:49] op_sel_hi:[1,0]
	v_pk_mul_f32 v[38:39], v[38:39], v[48:49] op_sel_hi:[1,0]
	ds_write_b128 v49, v[32:35] offset:0
	ds_write_b128 v49, v[36:39] offset:16
	v_add_u32_e32 v51, s8, v14
	global_load_dwordx4 v[68:71], v51, s[4:5]
	v_add_u32_e32 v51, s9, v14
	global_load_dwordx4 v[72:75], v51, s[4:5]
	v_add_u32_e32 v51, s10, v14
	global_load_dwordx4 v[76:79], v51, s[4:5]
	v_add_u32_e32 v51, s11, v14
	global_load_dwordx4 v[80:83], v51, s[4:5]
	v_add_u32_e32 v51, s12, v14
	global_load_dwordx4 v[84:87], v51, s[4:5]
	v_add_u32_e32 v51, s13, v14
	global_load_dwordx4 v[88:91], v51, s[4:5]
	v_add_u32_e32 v51, s14, v14
	global_load_dwordx4 v[92:95], v51, s[4:5]
	v_add_u32_e32 v51, s15, v14
	global_load_dwordx4 v[96:99], v51, s[4:5]
	v_add_u32_e32 v51, s16, v14
	global_load_dwordx4 v[100:103], v51, s[4:5]
	v_add_u32_e32 v51, s17, v14
	global_load_dwordx4 v[104:107], v51, s[4:5]
	v_add_u32_e32 v51, s18, v14
	global_load_dwordx4 v[108:111], v51, s[4:5]
	v_add_u32_e32 v51, s19, v14
	global_load_dwordx4 v[112:115], v51, s[4:5]
	v_add_u32_e32 v51, s20, v14
	global_load_dwordx4 v[116:119], v51, s[4:5]
	v_add_u32_e32 v51, s21, v14
	global_load_dwordx4 v[120:123], v51, s[4:5]
	v_add_u32_e32 v51, s22, v14
	global_load_dwordx4 v[124:127], v51, s[4:5]
	v_add_u32_e32 v51, s23, v14
	global_load_dwordx4 v[128:131], v51, s[4:5]
	s_waitcnt vmcnt(20)
; #define LAS __attribute__((address_space(3)))
; template <int HALFW>
; __device__ __forceinline__ void pool_item(const bf16* P, bf16* DP, LAS float* tmp, int tid, int b, int r, int g) {
;     ...
;     for (int q = 0; q < 4; ++q) { const int p = tid + 512 * q, c = p >> 5, ch0 = (p & 31) * 8; float acc[8]; v4u x[2 * HALFW];
; #pragma unroll
;         for (int u = 0; u < 2 * HALFW; ++u) { const int rr = (rlo + u < rhi) ? rlo + u : rlo; x[u] = *(const v4u*)(P + ((size_t)(b * 2048 + rr * 64 + c)) * 1024 + g * 256 + ch0); }
; #pragma unroll
;         for (int j = 0; j < 8; ++j) acc[j] = 0.f;
; #pragma unroll
;         for (int u = 0; u < 2 * HALFW; ++u) { const float m = (rlo + u < rhi) ? 1.f : 0.f;
;             acc[0] += m * bflo(x[u].x); acc[1] += m * bfhi(x[u].x); acc[2] += m * bflo(x[u].y); acc[3] += m * bfhi(x[u].y); acc[4] += m * bflo(x[u].z); acc[5] += m * bfhi(x[u].z); acc[6] += m * bflo(x[u].w); acc[7] += m * bfhi(x[u].w); }
;         *(LAS f32x4*)(tmp + c * 256 + ch0) = (f32x4){acc[0] * rinv, acc[1] * rinv, acc[2] * rinv, acc[3] * rinv};
;         *(LAS f32x4*)(tmp + c * 256 + ch0 + 4) = (f32x4){acc[4] * rinv, acc[5] * rinv, acc[6] * rinv, acc[7] * rinv}; }
	v_lshlrev_b32_e32 v52, 16, v132
	v_and_b32_e32 v53, 0xffff0000, v132
	v_lshlrev_b32_e32 v54, 16, v133
	v_and_b32_e32 v55, 0xffff0000, v133
	v_lshlrev_b32_e32 v56, 16, v134
	v_and_b32_e32 v57, 0xffff0000, v134
	v_lshlrev_b32_e32 v58, 16, v135
	v_and_b32_e32 v59, 0xffff0000, v135
	v_lshlrev_b32_e32 v40, 16, v136
	v_and_b32_e32 v41, 0xffff0000, v136
	v_lshlrev_b32_e32 v42, 16, v137
	v_and_b32_e32 v43, 0xffff0000, v137
	v_lshlrev_b32_e32 v44, 16, v138
	v_and_b32_e32 v45, 0xffff0000, v138
	v_lshlrev_b32_e32 v46, 16, v139
	v_and_b32_e32 v47, 0xffff0000, v139
	v_pk_add_f32 v[52:53], v[52:53], v[40:41]
	v_pk_add_f32 v[54:55], v[54:55], v[42:43]
	v_pk_add_f32 v[56:57], v[56:57], v[44:45]
	v_pk_add_f32 v[58:59], v[58:59], v[46:47]
	v_lshlrev_b32_e32 v40, 16, v140
	v_and_b32_e32 v41, 0xffff0000, v140
	v_lshlrev_b32_e32 v42, 16, v141
	v_and_b32_e32 v43, 0xffff0000, v141
	v_lshlrev_b32_e32 v44, 16, v142
	v_and_b32_e32 v45, 0xffff0000, v142
	v_lshlrev_b32_e32 v46, 16, v143
	v_and_b32_e32 v47, 0xffff0000, v143
	v_pk_add_f32 v[52:53], v[52:53], v[40:41]
	v_pk_add_f32 v[54:55], v[54:55], v[42:43]
	v_pk_add_f32 v[56:57], v[56:57], v[44:45]
	v_pk_add_f32 v[58:59], v[58:59], v[46:47]
	v_lshlrev_b32_e32 v40, 16, v144
	v_and_b32_e32 v41, 0xffff0000, v144
	v_lshlrev_b32_e32 v42, 16, v145
	v_and_b32_e32 v43, 0xffff0000, v145
	v_lshlrev_b32_e32 v44, 16, v146
	v_and_b32_e32 v45, 0xffff0000, v146
	v_lshlrev_b32_e32 v46, 16, v147
	v_and_b32_e32 v47, 0xffff0000, v147
	v_pk_add_f32 v[52:53], v[52:53], v[40:41]
	v_pk_add_f32 v[54:55], v[54:55], v[42:43]
	v_pk_add_f32 v[56:57], v[56:57], v[44:45]
	v_pk_add_f32 v[58:59], v[58:59], v[46:47]
	v_lshlrev_b32_e32 v40, 16, v148
	v_and_b32_e32 v41, 0xffff0000, v148
	v_lshlrev_b32_e32 v42, 16, v149
	v_and_b32_e32 v43, 0xffff0000, v149
	v_lshlrev_b32_e32 v44, 16, v150
	v_and_b32_e32 v45, 0xffff0000, v150
	v_lshlrev_b32_e32 v46, 16, v151
	v_and_b32_e32 v47, 0xffff0000, v151
	v_pk_add_f32 v[52:53], v[52:53], v[40:41]
	v_pk_add_f32 v[54:55], v[54:55], v[42:43]
	v_pk_add_f32 v[56:57], v[56:57], v[44:45]
	v_pk_add_f32 v[58:59], v[58:59], v[46:47]
	v_lshlrev_b32_e32 v40, 16, v152
	v_and_b32_e32 v41, 0xffff0000, v152
	v_lshlrev_b32_e32 v42, 16, v153
	v_and_b32_e32 v43, 0xffff0000, v153
	v_lshlrev_b32_e32 v44, 16, v154
	v_and_b32_e32 v45, 0xffff0000, v154
	v_lshlrev_b32_e32 v46, 16, v155
	v_and_b32_e32 v47, 0xffff0000, v155
	v_pk_add_f32 v[52:53], v[52:53], v[40:41]
	v_pk_add_f32 v[54:55], v[54:55], v[42:43]
	v_pk_add_f32 v[56:57], v[56:57], v[44:45]
	v_pk_add_f32 v[58:59], v[58:59], v[46:47]
	v_lshlrev_b32_e32 v40, 16, v156
	v_and_b32_e32 v41, 0xffff0000, v156
	v_lshlrev_b32_e32 v42, 16, v157
	v_and_b32_e32 v43, 0xffff0000, v157
	v_lshlrev_b32_e32 v44, 16, v158
	v_and_b32_e32 v45, 0xffff0000, v158
	v_lshlrev_b32_e32 v46, 16, v159
	v_and_b32_e32 v47, 0xffff0000, v159
	v_pk_add_f32 v[52:53], v[52:53], v[40:41]
	v_pk_add_f32 v[54:55], v[54:55], v[42:43]
	v_pk_add_f32 v[56:57], v[56:57], v[44:45]
	v_pk_add_f32 v[58:59], v[58:59], v[46:47]
	v_lshlrev_b32_e32 v40, 16, v160
	v_and_b32_e32 v41, 0xffff0000, v160
	v_lshlrev_b32_e32 v42, 16, v161
	v_and_b32_e32 v43, 0xffff0000, v161
	v_lshlrev_b32_e32 v44, 16, v162
	v_and_b32_e32 v45, 0xffff0000, v162
	v_lshlrev_b32_e32 v46, 16, v163
	v_and_b32_e32 v47, 0xffff0000, v163
	v_pk_add_f32 v[52:53], v[52:53], v[40:41]
	v_pk_add_f32 v[54:55], v[54:55], v[42:43]
	v_pk_add_f32 v[56:57], v[56:57], v[44:45]
	v_pk_add_f32 v[58:59], v[58:59], v[46:47]
	s_cmp_gt_u32 s26, 8
	s_cbranch_scc0 .Lpool_h8_q1
	v_lshlrev_b32_e32 v40, 16, v164
	v_and_b32_e32 v41, 0xffff0000, v164
	v_lshlrev_b32_e32 v42, 16, v165
	v_and_b32_e32 v43, 0xffff0000, v165
	v_lshlrev_b32_e32 v44, 16, v166
	v_and_b32_e32 v45, 0xffff0000, v166
	v_lshlrev_b32_e32 v46, 16, v167
	v_and_b32_e32 v47, 0xffff0000, v167
	v_pk_add_f32 v[52:53], v[52:53], v[40:41]
	v_pk_add_f32 v[54:55], v[54:55], v[42:43]
	v_pk_add_f32 v[56:57], v[56:57], v[44:45]
	v_pk_add_f32 v[58:59], v[58:59], v[46:47]
	s_cmp_gt_u32 s26, 9
	s_cbranch_scc0 .Lpool_h8_q1
	v_lshlrev_b32_e32 v40, 16, v168
	v_and_b32_e32 v41, 0xffff0000, v168
	v_lshlrev_b32_e32 v42, 16, v169
	v_and_b32_e32 v43, 0xffff0000, v169
	v_lshlrev_b32_e32 v44, 16, v170
	v_and_b32_e32 v45, 0xffff0000, v170
	v_lshlrev_b32_e32 v46, 16, v171
	v_and_b32_e32 v47, 0xffff0000, v171
	v_pk_add_f32 v[52:53], v[52:53], v[40:41]
	v_pk_add_f32 v[54:55], v[54:55], v[42:43]
	v_pk_add_f32 v[56:57], v[56:57], v[44:45]
	v_pk_add_f32 v[58:59], v[58:59], v[46:47]
	s_cmp_gt_u32 s26, 10
	s_cbranch_scc0 .Lpool_h8_q1
	v_lshlrev_b32_e32 v40, 16, v172
	v_and_b32_e32 v41, 0xffff0000, v172
	v_lshlrev_b32_e32 v42, 16, v173
	v_and_b32_e32 v43, 0xffff0000, v173
	v_lshlrev_b32_e32 v44, 16, v174
	v_and_b32_e32 v45, 0xffff0000, v174
	v_lshlrev_b32_e32 v46, 16, v175
	v_and_b32_e32 v47, 0xffff0000, v175
	v_pk_add_f32 v[52:53], v[52:53], v[40:41]
	v_pk_add_f32 v[54:55], v[54:55], v[42:43]
	v_pk_add_f32 v[56:57], v[56:57], v[44:45]
	v_pk_add_f32 v[58:59], v[58:59], v[46:47]
	s_cmp_gt_u32 s26, 11
	s_cbranch_scc0 .Lpool_h8_q1
	v_lshlrev_b32_e32 v40, 16, v176
	v_and_b32_e32 v41, 0xffff0000, v176
	v_lshlrev_b32_e32 v42, 16, v177
	v_and_b32_e32 v43, 0xffff0000, v177
	v_lshlrev_b32_e32 v44, 16, v178
	v_and_b32_e32 v45, 0xffff0000, v178
	v_lshlrev_b32_e32 v46, 16, v179
	v_and_b32_e32 v47, 0xffff0000, v179
	v_pk_add_f32 v[52:53], v[52:53], v[40:41]
	v_pk_add_f32 v[54:55], v[54:55], v[42:43]
	v_pk_add_f32 v[56:57], v[56:57], v[44:45]
	v_pk_add_f32 v[58:59], v[58:59], v[46:47]
	s_cmp_gt_u32 s26, 12
	s_cbranch_scc0 .Lpool_h8_q1
; #define LAS __attribute__((address_space(3)))
; template <int HALFW>
; __device__ __forceinline__ void pool_item(const bf16* P, bf16* DP, LAS float* tmp, int tid, int b, int r, int g) {
;     ...
;     for (int q = 0; q < 4; ++q) { const int p = tid + 512 * q, c = p >> 5, ch0 = (p & 31) * 8; float acc[8]; v4u x[2 * HALFW];
; #pragma unroll
;         for (int u = 0; u < 2 * HALFW; ++u) { const int rr = (rlo + u < rhi) ? rlo + u : rlo; x[u] = *(const v4u*)(P + ((size_t)(b * 2048 + rr * 64 + c)) * 1024 + g * 256 + ch0); }
; #pragma unroll
;         for (int j = 0; j < 8; ++j) acc[j] = 0.f;
; #pragma unroll
;         for (int u = 0; u < 2 * HALFW; ++u) { const float m = (rlo + u < rhi) ? 1.f : 0.f;
;             acc[0] += m * bflo(x[u].x); acc[1] += m * bfhi(x[u].x); acc[2] += m * bflo(x[u].y); acc[3] += m * bfhi(x[u].y); acc[4] += m * bflo(x[u].z); acc[5] += m * bfhi(x[u].z); acc[6] += m * bflo(x[u].w); acc[7] += m * bfhi(x[u].w); }
;         *(LAS f32x4*)(tmp + c * 256 + ch0) = (f32x4){acc[0] * rinv, acc[1] * rinv, acc[2] * rinv, acc[3] * rinv};
;         *(LAS f32x4*)(tmp + c * 256 + ch0 + 4) = (f32x4){acc[4] * rinv, acc[5] * rinv, acc[6] * rinv, acc[7] * rinv}; }
	v_lshlrev_b32_e32 v40, 16, v180
	v_and_b32_e32 v41, 0xffff0000, v180
	v_lshlrev_b32_e32 v42, 16, v181
	v_and_b32_e32 v43, 0xffff0000, v181
	v_lshlrev_b32_e32 v44, 16, v182
	v_and_b32_e32 v45, 0xffff0000, v182
	v_lshlrev_b32_e32 v46, 16, v183
	v_and_b32_e32 v47, 0xffff0000, v183
	v_pk_add_f32 v[52:53], v[52:53], v[40:41]
	v_pk_add_f32 v[54:55], v[54:55], v[42:43]
	v_pk_add_f32 v[56:57], v[56:57], v[44:45]
	v_pk_add_f32 v[58:59], v[58:59], v[46:47]
	s_cmp_gt_u32 s26, 13
	s_cbranch_scc0 .Lpool_h8_q1
	v_lshlrev_b32_e32 v40, 16, v184
	v_and_b32_e32 v41, 0xffff0000, v184
	v_lshlrev_b32_e32 v42, 16, v185
	v_and_b32_e32 v43, 0xffff0000, v185
	v_lshlrev_b32_e32 v44, 16, v186
	v_and_b32_e32 v45, 0xffff0000, v186
	v_lshlrev_b32_e32 v46, 16, v187
	v_and_b32_e32 v47, 0xffff0000, v187
	v_pk_add_f32 v[52:53], v[52:53], v[40:41]
	v_pk_add_f32 v[54:55], v[54:55], v[42:43]
	v_pk_add_f32 v[56:57], v[56:57], v[44:45]
	v_pk_add_f32 v[58:59], v[58:59], v[46:47]
	s_cmp_gt_u32 s26, 14
	s_cbranch_scc0 .Lpool_h8_q1
	v_lshlrev_b32_e32 v40, 16, v188
	v_and_b32_e32 v41, 0xffff0000, v188
	v_lshlrev_b32_e32 v42, 16, v189
	v_and_b32_e32 v43, 0xffff0000, v189
	v_lshlrev_b32_e32 v44, 16, v190
	v_and_b32_e32 v45, 0xffff0000, v190
	v_lshlrev_b32_e32 v46, 16, v191
	v_and_b32_e32 v47, 0xffff0000, v191
	v_pk_add_f32 v[52:53], v[52:53], v[40:41]
	v_pk_add_f32 v[54:55], v[54:55], v[42:43]
	v_pk_add_f32 v[56:57], v[56:57], v[44:45]
	v_pk_add_f32 v[58:59], v[58:59], v[46:47]
	s_cmp_gt_u32 s26, 15
	s_cbranch_scc0 .Lpool_h8_q1
	v_lshlrev_b32_e32 v40, 16, v192
	v_and_b32_e32 v41, 0xffff0000, v192
	v_lshlrev_b32_e32 v42, 16, v193
	v_and_b32_e32 v43, 0xffff0000, v193
	v_lshlrev_b32_e32 v44, 16, v194
	v_and_b32_e32 v45, 0xffff0000, v194
	v_lshlrev_b32_e32 v46, 16, v195
	v_and_b32_e32 v47, 0xffff0000, v195
	v_pk_add_f32 v[52:53], v[52:53], v[40:41]
	v_pk_add_f32 v[54:55], v[54:55], v[42:43]
	v_pk_add_f32 v[56:57], v[56:57], v[44:45]
	v_pk_add_f32 v[58:59], v[58:59], v[46:47]
.Lpool_h8_q1:
	v_pk_mul_f32 v[52:53], v[52:53], v[48:49] op_sel_hi:[1,0]
	v_pk_mul_f32 v[54:55], v[54:55], v[48:49] op_sel_hi:[1,0]
	v_pk_mul_f32 v[56:57], v[56:57], v[48:49] op_sel_hi:[1,0]
	v_pk_mul_f32 v[58:59], v[58:59], v[48:49] op_sel_hi:[1,0]
	ds_write_b128 v49, v[52:55] offset:16384
	ds_write_b128 v49, v[56:59] offset:16400
	v_add_u32_e32 v51, s8, v15
	global_load_dwordx4 v[132:135], v51, s[4:5]
	v_add_u32_e32 v51, s9, v15
	global_load_dwordx4 v[136:139], v51, s[4:5]
	v_add_u32_e32 v51, s10, v15
	global_load_dwordx4 v[140:143], v51, s[4:5]
	v_add_u32_e32 v51, s11, v15
	global_load_dwordx4 v[144:147], v51, s[4:5]
	v_add_u32_e32 v51, s12, v15
	global_load_dwordx4 v[148:151], v51, s[4:5]
	v_add_u32_e32 v51, s13, v15
	global_load_dwordx4 v[152:155], v51, s[4:5]
	v_add_u32_e32 v51, s14, v15
	global_load_dwordx4 v[156:159], v51, s[4:5]
	v_add_u32_e32 v51, s15, v15
	global_load_dwordx4 v[160:163], v51, s[4:5]
	v_add_u32_e32 v51, s16, v15
	global_load_dwordx4 v[164:167], v51, s[4:5]
	v_add_u32_e32 v51, s17, v15
	global_load_dwordx4 v[168:171], v51, s[4:5]
	v_add_u32_e32 v51, s18, v15
	global_load_dwordx4 v[172:175], v51, s[4:5]
	v_add_u32_e32 v51, s19, v15
	global_load_dwordx4 v[176:179], v51, s[4:5]
	v_add_u32_e32 v51, s20, v15
	global_load_dwordx4 v[180:183], v51, s[4:5]
	v_add_u32_e32 v51, s21, v15
	global_load_dwordx4 v[184:187], v51, s[4:5]
	v_add_u32_e32 v51, s22, v15
	global_load_dwordx4 v[188:191], v51, s[4:5]
	v_add_u32_e32 v51, s23, v15
	global_load_dwordx4 v[192:195], v51, s[4:5]
	s_waitcnt vmcnt(16)
	v_lshlrev_b32_e32 v32, 16, v68
	v_and_b32_e32 v33, 0xffff0000, v68
	v_lshlrev_b32_e32 v34, 16, v69
	v_and_b32_e32 v35, 0xffff0000, v69
	v_lshlrev_b32_e32 v36, 16, v70
	v_and_b32_e32 v37, 0xffff0000, v70
	v_lshlrev_b32_e32 v38, 16, v71
	v_and_b32_e32 v39, 0xffff0000, v71
	v_lshlrev_b32_e32 v40, 16, v72
	v_and_b32_e32 v41, 0xffff0000, v72
	v_lshlrev_b32_e32 v42, 16, v73
	v_and_b32_e32 v43, 0xffff0000, v73
	v_lshlrev_b32_e32 v44, 16, v74
	v_and_b32_e32 v45, 0xffff0000, v74
	v_lshlrev_b32_e32 v46, 16, v75
	v_and_b32_e32 v47, 0xffff0000, v75
	v_pk_add_f32 v[32:33], v[32:33], v[40:41]
	v_pk_add_f32 v[34:35], v[34:35], v[42:43]
	v_pk_add_f32 v[36:37], v[36:37], v[44:45]
	v_pk_add_f32 v[38:39], v[38:39], v[46:47]
	v_lshlrev_b32_e32 v40, 16, v76
	v_and_b32_e32 v41, 0xffff0000, v76
	v_lshlrev_b32_e32 v42, 16, v77
	v_and_b32_e32 v43, 0xffff0000, v77
	v_lshlrev_b32_e32 v44, 16, v78
	v_and_b32_e32 v45, 0xffff0000, v78
	v_lshlrev_b32_e32 v46, 16, v79
	v_and_b32_e32 v47, 0xffff0000, v79
	v_pk_add_f32 v[32:33], v[32:33], v[40:41]
	v_pk_add_f32 v[34:35], v[34:35], v[42:43]
	v_pk_add_f32 v[36:37], v[36:37], v[44:45]
	v_pk_add_f32 v[38:39], v[38:39], v[46:47]
	v_lshlrev_b32_e32 v40, 16, v80
	v_and_b32_e32 v41, 0xffff0000, v80
	v_lshlrev_b32_e32 v42, 16, v81
	v_and_b32_e32 v43, 0xffff0000, v81
	v_lshlrev_b32_e32 v44, 16, v82
	v_and_b32_e32 v45, 0xffff0000, v82
	v_lshlrev_b32_e32 v46, 16, v83
	v_and_b32_e32 v47, 0xffff0000, v83
	v_pk_add_f32 v[32:33], v[32:33], v[40:41]
	v_pk_add_f32 v[34:35], v[34:35], v[42:43]
	v_pk_add_f32 v[36:37], v[36:37], v[44:45]
	v_pk_add_f32 v[38:39], v[38:39], v[46:47]
	v_lshlrev_b32_e32 v40, 16, v84
	v_and_b32_e32 v41, 0xffff0000, v84
	v_lshlrev_b32_e32 v42, 16, v85
	v_and_b32_e32 v43, 0xffff0000, v85
	v_lshlrev_b32_e32 v44, 16, v86
	v_and_b32_e32 v45, 0xffff0000, v86
	v_lshlrev_b32_e32 v46, 16, v87
	v_and_b32_e32 v47, 0xffff0000, v87
	v_pk_add_f32 v[32:33], v[32:33], v[40:41]
	v_pk_add_f32 v[34:35], v[34:35], v[42:43]
	v_pk_add_f32 v[36:37], v[36:37], v[44:45]
	v_pk_add_f32 v[38:39], v[38:39], v[46:47]
	v_lshlrev_b32_e32 v40, 16, v88
	v_and_b32_e32 v41, 0xffff0000, v88
	v_lshlrev_b32_e32 v42, 16, v89
	v_and_b32_e32 v43, 0xffff0000, v89
	v_lshlrev_b32_e32 v44, 16, v90
	v_and_b32_e32 v45, 0xffff0000, v90
	v_lshlrev_b32_e32 v46, 16, v91
	v_and_b32_e32 v47, 0xffff0000, v91
	v_pk_add_f32 v[32:33], v[32:33], v[40:41]
	v_pk_add_f32 v[34:35], v[34:35], v[42:43]
	v_pk_add_f32 v[36:37], v[36:37], v[44:45]
	v_pk_add_f32 v[38:39], v[38:39], v[46:47]
	v_lshlrev_b32_e32 v40, 16, v92
	v_and_b32_e32 v41, 0xffff0000, v92
	v_lshlrev_b32_e32 v42, 16, v93
	v_and_b32_e32 v43, 0xffff0000, v93
	v_lshlrev_b32_e32 v44, 16, v94
	v_and_b32_e32 v45, 0xffff0000, v94
	v_lshlrev_b32_e32 v46, 16, v95
	v_and_b32_e32 v47, 0xffff0000, v95
	v_pk_add_f32 v[32:33], v[32:33], v[40:41]
	v_pk_add_f32 v[34:35], v[34:35], v[42:43]
	v_pk_add_f32 v[36:37], v[36:37], v[44:45]
	v_pk_add_f32 v[38:39], v[38:39], v[46:47]
	v_lshlrev_b32_e32 v40, 16, v96
	v_and_b32_e32 v41, 0xffff0000, v96
	v_lshlrev_b32_e32 v42, 16, v97
	v_and_b32_e32 v43, 0xffff0000, v97
	v_lshlrev_b32_e32 v44, 16, v98
	v_and_b32_e32 v45, 0xffff0000, v98
	v_lshlrev_b32_e32 v46, 16, v99
	v_and_b32_e32 v47, 0xffff0000, v99
	v_pk_add_f32 v[32:33], v[32:33], v[40:41]
	v_pk_add_f32 v[34:35], v[34:35], v[42:43]
	v_pk_add_f32 v[36:37], v[36:37], v[44:45]
	v_pk_add_f32 v[38:39], v[38:39], v[46:47]
	s_cmp_gt_u32 s26, 8
	s_cbranch_scc0 .Lpool_h8_q2
; #define LAS __attribute__((address_space(3)))
; template <int HALFW>
; __device__ __forceinline__ void pool_item(const bf16* P, bf16* DP, LAS float* tmp, int tid, int b, int r, int g) {
;     ...
;     for (int q = 0; q < 4; ++q) { const int p = tid + 512 * q, c = p >> 5, ch0 = (p & 31) * 8; float acc[8]; v4u x[2 * HALFW];
; #pragma unroll
;         for (int u = 0; u < 2 * HALFW; ++u) { const int rr = (rlo + u < rhi) ? rlo + u : rlo; x[u] = *(const v4u*)(P + ((size_t)(b * 2048 + rr * 64 + c)) * 1024 + g * 256 + ch0); }
; #pragma unroll
;         for (int j = 0; j < 8; ++j) acc[j] = 0.f;
; #pragma unroll
;         for (int u = 0; u < 2 * HALFW; ++u) { const float m = (rlo + u < rhi) ? 1.f : 0.f;
;             acc[0] += m * bflo(x[u].x); acc[1] += m * bfhi(x[u].x); acc[2] += m * bflo(x[u].y); acc[3] += m * bfhi(x[u].y); acc[4] += m * bflo(x[u].z); acc[5] += m * bfhi(x[u].z); acc[6] += m * bflo(x[u].w); acc[7] += m * bfhi(x[u].w); }
;         *(LAS f32x4*)(tmp + c * 256 + ch0) = (f32x4){acc[0] * rinv, acc[1] * rinv, acc[2] * rinv, acc[3] * rinv};
;         *(LAS f32x4*)(tmp + c * 256 + ch0 + 4) = (f32x4){acc[4] * rinv, acc[5] * rinv, acc[6] * rinv, acc[7] * rinv}; }
	v_lshlrev_b32_e32 v40, 16, v100
	v_and_b32_e32 v41, 0xffff0000, v100
	v_lshlrev_b32_e32 v42, 16, v101
	v_and_b32_e32 v43, 0xffff0000, v101
	v_lshlrev_b32_e32 v44, 16, v102
	v_and_b32_e32 v45, 0xffff0000, v102
	v_lshlrev_b32_e32 v46, 16, v103
	v_and_b32_e32 v47, 0xffff0000, v103
	v_pk_add_f32 v[32:33], v[32:33], v[40:41]
	v_pk_add_f32 v[34:35], v[34:35], v[42:43]
	v_pk_add_f32 v[36:37], v[36:37], v[44:45]
	v_pk_add_f32 v[38:39], v[38:39], v[46:47]
	s_cmp_gt_u32 s26, 9
	s_cbranch_scc0 .Lpool_h8_q2
	v_lshlrev_b32_e32 v40, 16, v104
	v_and_b32_e32 v41, 0xffff0000, v104
	v_lshlrev_b32_e32 v42, 16, v105
	v_and_b32_e32 v43, 0xffff0000, v105
	v_lshlrev_b32_e32 v44, 16, v106
	v_and_b32_e32 v45, 0xffff0000, v106
	v_lshlrev_b32_e32 v46, 16, v107
	v_and_b32_e32 v47, 0xffff0000, v107
	v_pk_add_f32 v[32:33], v[32:33], v[40:41]
	v_pk_add_f32 v[34:35], v[34:35], v[42:43]
	v_pk_add_f32 v[36:37], v[36:37], v[44:45]
	v_pk_add_f32 v[38:39], v[38:39], v[46:47]
	s_cmp_gt_u32 s26, 10
	s_cbranch_scc0 .Lpool_h8_q2
	v_lshlrev_b32_e32 v40, 16, v108
	v_and_b32_e32 v41, 0xffff0000, v108
	v_lshlrev_b32_e32 v42, 16, v109
	v_and_b32_e32 v43, 0xffff0000, v109
	v_lshlrev_b32_e32 v44, 16, v110
	v_and_b32_e32 v45, 0xffff0000, v110
	v_lshlrev_b32_e32 v46, 16, v111
	v_and_b32_e32 v47, 0xffff0000, v111
	v_pk_add_f32 v[32:33], v[32:33], v[40:41]
	v_pk_add_f32 v[34:35], v[34:35], v[42:43]
	v_pk_add_f32 v[36:37], v[36:37], v[44:45]
	v_pk_add_f32 v[38:39], v[38:39], v[46:47]
	s_cmp_gt_u32 s26, 11
	s_cbranch_scc0 .Lpool_h8_q2
	v_lshlrev_b32_e32 v40, 16, v112
	v_and_b32_e32 v41, 0xffff0000, v112
	v_lshlrev_b32_e32 v42, 16, v113
	v_and_b32_e32 v43, 0xffff0000, v113
	v_lshlrev_b32_e32 v44, 16, v114
	v_and_b32_e32 v45, 0xffff0000, v114
	v_lshlrev_b32_e32 v46, 16, v115
	v_and_b32_e32 v47, 0xffff0000, v115
	v_pk_add_f32 v[32:33], v[32:33], v[40:41]
	v_pk_add_f32 v[34:35], v[34:35], v[42:43]
	v_pk_add_f32 v[36:37], v[36:37], v[44:45]
	v_pk_add_f32 v[38:39], v[38:39], v[46:47]
	s_cmp_gt_u32 s26, 12
	s_cbranch_scc0 .Lpool_h8_q2
	v_lshlrev_b32_e32 v40, 16, v116
	v_and_b32_e32 v41, 0xffff0000, v116
	v_lshlrev_b32_e32 v42, 16, v117
	v_and_b32_e32 v43, 0xffff0000, v117
	v_lshlrev_b32_e32 v44, 16, v118
	v_and_b32_e32 v45, 0xffff0000, v118
	v_lshlrev_b32_e32 v46, 16, v119
	v_and_b32_e32 v47, 0xffff0000, v119
	v_pk_add_f32 v[32:33], v[32:33], v[40:41]
	v_pk_add_f32 v[34:35], v[34:35], v[42:43]
	v_pk_add_f32 v[36:37], v[36:37], v[44:45]
	v_pk_add_f32 v[38:39], v[38:39], v[46:47]
	s_cmp_gt_u32 s26, 13
	s_cbranch_scc0 .Lpool_h8_q2
	v_lshlrev_b32_e32 v40, 16, v120
	v_and_b32_e32 v41, 0xffff0000, v120
	v_lshlrev_b32_e32 v42, 16, v121
	v_and_b32_e32 v43, 0xffff0000, v121
	v_lshlrev_b32_e32 v44, 16, v122
	v_and_b32_e32 v45, 0xffff0000, v122
	v_lshlrev_b32_e32 v46, 16, v123
	v_and_b32_e32 v47, 0xffff0000, v123
	v_pk_add_f32 v[32:33], v[32:33], v[40:41]
	v_pk_add_f32 v[34:35], v[34:35], v[42:43]
	v_pk_add_f32 v[36:37], v[36:37], v[44:45]
	v_pk_add_f32 v[38:39], v[38:39], v[46:47]
	s_cmp_gt_u32 s26, 14
	s_cbranch_scc0 .Lpool_h8_q2
	v_lshlrev_b32_e32 v40, 16, v124
	v_and_b32_e32 v41, 0xffff0000, v124
	v_lshlrev_b32_e32 v42, 16, v125
	v_and_b32_e32 v43, 0xffff0000, v125
	v_lshlrev_b32_e32 v44, 16, v126
	v_and_b32_e32 v45, 0xffff0000, v126
	v_lshlrev_b32_e32 v46, 16, v127
	v_and_b32_e32 v47, 0xffff0000, v127
	v_pk_add_f32 v[32:33], v[32:33], v[40:41]
	v_pk_add_f32 v[34:35], v[34:35], v[42:43]
	v_pk_add_f32 v[36:37], v[36:37], v[44:45]
	v_pk_add_f32 v[38:39], v[38:39], v[46:47]
	s_cmp_gt_u32 s26, 15
	s_cbranch_scc0 .Lpool_h8_q2
	v_lshlrev_b32_e32 v40, 16, v128
	v_and_b32_e32 v41, 0xffff0000, v128
	v_lshlrev_b32_e32 v42, 16, v129
	v_and_b32_e32 v43, 0xffff0000, v129
	v_lshlrev_b32_e32 v44, 16, v130
	v_and_b32_e32 v45, 0xffff0000, v130
	v_lshlrev_b32_e32 v46, 16, v131
	v_and_b32_e32 v47, 0xffff0000, v131
	v_pk_add_f32 v[32:33], v[32:33], v[40:41]
	v_pk_add_f32 v[34:35], v[34:35], v[42:43]
	v_pk_add_f32 v[36:37], v[36:37], v[44:45]
	v_pk_add_f32 v[38:39], v[38:39], v[46:47]
.Lpool_h8_q2:
	v_pk_mul_f32 v[32:33], v[32:33], v[48:49] op_sel_hi:[1,0]
	v_pk_mul_f32 v[34:35], v[34:35], v[48:49] op_sel_hi:[1,0]
	v_pk_mul_f32 v[36:37], v[36:37], v[48:49] op_sel_hi:[1,0]
	v_pk_mul_f32 v[38:39], v[38:39], v[48:49] op_sel_hi:[1,0]
	ds_write_b128 v49, v[32:35] offset:32768
	ds_write_b128 v49, v[36:39] offset:32784
	s_waitcnt vmcnt(0)
; #define LAS __attribute__((address_space(3)))
; template <int HALFW>
; __device__ __forceinline__ void pool_item(const bf16* P, bf16* DP, LAS float* tmp, int tid, int b, int r, int g) {
;     ...
;     for (int q = 0; q < 4; ++q) { const int p = tid + 512 * q, c = p >> 5, ch0 = (p & 31) * 8; float acc[8]; v4u x[2 * HALFW];
; #pragma unroll
;         for (int u = 0; u < 2 * HALFW; ++u) { const int rr = (rlo + u < rhi) ? rlo + u : rlo; x[u] = *(const v4u*)(P + ((size_t)(b * 2048 + rr * 64 + c)) * 1024 + g * 256 + ch0); }
; #pragma unroll
;         for (int j = 0; j < 8; ++j) acc[j] = 0.f;
; #pragma unroll
;         for (int u = 0; u < 2 * HALFW; ++u) { const float m = (rlo + u < rhi) ? 1.f : 0.f;
;             acc[0] += m * bflo(x[u].x); acc[1] += m * bfhi(x[u].x); acc[2] += m * bflo(x[u].y); acc[3] += m * bfhi(x[u].y); acc[4] += m * bflo(x[u].z); acc[5] += m * bfhi(x[u].z); acc[6] += m * bflo(x[u].w); acc[7] += m * bfhi(x[u].w); }
;         *(LAS f32x4*)(tmp + c * 256 + ch0) = (f32x4){acc[0] * rinv, acc[1] * rinv, acc[2] * rinv, acc[3] * rinv};
;         *(LAS f32x4*)(tmp + c * 256 + ch0 + 4) = (f32x4){acc[4] * rinv, acc[5] * rinv, acc[6] * rinv, acc[7] * rinv}; }
	v_lshlrev_b32_e32 v52, 16, v132
	v_and_b32_e32 v53, 0xffff0000, v132
	v_lshlrev_b32_e32 v54, 16, v133
	v_and_b32_e32 v55, 0xffff0000, v133
	v_lshlrev_b32_e32 v56, 16, v134
	v_and_b32_e32 v57, 0xffff0000, v134
	v_lshlrev_b32_e32 v58, 16, v135
	v_and_b32_e32 v59, 0xffff0000, v135
	v_lshlrev_b32_e32 v40, 16, v136
	v_and_b32_e32 v41, 0xffff0000, v136
	v_lshlrev_b32_e32 v42, 16, v137
	v_and_b32_e32 v43, 0xffff0000, v137
	v_lshlrev_b32_e32 v44, 16, v138
	v_and_b32_e32 v45, 0xffff0000, v138
	v_lshlrev_b32_e32 v46, 16, v139
	v_and_b32_e32 v47, 0xffff0000, v139
	v_pk_add_f32 v[52:53], v[52:53], v[40:41]
	v_pk_add_f32 v[54:55], v[54:55], v[42:43]
	v_pk_add_f32 v[56:57], v[56:57], v[44:45]
	v_pk_add_f32 v[58:59], v[58:59], v[46:47]
	v_lshlrev_b32_e32 v40, 16, v140
	v_and_b32_e32 v41, 0xffff0000, v140
	v_lshlrev_b32_e32 v42, 16, v141
	v_and_b32_e32 v43, 0xffff0000, v141
	v_lshlrev_b32_e32 v44, 16, v142
	v_and_b32_e32 v45, 0xffff0000, v142
	v_lshlrev_b32_e32 v46, 16, v143
	v_and_b32_e32 v47, 0xffff0000, v143
	v_pk_add_f32 v[52:53], v[52:53], v[40:41]
	v_pk_add_f32 v[54:55], v[54:55], v[42:43]
	v_pk_add_f32 v[56:57], v[56:57], v[44:45]
	v_pk_add_f32 v[58:59], v[58:59], v[46:47]
	v_lshlrev_b32_e32 v40, 16, v144
	v_and_b32_e32 v41, 0xffff0000, v144
	v_lshlrev_b32_e32 v42, 16, v145
	v_and_b32_e32 v43, 0xffff0000, v145
	v_lshlrev_b32_e32 v44, 16, v146
	v_and_b32_e32 v45, 0xffff0000, v146
	v_lshlrev_b32_e32 v46, 16, v147
	v_and_b32_e32 v47, 0xffff0000, v147
	v_pk_add_f32 v[52:53], v[52:53], v[40:41]
	v_pk_add_f32 v[54:55], v[54:55], v[42:43]
	v_pk_add_f32 v[56:57], v[56:57], v[44:45]
	v_pk_add_f32 v[58:59], v[58:59], v[46:47]
	v_lshlrev_b32_e32 v40, 16, v148
	v_and_b32_e32 v41, 0xffff0000, v148
	v_lshlrev_b32_e32 v42, 16, v149
	v_and_b32_e32 v43, 0xffff0000, v149
	v_lshlrev_b32_e32 v44, 16, v150
	v_and_b32_e32 v45, 0xffff0000, v150
	v_lshlrev_b32_e32 v46, 16, v151
	v_and_b32_e32 v47, 0xffff0000, v151
	v_pk_add_f32 v[52:53], v[52:53], v[40:41]
	v_pk_add_f32 v[54:55], v[54:55], v[42:43]
	v_pk_add_f32 v[56:57], v[56:57], v[44:45]
	v_pk_add_f32 v[58:59], v[58:59], v[46:47]
	v_lshlrev_b32_e32 v40, 16, v152
	v_and_b32_e32 v41, 0xffff0000, v152
	v_lshlrev_b32_e32 v42, 16, v153
	v_and_b32_e32 v43, 0xffff0000, v153
	v_lshlrev_b32_e32 v44, 16, v154
	v_and_b32_e32 v45, 0xffff0000, v154
	v_lshlrev_b32_e32 v46, 16, v155
	v_and_b32_e32 v47, 0xffff0000, v155
	v_pk_add_f32 v[52:53], v[52:53], v[40:41]
	v_pk_add_f32 v[54:55], v[54:55], v[42:43]
	v_pk_add_f32 v[56:57], v[56:57], v[44:45]
	v_pk_add_f32 v[58:59], v[58:59], v[46:47]
	v_lshlrev_b32_e32 v40, 16, v156
	v_and_b32_e32 v41, 0xffff0000, v156
	v_lshlrev_b32_e32 v42, 16, v157
	v_and_b32_e32 v43, 0xffff0000, v157
	v_lshlrev_b32_e32 v44, 16, v158
	v_and_b32_e32 v45, 0xffff0000, v158
	v_lshlrev_b32_e32 v46, 16, v159
	v_and_b32_e32 v47, 0xffff0000, v159
	v_pk_add_f32 v[52:53], v[52:53], v[40:41]
	v_pk_add_f32 v[54:55], v[54:55], v[42:43]
	v_pk_add_f32 v[56:57], v[56:57], v[44:45]
	v_pk_add_f32 v[58:59], v[58:59], v[46:47]
	v_lshlrev_b32_e32 v40, 16, v160
	v_and_b32_e32 v41, 0xffff0000, v160
	v_lshlrev_b32_e32 v42, 16, v161
	v_and_b32_e32 v43, 0xffff0000, v161
	v_lshlrev_b32_e32 v44, 16, v162
	v_and_b32_e32 v45, 0xffff0000, v162
	v_lshlrev_b32_e32 v46, 16, v163
	v_and_b32_e32 v47, 0xffff0000, v163
	v_pk_add_f32 v[52:53], v[52:53], v[40:41]
	v_pk_add_f32 v[54:55], v[54:55], v[42:43]
	v_pk_add_f32 v[56:57], v[56:57], v[44:45]
	v_pk_add_f32 v[58:59], v[58:59], v[46:47]
	s_cmp_gt_u32 s26, 8
	s_cbranch_scc0 .Lpool_h8_q3
	v_lshlrev_b32_e32 v40, 16, v164
	v_and_b32_e32 v41, 0xffff0000, v164
	v_lshlrev_b32_e32 v42, 16, v165
	v_and_b32_e32 v43, 0xffff0000, v165
	v_lshlrev_b32_e32 v44, 16, v166
	v_and_b32_e32 v45, 0xffff0000, v166
	v_lshlrev_b32_e32 v46, 16, v167
	v_and_b32_e32 v47, 0xffff0000, v167
	v_pk_add_f32 v[52:53], v[52:53], v[40:41]
	v_pk_add_f32 v[54:55], v[54:55], v[42:43]
	v_pk_add_f32 v[56:57], v[56:57], v[44:45]
	v_pk_add_f32 v[58:59], v[58:59], v[46:47]
	s_cmp_gt_u32 s26, 9
	s_cbranch_scc0 .Lpool_h8_q3
	v_lshlrev_b32_e32 v40, 16, v168
	v_and_b32_e32 v41, 0xffff0000, v168
	v_lshlrev_b32_e32 v42, 16, v169
	v_and_b32_e32 v43, 0xffff0000, v169
	v_lshlrev_b32_e32 v44, 16, v170
	v_and_b32_e32 v45, 0xffff0000, v170
	v_lshlrev_b32_e32 v46, 16, v171
	v_and_b32_e32 v47, 0xffff0000, v171
	v_pk_add_f32 v[52:53], v[52:53], v[40:41]
	v_pk_add_f32 v[54:55], v[54:55], v[42:43]
	v_pk_add_f32 v[56:57], v[56:57], v[44:45]
	v_pk_add_f32 v[58:59], v[58:59], v[46:47]
	s_cmp_gt_u32 s26, 10
	s_cbranch_scc0 .Lpool_h8_q3
	v_lshlrev_b32_e32 v40, 16, v172
	v_and_b32_e32 v41, 0xffff0000, v172
	v_lshlrev_b32_e32 v42, 16, v173
	v_and_b32_e32 v43, 0xffff0000, v173
	v_lshlrev_b32_e32 v44, 16, v174
	v_and_b32_e32 v45, 0xffff0000, v174
	v_lshlrev_b32_e32 v46, 16, v175
	v_and_b32_e32 v47, 0xffff0000, v175
	v_pk_add_f32 v[52:53], v[52:53], v[40:41]
	v_pk_add_f32 v[54:55], v[54:55], v[42:43]
	v_pk_add_f32 v[56:57], v[56:57], v[44:45]
	v_pk_add_f32 v[58:59], v[58:59], v[46:47]
	s_cmp_gt_u32 s26, 11
	s_cbranch_scc0 .Lpool_h8_q3
	v_lshlrev_b32_e32 v40, 16, v176
	v_and_b32_e32 v41, 0xffff0000, v176
	v_lshlrev_b32_e32 v42, 16, v177
	v_and_b32_e32 v43, 0xffff0000, v177
	v_lshlrev_b32_e32 v44, 16, v178
	v_and_b32_e32 v45, 0xffff0000, v178
	v_lshlrev_b32_e32 v46, 16, v179
	v_and_b32_e32 v47, 0xffff0000, v179
	v_pk_add_f32 v[52:53], v[52:53], v[40:41]
	v_pk_add_f32 v[54:55], v[54:55], v[42:43]
	v_pk_add_f32 v[56:57], v[56:57], v[44:45]
	v_pk_add_f32 v[58:59], v[58:59], v[46:47]
	s_cmp_gt_u32 s26, 12
	s_cbranch_scc0 .Lpool_h8_q3
; #define LAS __attribute__((address_space(3)))
; template <int HALFW>
; __device__ __forceinline__ void pool_item(const bf16* P, bf16* DP, LAS float* tmp, int tid, int b, int r, int g) {
;     ...
;         for (int u = 0; u < 2 * HALFW; ++u) { const float m = (rlo + u < rhi) ? 1.f : 0.f;
;             acc[0] += m * bflo(x[u].x); acc[1] += m * bfhi(x[u].x); acc[2] += m * bflo(x[u].y); acc[3] += m * bfhi(x[u].y); acc[4] += m * bflo(x[u].z); acc[5] += m * bfhi(x[u].z); acc[6] += m * bflo(x[u].w); acc[7] += m * bfhi(x[u].w); }
;         *(LAS f32x4*)(tmp + c * 256 + ch0) = (f32x4){acc[0] * rinv, acc[1] * rinv, acc[2] * rinv, acc[3] * rinv};
;         *(LAS f32x4*)(tmp + c * 256 + ch0 + 4) = (f32x4){acc[4] * rinv, acc[5] * rinv, acc[6] * rinv, acc[7] * rinv}; }
;     __syncthreads();
; #pragma unroll 1
;     for (int q = 0; q < 4; ++q) { const int p = tid + 512 * q, c = p >> 5, ch0 = (p & 31) * 8;
;         const int clo = c - HALFW < 0 ? 0 : c - HALFW, chi = c + HALFW > 64 ? 64 : c + HALFW; const float cinv = 1.f / (float)(chi - clo);
	v_lshlrev_b32_e32 v40, 16, v180
	v_and_b32_e32 v41, 0xffff0000, v180
	v_lshlrev_b32_e32 v42, 16, v181
	v_and_b32_e32 v43, 0xffff0000, v181
	v_lshlrev_b32_e32 v44, 16, v182
	v_and_b32_e32 v45, 0xffff0000, v182
	v_lshlrev_b32_e32 v46, 16, v183
	v_and_b32_e32 v47, 0xffff0000, v183
	v_pk_add_f32 v[52:53], v[52:53], v[40:41]
	v_pk_add_f32 v[54:55], v[54:55], v[42:43]
	v_pk_add_f32 v[56:57], v[56:57], v[44:45]
	v_pk_add_f32 v[58:59], v[58:59], v[46:47]
	s_cmp_gt_u32 s26, 13
	s_cbranch_scc0 .Lpool_h8_q3
	v_lshlrev_b32_e32 v40, 16, v184
	v_and_b32_e32 v41, 0xffff0000, v184
	v_lshlrev_b32_e32 v42, 16, v185
	v_and_b32_e32 v43, 0xffff0000, v185
	v_lshlrev_b32_e32 v44, 16, v186
	v_and_b32_e32 v45, 0xffff0000, v186
	v_lshlrev_b32_e32 v46, 16, v187
	v_and_b32_e32 v47, 0xffff0000, v187
	v_pk_add_f32 v[52:53], v[52:53], v[40:41]
	v_pk_add_f32 v[54:55], v[54:55], v[42:43]
	v_pk_add_f32 v[56:57], v[56:57], v[44:45]
	v_pk_add_f32 v[58:59], v[58:59], v[46:47]
	s_cmp_gt_u32 s26, 14
	s_cbranch_scc0 .Lpool_h8_q3
	v_lshlrev_b32_e32 v40, 16, v188
	v_and_b32_e32 v41, 0xffff0000, v188
	v_lshlrev_b32_e32 v42, 16, v189
	v_and_b32_e32 v43, 0xffff0000, v189
	v_lshlrev_b32_e32 v44, 16, v190
	v_and_b32_e32 v45, 0xffff0000, v190
	v_lshlrev_b32_e32 v46, 16, v191
	v_and_b32_e32 v47, 0xffff0000, v191
	v_pk_add_f32 v[52:53], v[52:53], v[40:41]
	v_pk_add_f32 v[54:55], v[54:55], v[42:43]
	v_pk_add_f32 v[56:57], v[56:57], v[44:45]
	v_pk_add_f32 v[58:59], v[58:59], v[46:47]
	s_cmp_gt_u32 s26, 15
	s_cbranch_scc0 .Lpool_h8_q3
	v_lshlrev_b32_e32 v40, 16, v192
	v_and_b32_e32 v41, 0xffff0000, v192
	v_lshlrev_b32_e32 v42, 16, v193
	v_and_b32_e32 v43, 0xffff0000, v193
	v_lshlrev_b32_e32 v44, 16, v194
	v_and_b32_e32 v45, 0xffff0000, v194
	v_lshlrev_b32_e32 v46, 16, v195
	v_and_b32_e32 v47, 0xffff0000, v195
	v_pk_add_f32 v[52:53], v[52:53], v[40:41]
	v_pk_add_f32 v[54:55], v[54:55], v[42:43]
	v_pk_add_f32 v[56:57], v[56:57], v[44:45]
	v_pk_add_f32 v[58:59], v[58:59], v[46:47]
.Lpool_h8_q3:
	v_pk_mul_f32 v[52:53], v[52:53], v[48:49] op_sel_hi:[1,0]
	v_pk_mul_f32 v[54:55], v[54:55], v[48:49] op_sel_hi:[1,0]
	v_pk_mul_f32 v[56:57], v[56:57], v[48:49] op_sel_hi:[1,0]
	v_pk_mul_f32 v[58:59], v[58:59], v[48:49] op_sel_hi:[1,0]
	ds_write_b128 v49, v[52:55] offset:49152
	ds_write_b128 v49, v[56:59] offset:49168
	v_add_u32_e32 v51, 0, v50
	v_add_u32_e32 v60, 8, v51
	v_min_u32_e32 v60, 64, v60
	v_sub_u32_e64 v61, v51, 8 clamp
	v_sub_u32_e32 v60, v60, v61
	v_cvt_f32_u32_e32 v212, v60
	v_div_scale_f32 v213, s[30:31], v212, v212, 1.0
	v_div_scale_f32 v215, vcc, 1.0, v212, 1.0
	v_rcp_f32_e32 v214, v213
	s_nop 1
	v_fma_f32 v216, -v213, v214, 1.0
	v_fmac_f32_e32 v214, v216, v214
	v_mul_f32_e32 v216, v215, v214
	v_fma_f32 v217, -v213, v216, v215
	v_fmac_f32_e32 v216, v217, v214
	v_fma_f32 v213, -v213, v216, v215
	s_nop 1
	v_div_fmas_f32 v213, v213, v214, v216
	v_div_fixup_f32 v196, v213, v212, 1.0
	v_add_u32_e32 v51, 16, v50
	v_add_u32_e32 v60, 8, v51
	v_min_u32_e32 v60, 64, v60
	v_sub_u32_e64 v61, v51, 8 clamp
	v_sub_u32_e32 v60, v60, v61
	v_cvt_f32_u32_e32 v212, v60
	v_div_scale_f32 v213, s[30:31], v212, v212, 1.0
	v_div_scale_f32 v215, vcc, 1.0, v212, 1.0
	v_rcp_f32_e32 v214, v213
	s_nop 1
	v_fma_f32 v216, -v213, v214, 1.0
	v_fmac_f32_e32 v214, v216, v214
	v_mul_f32_e32 v216, v215, v214
	v_fma_f32 v217, -v213, v216, v215
	v_fmac_f32_e32 v216, v217, v214
	v_fma_f32 v213, -v213, v216, v215
	s_nop 1
	v_div_fmas_f32 v213, v213, v214, v216
	v_div_fixup_f32 v198, v213, v212, 1.0
	v_add_u32_e32 v51, 32, v50
	v_add_u32_e32 v60, 8, v51
	v_min_u32_e32 v60, 64, v60
	v_sub_u32_e64 v61, v51, 8 clamp
	v_sub_u32_e32 v60, v60, v61
	v_cvt_f32_u32_e32 v212, v60
	v_div_scale_f32 v213, s[30:31], v212, v212, 1.0
	v_div_scale_f32 v215, vcc, 1.0, v212, 1.0
	v_rcp_f32_e32 v214, v213
	s_nop 1
	v_fma_f32 v216, -v213, v214, 1.0
	v_fmac_f32_e32 v214, v216, v214
	v_mul_f32_e32 v216, v215, v214
	v_fma_f32 v217, -v213, v216, v215
	v_fmac_f32_e32 v216, v217, v214
	v_fma_f32 v213, -v213, v216, v215
	s_nop 1
	v_div_fmas_f32 v213, v213, v214, v216
	v_div_fixup_f32 v200, v213, v212, 1.0
	v_add_u32_e32 v51, 48, v50
	v_add_u32_e32 v60, 8, v51
	v_min_u32_e32 v60, 64, v60
	v_sub_u32_e64 v61, v51, 8 clamp
	v_sub_u32_e32 v60, v60, v61
	v_cvt_f32_u32_e32 v212, v60
	v_div_scale_f32 v213, s[30:31], v212, v212, 1.0
	v_div_scale_f32 v215, vcc, 1.0, v212, 1.0
	v_rcp_f32_e32 v214, v213
	s_nop 1
	v_fma_f32 v216, -v213, v214, 1.0
	v_fmac_f32_e32 v214, v216, v214
	v_mul_f32_e32 v216, v215, v214
	v_fma_f32 v217, -v213, v216, v215
	v_fmac_f32_e32 v216, v217, v214
	v_fma_f32 v213, -v213, v216, v215
	s_nop 1
	v_div_fmas_f32 v213, v213, v214, v216
	v_div_fixup_f32 v202, v213, v212, 1.0
	s_waitcnt lgkmcnt(0)
	s_barrier
; #define LAS __attribute__((address_space(3)))
; __device__ __forceinline__ unsigned pk2(float lo, float hi) { return f2bf(lo) | (f2bf(hi) << 16); }
; template <int HALFW>
; __device__ __forceinline__ void pool_item(const bf16* P, bf16* DP, LAS float* tmp, int tid, int b, int r, int g) {
;     ...
;     for (int q = 0; q < 4; ++q) { const int p = tid + 512 * q, c = p >> 5, ch0 = (p & 31) * 8;
;         const int clo = c - HALFW < 0 ? 0 : c - HALFW, chi = c + HALFW > 64 ? 64 : c + HALFW; const float cinv = 1.f / (float)(chi - clo);
;         const size_t o = ((size_t)(b * 2048 + r * 64 + c)) * 1024 + g * 256 + ch0;
;         const v4u x = *(const v4u*)(P + o);
;         f32x4 a0 = (f32x4){0.f, 0.f, 0.f, 0.f}, a1 = a0;
; #pragma unroll
;         for (int u = 0; u < 2 * HALFW; ++u) { const int cc = (clo + u < chi) ? clo + u : clo; const float m = (clo + u < chi) ? 1.f : 0.f;
;             a0 += *(const LAS f32x4*)(tmp + cc * 256 + ch0) * m; a1 += *(const LAS f32x4*)(tmp + cc * 256 + ch0 + 4) * m; }
;         v4u d; d.x = pk2(a0[0] * cinv - bflo(x.x), a0[1] * cinv - bfhi(x.x)); d.y = pk2(a0[2] * cinv - bflo(x.y), a0[3] * cinv - bfhi(x.y));
;         d.z = pk2(a1[0] * cinv - bflo(x.z), a1[1] * cinv - bfhi(x.z)); d.w = pk2(a1[2] * cinv - bflo(x.w), a1[3] * cinv - bfhi(x.w));
;         *(v4u*)(DP + o) = d; }
	v_add_u32_e32 v51, -8, v50
	v_add_u32_e32 v60, 0, v51
	v_min_u32_e32 v60, 64, v60
	v_lshl_add_u32 v60, v60, 10, v3
	ds_read_b128 v[204:207], v60
	ds_read_b128 v[208:211], v60 offset:16
	v_add_u32_e32 v60, 1, v51
	v_min_u32_e32 v60, 64, v60
	v_lshl_add_u32 v60, v60, 10, v3
	ds_read_b128 v[76:79], v60
	ds_read_b128 v[80:83], v60 offset:16
	v_add_u32_e32 v60, 2, v51
	v_min_u32_e32 v60, 64, v60
	v_lshl_add_u32 v60, v60, 10, v3
	ds_read_b128 v[84:87], v60
	ds_read_b128 v[88:91], v60 offset:16
	v_add_u32_e32 v60, 3, v51
	v_min_u32_e32 v60, 64, v60
	v_lshl_add_u32 v60, v60, 10, v3
	ds_read_b128 v[92:95], v60
	ds_read_b128 v[96:99], v60 offset:16
	v_add_u32_e32 v60, 4, v51
	v_min_u32_e32 v60, 64, v60
	v_lshl_add_u32 v60, v60, 10, v3
	ds_read_b128 v[100:103], v60
	ds_read_b128 v[104:107], v60 offset:16
	v_add_u32_e32 v60, 5, v51
	v_min_u32_e32 v60, 64, v60
	v_lshl_add_u32 v60, v60, 10, v3
	ds_read_b128 v[108:111], v60
	ds_read_b128 v[112:115], v60 offset:16
	s_waitcnt lgkmcnt(8)
	v_pk_add_f32 v[204:205], v[204:205], v[76:77]
	v_pk_add_f32 v[206:207], v[206:207], v[78:79]
	v_pk_add_f32 v[208:209], v[208:209], v[80:81]
	v_pk_add_f32 v[210:211], v[210:211], v[82:83]
	v_add_u32_e32 v60, 6, v51
	v_min_u32_e32 v60, 64, v60
	v_lshl_add_u32 v60, v60, 10, v3
	ds_read_b128 v[68:71], v60
	ds_read_b128 v[72:75], v60 offset:16
	v_add_u32_e32 v60, 7, v51
	v_min_u32_e32 v60, 64, v60
	v_lshl_add_u32 v60, v60, 10, v3
	ds_read_b128 v[76:79], v60
	ds_read_b128 v[80:83], v60 offset:16
	s_waitcnt lgkmcnt(8)
	v_pk_add_f32 v[204:205], v[204:205], v[84:85]
	v_pk_add_f32 v[206:207], v[206:207], v[86:87]
	v_pk_add_f32 v[208:209], v[208:209], v[88:89]
	v_pk_add_f32 v[210:211], v[210:211], v[90:91]
	v_pk_add_f32 v[204:205], v[204:205], v[92:93]
	v_pk_add_f32 v[206:207], v[206:207], v[94:95]
	v_pk_add_f32 v[208:209], v[208:209], v[96:97]
	v_pk_add_f32 v[210:211], v[210:211], v[98:99]
	v_add_u32_e32 v60, 8, v51
	v_min_u32_e32 v60, 64, v60
	v_lshl_add_u32 v60, v60, 10, v3
	ds_read_b128 v[84:87], v60
	ds_read_b128 v[88:91], v60 offset:16
	v_add_u32_e32 v60, 9, v51
	v_min_u32_e32 v60, 64, v60
	v_lshl_add_u32 v60, v60, 10, v3
	ds_read_b128 v[92:95], v60
	ds_read_b128 v[96:99], v60 offset:16
	s_waitcnt lgkmcnt(8)
	v_pk_add_f32 v[204:205], v[204:205], v[100:101]
	v_pk_add_f32 v[206:207], v[206:207], v[102:103]
	v_pk_add_f32 v[208:209], v[208:209], v[104:105]
	v_pk_add_f32 v[210:211], v[210:211], v[106:107]
	v_pk_add_f32 v[204:205], v[204:205], v[108:109]
	v_pk_add_f32 v[206:207], v[206:207], v[110:111]
	v_pk_add_f32 v[208:209], v[208:209], v[112:113]
	v_pk_add_f32 v[210:211], v[210:211], v[114:115]
	v_add_u32_e32 v60, 10, v51
	v_min_u32_e32 v60, 64, v60
	v_lshl_add_u32 v60, v60, 10, v3
	ds_read_b128 v[100:103], v60
	ds_read_b128 v[104:107], v60 offset:16
	v_add_u32_e32 v60, 11, v51
	v_min_u32_e32 v60, 64, v60
	v_lshl_add_u32 v60, v60, 10, v3
	ds_read_b128 v[108:111], v60
	ds_read_b128 v[112:115], v60 offset:16
	s_waitcnt lgkmcnt(8)
	v_pk_add_f32 v[204:205], v[204:205], v[68:69]
	v_pk_add_f32 v[206:207], v[206:207], v[70:71]
	v_pk_add_f32 v[208:209], v[208:209], v[72:73]
	v_pk_add_f32 v[210:211], v[210:211], v[74:75]
	v_pk_add_f32 v[204:205], v[204:205], v[76:77]
	v_pk_add_f32 v[206:207], v[206:207], v[78:79]
	v_pk_add_f32 v[208:209], v[208:209], v[80:81]
	v_pk_add_f32 v[210:211], v[210:211], v[82:83]
	v_add_u32_e32 v60, 12, v51
	v_min_u32_e32 v60, 64, v60
	v_lshl_add_u32 v60, v60, 10, v3
	ds_read_b128 v[68:71], v60
	ds_read_b128 v[72:75], v60 offset:16
	v_add_u32_e32 v60, 13, v51
	v_min_u32_e32 v60, 64, v60
	v_lshl_add_u32 v60, v60, 10, v3
	ds_read_b128 v[76:79], v60
	ds_read_b128 v[80:83], v60 offset:16
	s_waitcnt lgkmcnt(8)
	v_pk_add_f32 v[204:205], v[204:205], v[84:85]
	v_pk_add_f32 v[206:207], v[206:207], v[86:87]
	v_pk_add_f32 v[208:209], v[208:209], v[88:89]
	v_pk_add_f32 v[210:211], v[210:211], v[90:91]
	v_pk_add_f32 v[204:205], v[204:205], v[92:93]
	v_pk_add_f32 v[206:207], v[206:207], v[94:95]
	v_pk_add_f32 v[208:209], v[208:209], v[96:97]
	v_pk_add_f32 v[210:211], v[210:211], v[98:99]
	v_add_u32_e32 v60, 14, v51
	v_min_u32_e32 v60, 64, v60
	v_lshl_add_u32 v60, v60, 10, v3
	ds_read_b128 v[84:87], v60
	ds_read_b128 v[88:91], v60 offset:16
	v_add_u32_e32 v60, 15, v51
	v_min_u32_e32 v60, 64, v60
	v_lshl_add_u32 v60, v60, 10, v3
	ds_read_b128 v[92:95], v60
	ds_read_b128 v[96:99], v60 offset:16
	s_waitcnt lgkmcnt(8)
	v_pk_add_f32 v[204:205], v[204:205], v[100:101]
	v_pk_add_f32 v[206:207], v[206:207], v[102:103]
	v_pk_add_f32 v[208:209], v[208:209], v[104:105]
	v_pk_add_f32 v[210:211], v[210:211], v[106:107]
	v_pk_add_f32 v[204:205], v[204:205], v[108:109]
	v_pk_add_f32 v[206:207], v[206:207], v[110:111]
	v_pk_add_f32 v[208:209], v[208:209], v[112:113]
	v_pk_add_f32 v[210:211], v[210:211], v[114:115]
	s_waitcnt lgkmcnt(4)
	v_pk_add_f32 v[204:205], v[204:205], v[68:69]
	v_pk_add_f32 v[206:207], v[206:207], v[70:71]
	v_pk_add_f32 v[208:209], v[208:209], v[72:73]
	v_pk_add_f32 v[210:211], v[210:211], v[74:75]
	v_pk_add_f32 v[204:205], v[204:205], v[76:77]
	v_pk_add_f32 v[206:207], v[206:207], v[78:79]
	v_pk_add_f32 v[208:209], v[208:209], v[80:81]
	v_pk_add_f32 v[210:211], v[210:211], v[82:83]
	s_waitcnt lgkmcnt(0)
	v_pk_add_f32 v[204:205], v[204:205], v[84:85]
	v_pk_add_f32 v[206:207], v[206:207], v[86:87]
	v_pk_add_f32 v[208:209], v[208:209], v[88:89]
	v_pk_add_f32 v[210:211], v[210:211], v[90:91]
	v_pk_add_f32 v[204:205], v[204:205], v[92:93]
	v_pk_add_f32 v[206:207], v[206:207], v[94:95]
	v_pk_add_f32 v[208:209], v[208:209], v[96:97]
	v_pk_add_f32 v[210:211], v[210:211], v[98:99]
	s_waitcnt vmcnt(0)
; #define LAS __attribute__((address_space(3)))
; __device__ __forceinline__ unsigned pk2(float lo, float hi) { return f2bf(lo) | (f2bf(hi) << 16); }
; template <int HALFW>
; __device__ __forceinline__ void pool_item(const bf16* P, bf16* DP, LAS float* tmp, int tid, int b, int r, int g) {
;     ...
;     for (int q = 0; q < 4; ++q) { const int p = tid + 512 * q, c = p >> 5, ch0 = (p & 31) * 8;
;         const int clo = c - HALFW < 0 ? 0 : c - HALFW, chi = c + HALFW > 64 ? 64 : c + HALFW; const float cinv = 1.f / (float)(chi - clo);
;         const size_t o = ((size_t)(b * 2048 + r * 64 + c)) * 1024 + g * 256 + ch0;
;         const v4u x = *(const v4u*)(P + o);
;         f32x4 a0 = (f32x4){0.f, 0.f, 0.f, 0.f}, a1 = a0;
; #pragma unroll
;         for (int u = 0; u < 2 * HALFW; ++u) { const int cc = (clo + u < chi) ? clo + u : clo; const float m = (clo + u < chi) ? 1.f : 0.f;
;             a0 += *(const LAS f32x4*)(tmp + cc * 256 + ch0) * m; a1 += *(const LAS f32x4*)(tmp + cc * 256 + ch0 + 4) * m; }
;         v4u d; d.x = pk2(a0[0] * cinv - bflo(x.x), a0[1] * cinv - bfhi(x.x)); d.y = pk2(a0[2] * cinv - bflo(x.y), a0[3] * cinv - bfhi(x.y));
;         d.z = pk2(a1[0] * cinv - bflo(x.z), a1[1] * cinv - bfhi(x.z)); d.w = pk2(a1[2] * cinv - bflo(x.w), a1[3] * cinv - bfhi(x.w));
;         *(v4u*)(DP + o) = d; }
	v_lshlrev_b32_e32 v40, 16, v16
	v_and_b32_e32 v41, 0xffff0000, v16
	v_lshlrev_b32_e32 v42, 16, v17
	v_and_b32_e32 v43, 0xffff0000, v17
	v_lshlrev_b32_e32 v44, 16, v18
	v_and_b32_e32 v45, 0xffff0000, v18
	v_lshlrev_b32_e32 v46, 16, v19
	v_and_b32_e32 v47, 0xffff0000, v19
	v_pk_fma_f32 v[40:41], v[196:197], v[204:205], v[40:41] op_sel_hi:[0,1,1] neg_lo:[0,0,1] neg_hi:[0,0,1]
	v_pk_fma_f32 v[42:43], v[196:197], v[206:207], v[42:43] op_sel_hi:[0,1,1] neg_lo:[0,0,1] neg_hi:[0,0,1]
	v_pk_fma_f32 v[44:45], v[196:197], v[208:209], v[44:45] op_sel_hi:[0,1,1] neg_lo:[0,0,1] neg_hi:[0,0,1]
	v_pk_fma_f32 v[46:47], v[196:197], v[210:211], v[46:47] op_sel_hi:[0,1,1] neg_lo:[0,0,1] neg_hi:[0,0,1]
	v_cvt_pk_bf16_f32 v218, v40, v41
	v_cvt_pk_bf16_f32 v219, v42, v43
	v_cvt_pk_bf16_f32 v220, v44, v45
	v_cvt_pk_bf16_f32 v221, v46, v47
	global_store_dwordx4 v12, v[218:221], s[24:25]
	v_add_u32_e32 v51, 8, v50
	v_add_u32_e32 v60, 0, v51
	v_min_u32_e32 v60, 64, v60
	v_lshl_add_u32 v60, v60, 10, v3
	ds_read_b128 v[204:207], v60
	ds_read_b128 v[208:211], v60 offset:16
	v_add_u32_e32 v60, 1, v51
	v_min_u32_e32 v60, 64, v60
	v_lshl_add_u32 v60, v60, 10, v3
	ds_read_b128 v[76:79], v60
	ds_read_b128 v[80:83], v60 offset:16
	v_add_u32_e32 v60, 2, v51
	v_min_u32_e32 v60, 64, v60
	v_lshl_add_u32 v60, v60, 10, v3
	ds_read_b128 v[84:87], v60
	ds_read_b128 v[88:91], v60 offset:16
	v_add_u32_e32 v60, 3, v51
	v_min_u32_e32 v60, 64, v60
	v_lshl_add_u32 v60, v60, 10, v3
	ds_read_b128 v[92:95], v60
	ds_read_b128 v[96:99], v60 offset:16
	v_add_u32_e32 v60, 4, v51
	v_min_u32_e32 v60, 64, v60
	v_lshl_add_u32 v60, v60, 10, v3
	ds_read_b128 v[100:103], v60
	ds_read_b128 v[104:107], v60 offset:16
	v_add_u32_e32 v60, 5, v51
	v_min_u32_e32 v60, 64, v60
	v_lshl_add_u32 v60, v60, 10, v3
	ds_read_b128 v[108:111], v60
	ds_read_b128 v[112:115], v60 offset:16
	s_waitcnt lgkmcnt(8)
	v_pk_add_f32 v[204:205], v[204:205], v[76:77]
	v_pk_add_f32 v[206:207], v[206:207], v[78:79]
	v_pk_add_f32 v[208:209], v[208:209], v[80:81]
	v_pk_add_f32 v[210:211], v[210:211], v[82:83]
	v_add_u32_e32 v60, 6, v51
	v_min_u32_e32 v60, 64, v60
	v_lshl_add_u32 v60, v60, 10, v3
	ds_read_b128 v[68:71], v60
	ds_read_b128 v[72:75], v60 offset:16
	v_add_u32_e32 v60, 7, v51
	v_min_u32_e32 v60, 64, v60
	v_lshl_add_u32 v60, v60, 10, v3
	ds_read_b128 v[76:79], v60
	ds_read_b128 v[80:83], v60 offset:16
	s_waitcnt lgkmcnt(8)
	v_pk_add_f32 v[204:205], v[204:205], v[84:85]
	v_pk_add_f32 v[206:207], v[206:207], v[86:87]
	v_pk_add_f32 v[208:209], v[208:209], v[88:89]
	v_pk_add_f32 v[210:211], v[210:211], v[90:91]
	v_pk_add_f32 v[204:205], v[204:205], v[92:93]
	v_pk_add_f32 v[206:207], v[206:207], v[94:95]
	v_pk_add_f32 v[208:209], v[208:209], v[96:97]
	v_pk_add_f32 v[210:211], v[210:211], v[98:99]
	v_add_u32_e32 v60, 8, v51
	v_min_u32_e32 v60, 64, v60
	v_lshl_add_u32 v60, v60, 10, v3
	ds_read_b128 v[84:87], v60
	ds_read_b128 v[88:91], v60 offset:16
	v_add_u32_e32 v60, 9, v51
	v_min_u32_e32 v60, 64, v60
	v_lshl_add_u32 v60, v60, 10, v3
	ds_read_b128 v[92:95], v60
	ds_read_b128 v[96:99], v60 offset:16
	s_waitcnt lgkmcnt(8)
	v_pk_add_f32 v[204:205], v[204:205], v[100:101]
	v_pk_add_f32 v[206:207], v[206:207], v[102:103]
	v_pk_add_f32 v[208:209], v[208:209], v[104:105]
	v_pk_add_f32 v[210:211], v[210:211], v[106:107]
	v_pk_add_f32 v[204:205], v[204:205], v[108:109]
	v_pk_add_f32 v[206:207], v[206:207], v[110:111]
	v_pk_add_f32 v[208:209], v[208:209], v[112:113]
	v_pk_add_f32 v[210:211], v[210:211], v[114:115]
	v_add_u32_e32 v60, 10, v51
	v_min_u32_e32 v60, 64, v60
	v_lshl_add_u32 v60, v60, 10, v3
	ds_read_b128 v[100:103], v60
	ds_read_b128 v[104:107], v60 offset:16
	v_add_u32_e32 v60, 11, v51
	v_min_u32_e32 v60, 64, v60
	v_lshl_add_u32 v60, v60, 10, v3
	ds_read_b128 v[108:111], v60
	ds_read_b128 v[112:115], v60 offset:16
	s_waitcnt lgkmcnt(8)
	v_pk_add_f32 v[204:205], v[204:205], v[68:69]
	v_pk_add_f32 v[206:207], v[206:207], v[70:71]
	v_pk_add_f32 v[208:209], v[208:209], v[72:73]
	v_pk_add_f32 v[210:211], v[210:211], v[74:75]
	v_pk_add_f32 v[204:205], v[204:205], v[76:77]
	v_pk_add_f32 v[206:207], v[206:207], v[78:79]
	v_pk_add_f32 v[208:209], v[208:209], v[80:81]
	v_pk_add_f32 v[210:211], v[210:211], v[82:83]
	v_add_u32_e32 v60, 12, v51
	v_min_u32_e32 v60, 64, v60
	v_lshl_add_u32 v60, v60, 10, v3
	ds_read_b128 v[68:71], v60
	ds_read_b128 v[72:75], v60 offset:16
	v_add_u32_e32 v60, 13, v51
	v_min_u32_e32 v60, 64, v60
	v_lshl_add_u32 v60, v60, 10, v3
	ds_read_b128 v[76:79], v60
	ds_read_b128 v[80:83], v60 offset:16
	s_waitcnt lgkmcnt(8)
	v_pk_add_f32 v[204:205], v[204:205], v[84:85]
	v_pk_add_f32 v[206:207], v[206:207], v[86:87]
	v_pk_add_f32 v[208:209], v[208:209], v[88:89]
	v_pk_add_f32 v[210:211], v[210:211], v[90:91]
	v_pk_add_f32 v[204:205], v[204:205], v[92:93]
	v_pk_add_f32 v[206:207], v[206:207], v[94:95]
	v_pk_add_f32 v[208:209], v[208:209], v[96:97]
	v_pk_add_f32 v[210:211], v[210:211], v[98:99]
	v_add_u32_e32 v60, 14, v51
	v_min_u32_e32 v60, 64, v60
	v_lshl_add_u32 v60, v60, 10, v3
	ds_read_b128 v[84:87], v60
	ds_read_b128 v[88:91], v60 offset:16
	v_add_u32_e32 v60, 15, v51
	v_min_u32_e32 v60, 64, v60
	v_lshl_add_u32 v60, v60, 10, v3
	ds_read_b128 v[92:95], v60
	ds_read_b128 v[96:99], v60 offset:16
	s_waitcnt lgkmcnt(8)
	v_pk_add_f32 v[204:205], v[204:205], v[100:101]
	v_pk_add_f32 v[206:207], v[206:207], v[102:103]
	v_pk_add_f32 v[208:209], v[208:209], v[104:105]
	v_pk_add_f32 v[210:211], v[210:211], v[106:107]
	v_pk_add_f32 v[204:205], v[204:205], v[108:109]
	v_pk_add_f32 v[206:207], v[206:207], v[110:111]
	v_pk_add_f32 v[208:209], v[208:209], v[112:113]
	v_pk_add_f32 v[210:211], v[210:211], v[114:115]
	s_waitcnt lgkmcnt(4)
; #define LAS __attribute__((address_space(3)))
; __device__ __forceinline__ unsigned pk2(float lo, float hi) { return f2bf(lo) | (f2bf(hi) << 16); }
; template <int HALFW>
; __device__ __forceinline__ void pool_item(const bf16* P, bf16* DP, LAS float* tmp, int tid, int b, int r, int g) {
;     ...
;     for (int q = 0; q < 4; ++q) { const int p = tid + 512 * q, c = p >> 5, ch0 = (p & 31) * 8;
;         const int clo = c - HALFW < 0 ? 0 : c - HALFW, chi = c + HALFW > 64 ? 64 : c + HALFW; const float cinv = 1.f / (float)(chi - clo);
;         const size_t o = ((size_t)(b * 2048 + r * 64 + c)) * 1024 + g * 256 + ch0;
;         const v4u x = *(const v4u*)(P + o);
;         f32x4 a0 = (f32x4){0.f, 0.f, 0.f, 0.f}, a1 = a0;
; #pragma unroll
;         for (int u = 0; u < 2 * HALFW; ++u) { const int cc = (clo + u < chi) ? clo + u : clo; const float m = (clo + u < chi) ? 1.f : 0.f;
;             a0 += *(const LAS f32x4*)(tmp + cc * 256 + ch0) * m; a1 += *(const LAS f32x4*)(tmp + cc * 256 + ch0 + 4) * m; }
;         v4u d; d.x = pk2(a0[0] * cinv - bflo(x.x), a0[1] * cinv - bfhi(x.x)); d.y = pk2(a0[2] * cinv - bflo(x.y), a0[3] * cinv - bfhi(x.y));
;         d.z = pk2(a1[0] * cinv - bflo(x.z), a1[1] * cinv - bfhi(x.z)); d.w = pk2(a1[2] * cinv - bflo(x.w), a1[3] * cinv - bfhi(x.w));
;         *(v4u*)(DP + o) = d; }
	v_pk_add_f32 v[204:205], v[204:205], v[68:69]
	v_pk_add_f32 v[206:207], v[206:207], v[70:71]
	v_pk_add_f32 v[208:209], v[208:209], v[72:73]
	v_pk_add_f32 v[210:211], v[210:211], v[74:75]
	v_pk_add_f32 v[204:205], v[204:205], v[76:77]
	v_pk_add_f32 v[206:207], v[206:207], v[78:79]
	v_pk_add_f32 v[208:209], v[208:209], v[80:81]
	v_pk_add_f32 v[210:211], v[210:211], v[82:83]
	s_waitcnt lgkmcnt(0)
	v_pk_add_f32 v[204:205], v[204:205], v[84:85]
	v_pk_add_f32 v[206:207], v[206:207], v[86:87]
	v_pk_add_f32 v[208:209], v[208:209], v[88:89]
	v_pk_add_f32 v[210:211], v[210:211], v[90:91]
	v_pk_add_f32 v[204:205], v[204:205], v[92:93]
	v_pk_add_f32 v[206:207], v[206:207], v[94:95]
	v_pk_add_f32 v[208:209], v[208:209], v[96:97]
	v_pk_add_f32 v[210:211], v[210:211], v[98:99]
	v_lshlrev_b32_e32 v40, 16, v20
	v_and_b32_e32 v41, 0xffff0000, v20
	v_lshlrev_b32_e32 v42, 16, v21
	v_and_b32_e32 v43, 0xffff0000, v21
	v_lshlrev_b32_e32 v44, 16, v22
	v_and_b32_e32 v45, 0xffff0000, v22
	v_lshlrev_b32_e32 v46, 16, v23
	v_and_b32_e32 v47, 0xffff0000, v23
	v_pk_fma_f32 v[40:41], v[198:199], v[204:205], v[40:41] op_sel_hi:[0,1,1] neg_lo:[0,0,1] neg_hi:[0,0,1]
	v_pk_fma_f32 v[42:43], v[198:199], v[206:207], v[42:43] op_sel_hi:[0,1,1] neg_lo:[0,0,1] neg_hi:[0,0,1]
	v_pk_fma_f32 v[44:45], v[198:199], v[208:209], v[44:45] op_sel_hi:[0,1,1] neg_lo:[0,0,1] neg_hi:[0,0,1]
	v_pk_fma_f32 v[46:47], v[198:199], v[210:211], v[46:47] op_sel_hi:[0,1,1] neg_lo:[0,0,1] neg_hi:[0,0,1]
	v_cvt_pk_bf16_f32 v222, v40, v41
	v_cvt_pk_bf16_f32 v223, v42, v43
	v_cvt_pk_bf16_f32 v224, v44, v45
	v_cvt_pk_bf16_f32 v225, v46, v47
	global_store_dwordx4 v13, v[222:225], s[24:25]
	v_add_u32_e32 v51, 24, v50
	v_add_u32_e32 v60, 0, v51
	v_min_u32_e32 v60, 64, v60
	v_lshl_add_u32 v60, v60, 10, v3
	ds_read_b128 v[204:207], v60
	ds_read_b128 v[208:211], v60 offset:16
	v_add_u32_e32 v60, 1, v51
	v_min_u32_e32 v60, 64, v60
	v_lshl_add_u32 v60, v60, 10, v3
	ds_read_b128 v[76:79], v60
	ds_read_b128 v[80:83], v60 offset:16
	v_add_u32_e32 v60, 2, v51
	v_min_u32_e32 v60, 64, v60
	v_lshl_add_u32 v60, v60, 10, v3
	ds_read_b128 v[84:87], v60
	ds_read_b128 v[88:91], v60 offset:16
	v_add_u32_e32 v60, 3, v51
	v_min_u32_e32 v60, 64, v60
	v_lshl_add_u32 v60, v60, 10, v3
	ds_read_b128 v[92:95], v60
	ds_read_b128 v[96:99], v60 offset:16
	v_add_u32_e32 v60, 4, v51
	v_min_u32_e32 v60, 64, v60
	v_lshl_add_u32 v60, v60, 10, v3
	ds_read_b128 v[100:103], v60
	ds_read_b128 v[104:107], v60 offset:16
	v_add_u32_e32 v60, 5, v51
	v_min_u32_e32 v60, 64, v60
	v_lshl_add_u32 v60, v60, 10, v3
	ds_read_b128 v[108:111], v60
	ds_read_b128 v[112:115], v60 offset:16
	s_waitcnt lgkmcnt(8)
	v_pk_add_f32 v[204:205], v[204:205], v[76:77]
	v_pk_add_f32 v[206:207], v[206:207], v[78:79]
	v_pk_add_f32 v[208:209], v[208:209], v[80:81]
	v_pk_add_f32 v[210:211], v[210:211], v[82:83]
	v_add_u32_e32 v60, 6, v51
	v_min_u32_e32 v60, 64, v60
	v_lshl_add_u32 v60, v60, 10, v3
	ds_read_b128 v[68:71], v60
	ds_read_b128 v[72:75], v60 offset:16
	v_add_u32_e32 v60, 7, v51
	v_min_u32_e32 v60, 64, v60
	v_lshl_add_u32 v60, v60, 10, v3
	ds_read_b128 v[76:79], v60
	ds_read_b128 v[80:83], v60 offset:16
	s_waitcnt lgkmcnt(8)
	v_pk_add_f32 v[204:205], v[204:205], v[84:85]
	v_pk_add_f32 v[206:207], v[206:207], v[86:87]
	v_pk_add_f32 v[208:209], v[208:209], v[88:89]
	v_pk_add_f32 v[210:211], v[210:211], v[90:91]
	v_pk_add_f32 v[204:205], v[204:205], v[92:93]
	v_pk_add_f32 v[206:207], v[206:207], v[94:95]
	v_pk_add_f32 v[208:209], v[208:209], v[96:97]
	v_pk_add_f32 v[210:211], v[210:211], v[98:99]
	v_add_u32_e32 v60, 8, v51
	v_min_u32_e32 v60, 64, v60
	v_lshl_add_u32 v60, v60, 10, v3
	ds_read_b128 v[84:87], v60
	ds_read_b128 v[88:91], v60 offset:16
	v_add_u32_e32 v60, 9, v51
	v_min_u32_e32 v60, 64, v60
	v_lshl_add_u32 v60, v60, 10, v3
	ds_read_b128 v[92:95], v60
	ds_read_b128 v[96:99], v60 offset:16
	s_waitcnt lgkmcnt(8)
	v_pk_add_f32 v[204:205], v[204:205], v[100:101]
	v_pk_add_f32 v[206:207], v[206:207], v[102:103]
	v_pk_add_f32 v[208:209], v[208:209], v[104:105]
	v_pk_add_f32 v[210:211], v[210:211], v[106:107]
	v_pk_add_f32 v[204:205], v[204:205], v[108:109]
	v_pk_add_f32 v[206:207], v[206:207], v[110:111]
	v_pk_add_f32 v[208:209], v[208:209], v[112:113]
	v_pk_add_f32 v[210:211], v[210:211], v[114:115]
	v_add_u32_e32 v60, 10, v51
	v_min_u32_e32 v60, 64, v60
	v_lshl_add_u32 v60, v60, 10, v3
	ds_read_b128 v[100:103], v60
	ds_read_b128 v[104:107], v60 offset:16
	v_add_u32_e32 v60, 11, v51
	v_min_u32_e32 v60, 64, v60
	v_lshl_add_u32 v60, v60, 10, v3
	ds_read_b128 v[108:111], v60
	ds_read_b128 v[112:115], v60 offset:16
	s_waitcnt lgkmcnt(8)
	v_pk_add_f32 v[204:205], v[204:205], v[68:69]
	v_pk_add_f32 v[206:207], v[206:207], v[70:71]
	v_pk_add_f32 v[208:209], v[208:209], v[72:73]
	v_pk_add_f32 v[210:211], v[210:211], v[74:75]
	v_pk_add_f32 v[204:205], v[204:205], v[76:77]
	v_pk_add_f32 v[206:207], v[206:207], v[78:79]
	v_pk_add_f32 v[208:209], v[208:209], v[80:81]
	v_pk_add_f32 v[210:211], v[210:211], v[82:83]
	v_add_u32_e32 v60, 12, v51
	v_min_u32_e32 v60, 64, v60
	v_lshl_add_u32 v60, v60, 10, v3
	ds_read_b128 v[68:71], v60
	ds_read_b128 v[72:75], v60 offset:16
	v_add_u32_e32 v60, 13, v51
	v_min_u32_e32 v60, 64, v60
	v_lshl_add_u32 v60, v60, 10, v3
	ds_read_b128 v[76:79], v60
	ds_read_b128 v[80:83], v60 offset:16
	s_waitcnt lgkmcnt(8)
; #define LAS __attribute__((address_space(3)))
; __device__ __forceinline__ unsigned pk2(float lo, float hi) { return f2bf(lo) | (f2bf(hi) << 16); }
; template <int HALFW>
; __device__ __forceinline__ void pool_item(const bf16* P, bf16* DP, LAS float* tmp, int tid, int b, int r, int g) {
;     ...
;     for (int q = 0; q < 4; ++q) { const int p = tid + 512 * q, c = p >> 5, ch0 = (p & 31) * 8;
;         const int clo = c - HALFW < 0 ? 0 : c - HALFW, chi = c + HALFW > 64 ? 64 : c + HALFW; const float cinv = 1.f / (float)(chi - clo);
;         const size_t o = ((size_t)(b * 2048 + r * 64 + c)) * 1024 + g * 256 + ch0;
;         const v4u x = *(const v4u*)(P + o);
;         f32x4 a0 = (f32x4){0.f, 0.f, 0.f, 0.f}, a1 = a0;
; #pragma unroll
;         for (int u = 0; u < 2 * HALFW; ++u) { const int cc = (clo + u < chi) ? clo + u : clo; const float m = (clo + u < chi) ? 1.f : 0.f;
;             a0 += *(const LAS f32x4*)(tmp + cc * 256 + ch0) * m; a1 += *(const LAS f32x4*)(tmp + cc * 256 + ch0 + 4) * m; }
;         v4u d; d.x = pk2(a0[0] * cinv - bflo(x.x), a0[1] * cinv - bfhi(x.x)); d.y = pk2(a0[2] * cinv - bflo(x.y), a0[3] * cinv - bfhi(x.y));
;         d.z = pk2(a1[0] * cinv - bflo(x.z), a1[1] * cinv - bfhi(x.z)); d.w = pk2(a1[2] * cinv - bflo(x.w), a1[3] * cinv - bfhi(x.w));
;         *(v4u*)(DP + o) = d; }
	v_pk_add_f32 v[204:205], v[204:205], v[84:85]
	v_pk_add_f32 v[206:207], v[206:207], v[86:87]
	v_pk_add_f32 v[208:209], v[208:209], v[88:89]
	v_pk_add_f32 v[210:211], v[210:211], v[90:91]
	v_pk_add_f32 v[204:205], v[204:205], v[92:93]
	v_pk_add_f32 v[206:207], v[206:207], v[94:95]
	v_pk_add_f32 v[208:209], v[208:209], v[96:97]
	v_pk_add_f32 v[210:211], v[210:211], v[98:99]
	v_add_u32_e32 v60, 14, v51
	v_min_u32_e32 v60, 64, v60
	v_lshl_add_u32 v60, v60, 10, v3
	ds_read_b128 v[84:87], v60
	ds_read_b128 v[88:91], v60 offset:16
	v_add_u32_e32 v60, 15, v51
	v_min_u32_e32 v60, 64, v60
	v_lshl_add_u32 v60, v60, 10, v3
	ds_read_b128 v[92:95], v60
	ds_read_b128 v[96:99], v60 offset:16
	s_waitcnt lgkmcnt(8)
	v_pk_add_f32 v[204:205], v[204:205], v[100:101]
	v_pk_add_f32 v[206:207], v[206:207], v[102:103]
	v_pk_add_f32 v[208:209], v[208:209], v[104:105]
	v_pk_add_f32 v[210:211], v[210:211], v[106:107]
	v_pk_add_f32 v[204:205], v[204:205], v[108:109]
	v_pk_add_f32 v[206:207], v[206:207], v[110:111]
	v_pk_add_f32 v[208:209], v[208:209], v[112:113]
	v_pk_add_f32 v[210:211], v[210:211], v[114:115]
	s_waitcnt lgkmcnt(4)
	v_pk_add_f32 v[204:205], v[204:205], v[68:69]
	v_pk_add_f32 v[206:207], v[206:207], v[70:71]
	v_pk_add_f32 v[208:209], v[208:209], v[72:73]
	v_pk_add_f32 v[210:211], v[210:211], v[74:75]
	v_pk_add_f32 v[204:205], v[204:205], v[76:77]
	v_pk_add_f32 v[206:207], v[206:207], v[78:79]
	v_pk_add_f32 v[208:209], v[208:209], v[80:81]
	v_pk_add_f32 v[210:211], v[210:211], v[82:83]
	s_waitcnt lgkmcnt(0)
	v_pk_add_f32 v[204:205], v[204:205], v[84:85]
	v_pk_add_f32 v[206:207], v[206:207], v[86:87]
	v_pk_add_f32 v[208:209], v[208:209], v[88:89]
	v_pk_add_f32 v[210:211], v[210:211], v[90:91]
	v_pk_add_f32 v[204:205], v[204:205], v[92:93]
	v_pk_add_f32 v[206:207], v[206:207], v[94:95]
	v_pk_add_f32 v[208:209], v[208:209], v[96:97]
	v_pk_add_f32 v[210:211], v[210:211], v[98:99]
	v_lshlrev_b32_e32 v40, 16, v24
	v_and_b32_e32 v41, 0xffff0000, v24
	v_lshlrev_b32_e32 v42, 16, v25
	v_and_b32_e32 v43, 0xffff0000, v25
	v_lshlrev_b32_e32 v44, 16, v26
	v_and_b32_e32 v45, 0xffff0000, v26
	v_lshlrev_b32_e32 v46, 16, v27
	v_and_b32_e32 v47, 0xffff0000, v27
	v_pk_fma_f32 v[40:41], v[200:201], v[204:205], v[40:41] op_sel_hi:[0,1,1] neg_lo:[0,0,1] neg_hi:[0,0,1]
	v_pk_fma_f32 v[42:43], v[200:201], v[206:207], v[42:43] op_sel_hi:[0,1,1] neg_lo:[0,0,1] neg_hi:[0,0,1]
	v_pk_fma_f32 v[44:45], v[200:201], v[208:209], v[44:45] op_sel_hi:[0,1,1] neg_lo:[0,0,1] neg_hi:[0,0,1]
	v_pk_fma_f32 v[46:47], v[200:201], v[210:211], v[46:47] op_sel_hi:[0,1,1] neg_lo:[0,0,1] neg_hi:[0,0,1]
	v_cvt_pk_bf16_f32 v218, v40, v41
	v_cvt_pk_bf16_f32 v219, v42, v43
	v_cvt_pk_bf16_f32 v220, v44, v45
	v_cvt_pk_bf16_f32 v221, v46, v47
	global_store_dwordx4 v14, v[218:221], s[24:25]
	v_add_u32_e32 v51, 40, v50
	v_add_u32_e32 v60, 0, v51
	v_min_u32_e32 v60, 64, v60
	v_lshl_add_u32 v60, v60, 10, v3
	ds_read_b128 v[204:207], v60
	ds_read_b128 v[208:211], v60 offset:16
	v_add_u32_e32 v60, 1, v51
	v_min_u32_e32 v60, 64, v60
	v_lshl_add_u32 v60, v60, 10, v3
	ds_read_b128 v[76:79], v60
	ds_read_b128 v[80:83], v60 offset:16
	v_add_u32_e32 v60, 2, v51
	v_min_u32_e32 v60, 64, v60
	v_lshl_add_u32 v60, v60, 10, v3
	ds_read_b128 v[84:87], v60
	ds_read_b128 v[88:91], v60 offset:16
	v_add_u32_e32 v60, 3, v51
	v_min_u32_e32 v60, 64, v60
	v_lshl_add_u32 v60, v60, 10, v3
	ds_read_b128 v[92:95], v60
	ds_read_b128 v[96:99], v60 offset:16
	v_add_u32_e32 v60, 4, v51
	v_min_u32_e32 v60, 64, v60
	v_lshl_add_u32 v60, v60, 10, v3
	ds_read_b128 v[100:103], v60
	ds_read_b128 v[104:107], v60 offset:16
	v_add_u32_e32 v60, 5, v51
	v_min_u32_e32 v60, 64, v60
	v_lshl_add_u32 v60, v60, 10, v3
	ds_read_b128 v[108:111], v60
	ds_read_b128 v[112:115], v60 offset:16
	s_waitcnt lgkmcnt(8)
	v_pk_add_f32 v[204:205], v[204:205], v[76:77]
	v_pk_add_f32 v[206:207], v[206:207], v[78:79]
	v_pk_add_f32 v[208:209], v[208:209], v[80:81]
	v_pk_add_f32 v[210:211], v[210:211], v[82:83]
	v_add_u32_e32 v60, 6, v51
	v_min_u32_e32 v60, 64, v60
	v_lshl_add_u32 v60, v60, 10, v3
	ds_read_b128 v[68:71], v60
	ds_read_b128 v[72:75], v60 offset:16
	v_add_u32_e32 v60, 7, v51
	v_min_u32_e32 v60, 64, v60
	v_lshl_add_u32 v60, v60, 10, v3
	ds_read_b128 v[76:79], v60
	ds_read_b128 v[80:83], v60 offset:16
	s_waitcnt lgkmcnt(8)
; #define LAS __attribute__((address_space(3)))
; __device__ __forceinline__ unsigned pk2(float lo, float hi) { return f2bf(lo) | (f2bf(hi) << 16); }
; template <int HALFW>
; __device__ __forceinline__ void pool_item(const bf16* P, bf16* DP, LAS float* tmp, int tid, int b, int r, int g) {
;     ...
;     for (int q = 0; q < 4; ++q) { const int p = tid + 512 * q, c = p >> 5, ch0 = (p & 31) * 8;
;         const int clo = c - HALFW < 0 ? 0 : c - HALFW, chi = c + HALFW > 64 ? 64 : c + HALFW; const float cinv = 1.f / (float)(chi - clo);
;         const size_t o = ((size_t)(b * 2048 + r * 64 + c)) * 1024 + g * 256 + ch0;
;         const v4u x = *(const v4u*)(P + o);
;         f32x4 a0 = (f32x4){0.f, 0.f, 0.f, 0.f}, a1 = a0;
; #pragma unroll
;         for (int u = 0; u < 2 * HALFW; ++u) { const int cc = (clo + u < chi) ? clo + u : clo; const float m = (clo + u < chi) ? 1.f : 0.f;
;             a0 += *(const LAS f32x4*)(tmp + cc * 256 + ch0) * m; a1 += *(const LAS f32x4*)(tmp + cc * 256 + ch0 + 4) * m; }
;         v4u d; d.x = pk2(a0[0] * cinv - bflo(x.x), a0[1] * cinv - bfhi(x.x)); d.y = pk2(a0[2] * cinv - bflo(x.y), a0[3] * cinv - bfhi(x.y));
;         d.z = pk2(a1[0] * cinv - bflo(x.z), a1[1] * cinv - bfhi(x.z)); d.w = pk2(a1[2] * cinv - bflo(x.w), a1[3] * cinv - bfhi(x.w));
;         *(v4u*)(DP + o) = d; }
	v_pk_add_f32 v[204:205], v[204:205], v[84:85]
	v_pk_add_f32 v[206:207], v[206:207], v[86:87]
	v_pk_add_f32 v[208:209], v[208:209], v[88:89]
	v_pk_add_f32 v[210:211], v[210:211], v[90:91]
	v_pk_add_f32 v[204:205], v[204:205], v[92:93]
	v_pk_add_f32 v[206:207], v[206:207], v[94:95]
	v_pk_add_f32 v[208:209], v[208:209], v[96:97]
	v_pk_add_f32 v[210:211], v[210:211], v[98:99]
	v_add_u32_e32 v60, 8, v51
	v_min_u32_e32 v60, 64, v60
	v_lshl_add_u32 v60, v60, 10, v3
	ds_read_b128 v[84:87], v60
	ds_read_b128 v[88:91], v60 offset:16
	v_add_u32_e32 v60, 9, v51
	v_min_u32_e32 v60, 64, v60
	v_lshl_add_u32 v60, v60, 10, v3
	ds_read_b128 v[92:95], v60
	ds_read_b128 v[96:99], v60 offset:16
	s_waitcnt lgkmcnt(8)
	v_pk_add_f32 v[204:205], v[204:205], v[100:101]
	v_pk_add_f32 v[206:207], v[206:207], v[102:103]
	v_pk_add_f32 v[208:209], v[208:209], v[104:105]
	v_pk_add_f32 v[210:211], v[210:211], v[106:107]
	v_pk_add_f32 v[204:205], v[204:205], v[108:109]
	v_pk_add_f32 v[206:207], v[206:207], v[110:111]
	v_pk_add_f32 v[208:209], v[208:209], v[112:113]
	v_pk_add_f32 v[210:211], v[210:211], v[114:115]
	v_add_u32_e32 v60, 10, v51
	v_min_u32_e32 v60, 64, v60
	v_lshl_add_u32 v60, v60, 10, v3
	ds_read_b128 v[100:103], v60
	ds_read_b128 v[104:107], v60 offset:16
	v_add_u32_e32 v60, 11, v51
	v_min_u32_e32 v60, 64, v60
	v_lshl_add_u32 v60, v60, 10, v3
	ds_read_b128 v[108:111], v60
	ds_read_b128 v[112:115], v60 offset:16
	s_waitcnt lgkmcnt(8)
	v_pk_add_f32 v[204:205], v[204:205], v[68:69]
	v_pk_add_f32 v[206:207], v[206:207], v[70:71]
	v_pk_add_f32 v[208:209], v[208:209], v[72:73]
	v_pk_add_f32 v[210:211], v[210:211], v[74:75]
	v_pk_add_f32 v[204:205], v[204:205], v[76:77]
	v_pk_add_f32 v[206:207], v[206:207], v[78:79]
	v_pk_add_f32 v[208:209], v[208:209], v[80:81]
	v_pk_add_f32 v[210:211], v[210:211], v[82:83]
	v_add_u32_e32 v60, 12, v51
	v_min_u32_e32 v60, 64, v60
	v_lshl_add_u32 v60, v60, 10, v3
	ds_read_b128 v[68:71], v60
	ds_read_b128 v[72:75], v60 offset:16
	v_add_u32_e32 v60, 13, v51
	v_min_u32_e32 v60, 64, v60
	v_lshl_add_u32 v60, v60, 10, v3
	ds_read_b128 v[76:79], v60
	ds_read_b128 v[80:83], v60 offset:16
	s_waitcnt lgkmcnt(8)
	v_pk_add_f32 v[204:205], v[204:205], v[84:85]
	v_pk_add_f32 v[206:207], v[206:207], v[86:87]
	v_pk_add_f32 v[208:209], v[208:209], v[88:89]
	v_pk_add_f32 v[210:211], v[210:211], v[90:91]
	v_pk_add_f32 v[204:205], v[204:205], v[92:93]
	v_pk_add_f32 v[206:207], v[206:207], v[94:95]
	v_pk_add_f32 v[208:209], v[208:209], v[96:97]
	v_pk_add_f32 v[210:211], v[210:211], v[98:99]
	v_add_u32_e32 v60, 14, v51
	v_min_u32_e32 v60, 64, v60
	v_lshl_add_u32 v60, v60, 10, v3
	ds_read_b128 v[84:87], v60
	ds_read_b128 v[88:91], v60 offset:16
	v_add_u32_e32 v60, 15, v51
	v_min_u32_e32 v60, 64, v60
	v_lshl_add_u32 v60, v60, 10, v3
	ds_read_b128 v[92:95], v60
	ds_read_b128 v[96:99], v60 offset:16
	s_waitcnt lgkmcnt(8)
	v_pk_add_f32 v[204:205], v[204:205], v[100:101]
	v_pk_add_f32 v[206:207], v[206:207], v[102:103]
	v_pk_add_f32 v[208:209], v[208:209], v[104:105]
	v_pk_add_f32 v[210:211], v[210:211], v[106:107]
	v_pk_add_f32 v[204:205], v[204:205], v[108:109]
	v_pk_add_f32 v[206:207], v[206:207], v[110:111]
	v_pk_add_f32 v[208:209], v[208:209], v[112:113]
	v_pk_add_f32 v[210:211], v[210:211], v[114:115]
	s_waitcnt lgkmcnt(4)
	v_pk_add_f32 v[204:205], v[204:205], v[68:69]
	v_pk_add_f32 v[206:207], v[206:207], v[70:71]
	v_pk_add_f32 v[208:209], v[208:209], v[72:73]
	v_pk_add_f32 v[210:211], v[210:211], v[74:75]
	v_pk_add_f32 v[204:205], v[204:205], v[76:77]
	v_pk_add_f32 v[206:207], v[206:207], v[78:79]
	v_pk_add_f32 v[208:209], v[208:209], v[80:81]
	v_pk_add_f32 v[210:211], v[210:211], v[82:83]
	s_waitcnt lgkmcnt(0)
	v_pk_add_f32 v[204:205], v[204:205], v[84:85]
	v_pk_add_f32 v[206:207], v[206:207], v[86:87]
	v_pk_add_f32 v[208:209], v[208:209], v[88:89]
	v_pk_add_f32 v[210:211], v[210:211], v[90:91]
	v_pk_add_f32 v[204:205], v[204:205], v[92:93]
	v_pk_add_f32 v[206:207], v[206:207], v[94:95]
	v_pk_add_f32 v[208:209], v[208:209], v[96:97]
	v_pk_add_f32 v[210:211], v[210:211], v[98:99]
	v_lshlrev_b32_e32 v40, 16, v28
	v_and_b32_e32 v41, 0xffff0000, v28
	v_lshlrev_b32_e32 v42, 16, v29
	v_and_b32_e32 v43, 0xffff0000, v29
	v_lshlrev_b32_e32 v44, 16, v30
	v_and_b32_e32 v45, 0xffff0000, v30
	v_lshlrev_b32_e32 v46, 16, v31
	v_and_b32_e32 v47, 0xffff0000, v31
	v_pk_fma_f32 v[40:41], v[202:203], v[204:205], v[40:41] op_sel_hi:[0,1,1] neg_lo:[0,0,1] neg_hi:[0,0,1]
	v_pk_fma_f32 v[42:43], v[202:203], v[206:207], v[42:43] op_sel_hi:[0,1,1] neg_lo:[0,0,1] neg_hi:[0,0,1]
	v_pk_fma_f32 v[44:45], v[202:203], v[208:209], v[44:45] op_sel_hi:[0,1,1] neg_lo:[0,0,1] neg_hi:[0,0,1]
	v_pk_fma_f32 v[46:47], v[202:203], v[210:211], v[46:47] op_sel_hi:[0,1,1] neg_lo:[0,0,1] neg_hi:[0,0,1]
	v_cvt_pk_bf16_f32 v222, v40, v41
	v_cvt_pk_bf16_f32 v223, v42, v43
	v_cvt_pk_bf16_f32 v224, v44, v45
	v_cvt_pk_bf16_f32 v225, v46, v47
	global_store_dwordx4 v15, v[222:225], s[24:25]
	s_barrier
	s_branch .LBB0_678
